# hand-written residual epilogue for P2/P12/P14 (loads pipelined two quarters ahead, stores after compute, batched row-sum reduction) on top of v48-assignment converters
# baseline (speedup 1.0000x reference)
;     __device__ __forceinline__ void operator()(AccRef acc, const Unit& u, int wr, int wc, int, int) const {
;         const int ln_ = fresh_lane(), fr = ln_ & 15, fq = ln_ >> 4;
;         const int row0 = u.pm * 256 + wr * 64 + fr, col0 = u.pn * 256 + wc * 32 + 8 * fq;
; #pragma unroll
;         for (int ai = 0; ai < 2; ++ai)
; #pragma unroll
;             for (int m = 0; m < 4; ++m) {
;                 const int row = row0 + ai * 128 + m * 16; float s = 0.f;
; #pragma unroll
;                 for (int bj = 0; bj < 2; ++bj) {
;                     const size_t p = (size_t)row * D + col0 + bj * 128;
;                     f32x4 x0, x1;
;                     if (xin32) { x0 = *(const f32x4*)(xin32 + p); x1 = *(const f32x4*)(xin32 + p + 4); }
;                     else { const v4u h = *(const v4u*)(xb + p), lo = *(const v4u*)(xl + p);
;                         x0 = (f32x4){bflo(h.x) + bflo(lo.x), bfhi(h.x) + bfhi(lo.x), bflo(h.y) + bflo(lo.y), bfhi(h.y) + bfhi(lo.y)};
;                         x1 = (f32x4){bflo(h.z) + bflo(lo.z), bfhi(h.z) + bfhi(lo.z), bflo(h.w) + bflo(lo.w), bfhi(h.w) + bfhi(lo.w)}; }
;                     x0 = x0 + alpha * acc[ai][bj][m][0]; x1 = x1 + alpha * acc[ai][bj][m][1];
;                     if (PROBE_ON) { x0 = x0 * pscale; x1 = x1 * pscale; if (p == 0) x0[0] += pspike; }
;                     if (xout32) { *(f32x4*)(xout32 + p) = x0; *(f32x4*)(xout32 + p + 4) = x1; }
;                     else {
;                         v4u w; w.x = cvt_pk_bf16(x0[0], x0[1]); w.y = cvt_pk_bf16(x0[2], x0[3]); w.z = cvt_pk_bf16(x1[0], x1[1]); w.w = cvt_pk_bf16(x1[2], x1[3]);
;                         *(v4u*)(xb + p) = w;
;                         const f32x4 r0 = {x0[0] - bflo(w.x), x0[1] - bfhi(w.x), x0[2] - bflo(w.y), x0[3] - bfhi(w.y)}, r1 = {x1[0] - bflo(w.z), x1[1] - bfhi(w.z), x1[2] - bflo(w.w), x1[3] - bfhi(w.w)};
;                         v4u q; q.x = cvt_pk_bf16(r0[0], r0[1]); q.y = cvt_pk_bf16(r0[2], r0[3]); q.z = cvt_pk_bf16(r1[0], r1[1]); q.w = cvt_pk_bf16(r1[2], r1[3]);
;                         *(v4u*)(xl + p) = q;
;                     }
;                     s += (x0[0] * x0[0] + x0[1] * x0[1]) + (x0[2] * x0[2] + x0[3] * x0[3]) + (x1[0] * x1[0] + x1[1] * x1[1]) + (x1[2] * x1[2] + x1[3] * x1[3]);
.LBB0_204:
	s_and_b64 vcc, exec, s[20:21]
	s_cbranch_vccnz .Lmy_re2_orig
	v_mbcnt_lo_u32_b32 v152, -1, 0
	v_mbcnt_hi_u32_b32 v152, -1, v152
	s_lshl_b32 s96, s3, 8
	s_add_i32 s96, s96, s44
	v_and_b32_e32 v153, 15, v152
	v_add_u32_e32 v153, s96, v153
	v_lshrrev_b32_e32 v154, 4, v152
	s_lshl_b32 s96, s2, 8
	s_or_b32 s96, s96, s45
	v_lshl_add_u32 v154, v154, 3, s96
	v_lshlrev_b32_e32 v248, 12, v153
	v_lshl_add_u32 v248, v154, 1, v248
	s_lshl_b32 s96, s2, 4
	s_lshl_b32 s28, s43, 2
	s_add_i32 s96, s96, s28
	v_lshl_add_u32 v249, v153, 7, s96
	v_lshlrev_b32_e32 v162, 2, v152
	v_xor_b32_e32 v163, 0x80, v162
	v_xor_b32_e32 v162, 64, v162
	s_mov_b64 s[28:29], s[12:13]
	s_mov_b64 s[98:99], s[14:15]
	global_load_dwordx4 v[164:167], v248, s[28:29]
	global_load_dwordx4 v[168:171], v248, s[98:99]
	global_load_dwordx4 v[172:175], v248, s[28:29] offset:256
	global_load_dwordx4 v[176:179], v248, s[98:99] offset:256
	s_add_u32 s28, s12, 0x10000
	s_addc_u32 s29, s13, 0
	s_add_u32 s98, s14, 0x10000
	s_addc_u32 s99, s15, 0
	global_load_dwordx4 v[180:183], v248, s[28:29]
	global_load_dwordx4 v[184:187], v248, s[98:99]
	global_load_dwordx4 v[188:191], v248, s[28:29] offset:256
	global_load_dwordx4 v[192:195], v248, s[98:99] offset:256
	s_add_u32 s28, s12, 0x20000
	s_addc_u32 s29, s13, 0
	s_add_u32 s98, s14, 0x20000
	s_addc_u32 s99, s15, 0
	global_load_dwordx4 v[196:199], v248, s[28:29]
	global_load_dwordx4 v[200:203], v248, s[98:99]
	global_load_dwordx4 v[204:207], v248, s[28:29] offset:256
	global_load_dwordx4 v[208:211], v248, s[98:99] offset:256
	s_add_u32 s28, s12, 0x30000
	s_addc_u32 s29, s13, 0
	s_add_u32 s98, s14, 0x30000
	s_addc_u32 s99, s15, 0
	global_load_dwordx4 v[224:227], v248, s[28:29]
	global_load_dwordx4 v[228:231], v248, s[98:99]
	global_load_dwordx4 v[232:235], v248, s[28:29] offset:256
	global_load_dwordx4 v[236:239], v248, s[98:99] offset:256
	s_waitcnt vmcnt(8)
	v_lshlrev_b32_e32 v152, 16, v164
	v_and_b32_e32 v153, 0xffff0000, v164
	v_lshlrev_b32_e32 v154, 16, v168
	v_and_b32_e32 v155, 0xffff0000, v168
	v_pk_add_f32 v[152:153], v[152:153], v[154:155]
	v_pk_fma_f32 v[126:127], v[126:127], 0.5, v[152:153] op_sel_hi:[1,0,1]
	v_lshlrev_b32_e32 v156, 16, v165
	v_and_b32_e32 v157, 0xffff0000, v165
	v_lshlrev_b32_e32 v158, 16, v169
	v_and_b32_e32 v159, 0xffff0000, v169
	v_pk_add_f32 v[156:157], v[156:157], v[158:159]
	v_pk_fma_f32 v[128:129], v[128:129], 0.5, v[156:157] op_sel_hi:[1,0,1]
	v_lshlrev_b32_e32 v152, 16, v166
	v_and_b32_e32 v153, 0xffff0000, v166
	v_lshlrev_b32_e32 v154, 16, v170
	v_and_b32_e32 v155, 0xffff0000, v170
	v_pk_add_f32 v[152:153], v[152:153], v[154:155]
	v_pk_fma_f32 v[122:123], v[122:123], 0.5, v[152:153] op_sel_hi:[1,0,1]
	v_lshlrev_b32_e32 v156, 16, v167
	v_and_b32_e32 v157, 0xffff0000, v167
	v_lshlrev_b32_e32 v158, 16, v171
	v_and_b32_e32 v159, 0xffff0000, v171
	v_pk_add_f32 v[156:157], v[156:157], v[158:159]
	v_pk_fma_f32 v[124:125], v[124:125], 0.5, v[156:157] op_sel_hi:[1,0,1]
	v_cvt_pk_bf16_f32 v164, v126, v127
	v_cvt_pk_bf16_f32 v165, v128, v129
	v_cvt_pk_bf16_f32 v166, v122, v123
	v_cvt_pk_bf16_f32 v167, v124, v125
	v_lshlrev_b32_e32 v152, 16, v164
	v_and_b32_e32 v153, 0xffff0000, v164
	v_pk_add_f32 v[152:153], v[126:127], v[152:153] neg_lo:[0,1] neg_hi:[0,1]
	v_lshlrev_b32_e32 v154, 16, v165
	v_and_b32_e32 v155, 0xffff0000, v165
	v_pk_add_f32 v[154:155], v[128:129], v[154:155] neg_lo:[0,1] neg_hi:[0,1]
	v_lshlrev_b32_e32 v156, 16, v166
	v_and_b32_e32 v157, 0xffff0000, v166
	v_pk_add_f32 v[156:157], v[122:123], v[156:157] neg_lo:[0,1] neg_hi:[0,1]
	v_lshlrev_b32_e32 v158, 16, v167
	v_and_b32_e32 v159, 0xffff0000, v167
	v_pk_add_f32 v[158:159], v[124:125], v[158:159] neg_lo:[0,1] neg_hi:[0,1]
	v_cvt_pk_bf16_f32 v168, v152, v153
	v_cvt_pk_bf16_f32 v169, v154, v155
	v_cvt_pk_bf16_f32 v170, v156, v157
	v_cvt_pk_bf16_f32 v171, v158, v159
	v_pk_mul_f32 v[152:153], v[126:127], v[126:127]
	v_pk_mul_f32 v[154:155], v[128:129], v[128:129]
	v_pk_mul_f32 v[156:157], v[122:123], v[122:123]
	v_pk_mul_f32 v[158:159], v[124:125], v[124:125]
	v_pk_add_f32 v[152:153], v[152:153], v[154:155]
	v_pk_add_f32 v[156:157], v[156:157], v[158:159]
	v_pk_add_f32 v[152:153], v[152:153], v[156:157]
	v_add_f32_e32 v240, v152, v153
	v_lshlrev_b32_e32 v152, 16, v172
	v_and_b32_e32 v153, 0xffff0000, v172
	v_lshlrev_b32_e32 v154, 16, v176
	v_and_b32_e32 v155, 0xffff0000, v176
	v_pk_add_f32 v[152:153], v[152:153], v[154:155]
	v_pk_fma_f32 v[118:119], v[118:119], 0.5, v[152:153] op_sel_hi:[1,0,1]
	v_lshlrev_b32_e32 v156, 16, v173
	v_and_b32_e32 v157, 0xffff0000, v173
	v_lshlrev_b32_e32 v158, 16, v177
	v_and_b32_e32 v159, 0xffff0000, v177
	v_pk_add_f32 v[156:157], v[156:157], v[158:159]
	v_pk_fma_f32 v[120:121], v[120:121], 0.5, v[156:157] op_sel_hi:[1,0,1]
	v_lshlrev_b32_e32 v152, 16, v174
	v_and_b32_e32 v153, 0xffff0000, v174
	v_lshlrev_b32_e32 v154, 16, v178
	v_and_b32_e32 v155, 0xffff0000, v178
	v_pk_add_f32 v[152:153], v[152:153], v[154:155]
	v_pk_fma_f32 v[114:115], v[114:115], 0.5, v[152:153] op_sel_hi:[1,0,1]
	v_lshlrev_b32_e32 v156, 16, v175
	v_and_b32_e32 v157, 0xffff0000, v175
	v_lshlrev_b32_e32 v158, 16, v179
	v_and_b32_e32 v159, 0xffff0000, v179
	v_pk_add_f32 v[156:157], v[156:157], v[158:159]
	v_pk_fma_f32 v[116:117], v[116:117], 0.5, v[156:157] op_sel_hi:[1,0,1]
	v_cvt_pk_bf16_f32 v172, v118, v119
	v_cvt_pk_bf16_f32 v173, v120, v121
	v_cvt_pk_bf16_f32 v174, v114, v115
	v_cvt_pk_bf16_f32 v175, v116, v117
	v_lshlrev_b32_e32 v152, 16, v172
	v_and_b32_e32 v153, 0xffff0000, v172
	v_pk_add_f32 v[152:153], v[118:119], v[152:153] neg_lo:[0,1] neg_hi:[0,1]
	v_lshlrev_b32_e32 v154, 16, v173
	v_and_b32_e32 v155, 0xffff0000, v173
; __device__ __forceinline__ unsigned cvt_pk_bf16(float lo, float hi) { unsigned r; asm volatile("v_cvt_pk_bf16_f32 %0, %1, %2" : "=v"(r) : "v"(lo), "v"(hi)); return r; }
;     __device__ __forceinline__ void operator()(AccRef acc, const Unit& u, int wr, int wc, int, int) const {
;     ...
;             for (int m = 0; m < 4; ++m) {
;                 const int row = row0 + ai * 128 + m * 16; float s = 0.f;
; #pragma unroll
;                 for (int bj = 0; bj < 2; ++bj) {
;                     const size_t p = (size_t)row * D + col0 + bj * 128;
;                     f32x4 x0, x1;
;                     if (xin32) { x0 = *(const f32x4*)(xin32 + p); x1 = *(const f32x4*)(xin32 + p + 4); }
;                     else { const v4u h = *(const v4u*)(xb + p), lo = *(const v4u*)(xl + p);
;                         x0 = (f32x4){bflo(h.x) + bflo(lo.x), bfhi(h.x) + bfhi(lo.x), bflo(h.y) + bflo(lo.y), bfhi(h.y) + bfhi(lo.y)};
;                         x1 = (f32x4){bflo(h.z) + bflo(lo.z), bfhi(h.z) + bfhi(lo.z), bflo(h.w) + bflo(lo.w), bfhi(h.w) + bfhi(lo.w)}; }
;                     x0 = x0 + alpha * acc[ai][bj][m][0]; x1 = x1 + alpha * acc[ai][bj][m][1];
;                     if (PROBE_ON) { x0 = x0 * pscale; x1 = x1 * pscale; if (p == 0) x0[0] += pspike; }
;                     if (xout32) { *(f32x4*)(xout32 + p) = x0; *(f32x4*)(xout32 + p + 4) = x1; }
;                     else {
;                         v4u w; w.x = cvt_pk_bf16(x0[0], x0[1]); w.y = cvt_pk_bf16(x0[2], x0[3]); w.z = cvt_pk_bf16(x1[0], x1[1]); w.w = cvt_pk_bf16(x1[2], x1[3]);
;                         *(v4u*)(xb + p) = w;
;                         const f32x4 r0 = {x0[0] - bflo(w.x), x0[1] - bfhi(w.x), x0[2] - bflo(w.y), x0[3] - bfhi(w.y)}, r1 = {x1[0] - bflo(w.z), x1[1] - bfhi(w.z), x1[2] - bflo(w.w), x1[3] - bfhi(w.w)};
;                         v4u q; q.x = cvt_pk_bf16(r0[0], r0[1]); q.y = cvt_pk_bf16(r0[2], r0[3]); q.z = cvt_pk_bf16(r1[0], r1[1]); q.w = cvt_pk_bf16(r1[2], r1[3]);
;                         *(v4u*)(xl + p) = q;
;                     }
;                     s += (x0[0] * x0[0] + x0[1] * x0[1]) + (x0[2] * x0[2] + x0[3] * x0[3]) + (x1[0] * x1[0] + x1[1] * x1[1]) + (x1[2] * x1[2] + x1[3] * x1[3]);
	v_pk_add_f32 v[154:155], v[120:121], v[154:155] neg_lo:[0,1] neg_hi:[0,1]
	v_lshlrev_b32_e32 v156, 16, v174
	v_and_b32_e32 v157, 0xffff0000, v174
	v_pk_add_f32 v[156:157], v[114:115], v[156:157] neg_lo:[0,1] neg_hi:[0,1]
	v_lshlrev_b32_e32 v158, 16, v175
	v_and_b32_e32 v159, 0xffff0000, v175
	v_pk_add_f32 v[158:159], v[116:117], v[158:159] neg_lo:[0,1] neg_hi:[0,1]
	v_cvt_pk_bf16_f32 v176, v152, v153
	v_cvt_pk_bf16_f32 v177, v154, v155
	v_cvt_pk_bf16_f32 v178, v156, v157
	v_cvt_pk_bf16_f32 v179, v158, v159
	v_pk_mul_f32 v[152:153], v[118:119], v[118:119]
	v_pk_mul_f32 v[154:155], v[120:121], v[120:121]
	v_pk_mul_f32 v[156:157], v[114:115], v[114:115]
	v_pk_mul_f32 v[158:159], v[116:117], v[116:117]
	v_pk_add_f32 v[152:153], v[152:153], v[154:155]
	v_pk_add_f32 v[156:157], v[156:157], v[158:159]
	v_pk_add_f32 v[152:153], v[152:153], v[156:157]
	v_add_f32_e32 v152, v152, v153
	v_add_f32_e32 v240, v240, v152
	v_lshlrev_b32_e32 v152, 16, v180
	v_and_b32_e32 v153, 0xffff0000, v180
	v_lshlrev_b32_e32 v154, 16, v184
	v_and_b32_e32 v155, 0xffff0000, v184
	v_pk_add_f32 v[152:153], v[152:153], v[154:155]
	v_pk_fma_f32 v[110:111], v[110:111], 0.5, v[152:153] op_sel_hi:[1,0,1]
	v_lshlrev_b32_e32 v156, 16, v181
	v_and_b32_e32 v157, 0xffff0000, v181
	v_lshlrev_b32_e32 v158, 16, v185
	v_and_b32_e32 v159, 0xffff0000, v185
	v_pk_add_f32 v[156:157], v[156:157], v[158:159]
	v_pk_fma_f32 v[112:113], v[112:113], 0.5, v[156:157] op_sel_hi:[1,0,1]
	v_lshlrev_b32_e32 v152, 16, v182
	v_and_b32_e32 v153, 0xffff0000, v182
	v_lshlrev_b32_e32 v154, 16, v186
	v_and_b32_e32 v155, 0xffff0000, v186
	v_pk_add_f32 v[152:153], v[152:153], v[154:155]
	v_pk_fma_f32 v[106:107], v[106:107], 0.5, v[152:153] op_sel_hi:[1,0,1]
	v_lshlrev_b32_e32 v156, 16, v183
	v_and_b32_e32 v157, 0xffff0000, v183
	v_lshlrev_b32_e32 v158, 16, v187
	v_and_b32_e32 v159, 0xffff0000, v187
	v_pk_add_f32 v[156:157], v[156:157], v[158:159]
	v_pk_fma_f32 v[108:109], v[108:109], 0.5, v[156:157] op_sel_hi:[1,0,1]
	v_cvt_pk_bf16_f32 v180, v110, v111
	v_cvt_pk_bf16_f32 v181, v112, v113
	v_cvt_pk_bf16_f32 v182, v106, v107
	v_cvt_pk_bf16_f32 v183, v108, v109
	v_lshlrev_b32_e32 v152, 16, v180
	v_and_b32_e32 v153, 0xffff0000, v180
	v_pk_add_f32 v[152:153], v[110:111], v[152:153] neg_lo:[0,1] neg_hi:[0,1]
	v_lshlrev_b32_e32 v154, 16, v181
	v_and_b32_e32 v155, 0xffff0000, v181
	v_pk_add_f32 v[154:155], v[112:113], v[154:155] neg_lo:[0,1] neg_hi:[0,1]
	v_lshlrev_b32_e32 v156, 16, v182
	v_and_b32_e32 v157, 0xffff0000, v182
	v_pk_add_f32 v[156:157], v[106:107], v[156:157] neg_lo:[0,1] neg_hi:[0,1]
	v_lshlrev_b32_e32 v158, 16, v183
	v_and_b32_e32 v159, 0xffff0000, v183
	v_pk_add_f32 v[158:159], v[108:109], v[158:159] neg_lo:[0,1] neg_hi:[0,1]
	v_cvt_pk_bf16_f32 v184, v152, v153
	v_cvt_pk_bf16_f32 v185, v154, v155
	v_cvt_pk_bf16_f32 v186, v156, v157
	v_cvt_pk_bf16_f32 v187, v158, v159
	v_pk_mul_f32 v[152:153], v[110:111], v[110:111]
	v_pk_mul_f32 v[154:155], v[112:113], v[112:113]
	v_pk_mul_f32 v[156:157], v[106:107], v[106:107]
	v_pk_mul_f32 v[158:159], v[108:109], v[108:109]
	v_pk_add_f32 v[152:153], v[152:153], v[154:155]
	v_pk_add_f32 v[156:157], v[156:157], v[158:159]
	v_pk_add_f32 v[152:153], v[152:153], v[156:157]
	v_add_f32_e32 v241, v152, v153
	v_lshlrev_b32_e32 v152, 16, v188
	v_and_b32_e32 v153, 0xffff0000, v188
	v_lshlrev_b32_e32 v154, 16, v192
	v_and_b32_e32 v155, 0xffff0000, v192
	v_pk_add_f32 v[152:153], v[152:153], v[154:155]
	v_pk_fma_f32 v[102:103], v[102:103], 0.5, v[152:153] op_sel_hi:[1,0,1]
	v_lshlrev_b32_e32 v156, 16, v189
	v_and_b32_e32 v157, 0xffff0000, v189
	v_lshlrev_b32_e32 v158, 16, v193
	v_and_b32_e32 v159, 0xffff0000, v193
	v_pk_add_f32 v[156:157], v[156:157], v[158:159]
	v_pk_fma_f32 v[104:105], v[104:105], 0.5, v[156:157] op_sel_hi:[1,0,1]
	v_lshlrev_b32_e32 v152, 16, v190
	v_and_b32_e32 v153, 0xffff0000, v190
	v_lshlrev_b32_e32 v154, 16, v194
	v_and_b32_e32 v155, 0xffff0000, v194
	v_pk_add_f32 v[152:153], v[152:153], v[154:155]
	v_pk_fma_f32 v[98:99], v[98:99], 0.5, v[152:153] op_sel_hi:[1,0,1]
	v_lshlrev_b32_e32 v156, 16, v191
	v_and_b32_e32 v157, 0xffff0000, v191
	v_lshlrev_b32_e32 v158, 16, v195
	v_and_b32_e32 v159, 0xffff0000, v195
	v_pk_add_f32 v[156:157], v[156:157], v[158:159]
	v_pk_fma_f32 v[100:101], v[100:101], 0.5, v[156:157] op_sel_hi:[1,0,1]
	v_cvt_pk_bf16_f32 v188, v102, v103
	v_cvt_pk_bf16_f32 v189, v104, v105
	v_cvt_pk_bf16_f32 v190, v98, v99
	v_cvt_pk_bf16_f32 v191, v100, v101
	v_lshlrev_b32_e32 v152, 16, v188
	v_and_b32_e32 v153, 0xffff0000, v188
	v_pk_add_f32 v[152:153], v[102:103], v[152:153] neg_lo:[0,1] neg_hi:[0,1]
	v_lshlrev_b32_e32 v154, 16, v189
	v_and_b32_e32 v155, 0xffff0000, v189
	v_pk_add_f32 v[154:155], v[104:105], v[154:155] neg_lo:[0,1] neg_hi:[0,1]
	v_lshlrev_b32_e32 v156, 16, v190
	v_and_b32_e32 v157, 0xffff0000, v190
	v_pk_add_f32 v[156:157], v[98:99], v[156:157] neg_lo:[0,1] neg_hi:[0,1]
	v_lshlrev_b32_e32 v158, 16, v191
	v_and_b32_e32 v159, 0xffff0000, v191
	v_pk_add_f32 v[158:159], v[100:101], v[158:159] neg_lo:[0,1] neg_hi:[0,1]
	v_cvt_pk_bf16_f32 v192, v152, v153
	v_cvt_pk_bf16_f32 v193, v154, v155
	v_cvt_pk_bf16_f32 v194, v156, v157
	v_cvt_pk_bf16_f32 v195, v158, v159
	v_pk_mul_f32 v[152:153], v[102:103], v[102:103]
	v_pk_mul_f32 v[154:155], v[104:105], v[104:105]
	v_pk_mul_f32 v[156:157], v[98:99], v[98:99]
	v_pk_mul_f32 v[158:159], v[100:101], v[100:101]
	v_pk_add_f32 v[152:153], v[152:153], v[154:155]
	v_pk_add_f32 v[156:157], v[156:157], v[158:159]
	v_pk_add_f32 v[152:153], v[152:153], v[156:157]
	v_add_f32_e32 v152, v152, v153
	v_add_f32_e32 v241, v241, v152
	s_mov_b64 s[28:29], s[12:13]
	s_mov_b64 s[98:99], s[14:15]
	global_store_dwordx4 v248, v[164:167], s[28:29]
	global_store_dwordx4 v248, v[168:171], s[98:99]
	global_store_dwordx4 v248, v[172:175], s[28:29] offset:256
	global_store_dwordx4 v248, v[176:179], s[98:99] offset:256
	s_add_u32 s28, s12, 0x10000
	s_addc_u32 s29, s13, 0
	s_add_u32 s98, s14, 0x10000
	s_addc_u32 s99, s15, 0
	global_store_dwordx4 v248, v[180:183], s[28:29]
	global_store_dwordx4 v248, v[184:187], s[98:99]
	global_store_dwordx4 v248, v[188:191], s[28:29] offset:256
	global_store_dwordx4 v248, v[192:195], s[98:99] offset:256
	s_add_u32 s28, s12, 0x80000
	s_addc_u32 s29, s13, 0
	s_add_u32 s98, s14, 0x80000
	s_addc_u32 s99, s15, 0
	global_load_dwordx4 v[164:167], v248, s[28:29]
	global_load_dwordx4 v[168:171], v248, s[98:99]
	global_load_dwordx4 v[172:175], v248, s[28:29] offset:256
	global_load_dwordx4 v[176:179], v248, s[98:99] offset:256
	s_add_u32 s28, s12, 0x90000
	s_addc_u32 s29, s13, 0
	s_add_u32 s98, s14, 0x90000
	s_addc_u32 s99, s15, 0
	global_load_dwordx4 v[180:183], v248, s[28:29]
	global_load_dwordx4 v[184:187], v248, s[98:99]
	global_load_dwordx4 v[188:191], v248, s[28:29] offset:256
	global_load_dwordx4 v[192:195], v248, s[98:99] offset:256
	s_waitcnt vmcnt(16)
; __device__ __forceinline__ unsigned cvt_pk_bf16(float lo, float hi) { unsigned r; asm volatile("v_cvt_pk_bf16_f32 %0, %1, %2" : "=v"(r) : "v"(lo), "v"(hi)); return r; }
;     __device__ __forceinline__ void operator()(AccRef acc, const Unit& u, int wr, int wc, int, int) const {
;     ...
;             for (int m = 0; m < 4; ++m) {
;                 const int row = row0 + ai * 128 + m * 16; float s = 0.f;
; #pragma unroll
;                 for (int bj = 0; bj < 2; ++bj) {
;                     const size_t p = (size_t)row * D + col0 + bj * 128;
;                     f32x4 x0, x1;
;                     if (xin32) { x0 = *(const f32x4*)(xin32 + p); x1 = *(const f32x4*)(xin32 + p + 4); }
;                     else { const v4u h = *(const v4u*)(xb + p), lo = *(const v4u*)(xl + p);
;                         x0 = (f32x4){bflo(h.x) + bflo(lo.x), bfhi(h.x) + bfhi(lo.x), bflo(h.y) + bflo(lo.y), bfhi(h.y) + bfhi(lo.y)};
;                         x1 = (f32x4){bflo(h.z) + bflo(lo.z), bfhi(h.z) + bfhi(lo.z), bflo(h.w) + bflo(lo.w), bfhi(h.w) + bfhi(lo.w)}; }
;                     x0 = x0 + alpha * acc[ai][bj][m][0]; x1 = x1 + alpha * acc[ai][bj][m][1];
;                     if (PROBE_ON) { x0 = x0 * pscale; x1 = x1 * pscale; if (p == 0) x0[0] += pspike; }
;                     if (xout32) { *(f32x4*)(xout32 + p) = x0; *(f32x4*)(xout32 + p + 4) = x1; }
;                     else {
;                         v4u w; w.x = cvt_pk_bf16(x0[0], x0[1]); w.y = cvt_pk_bf16(x0[2], x0[3]); w.z = cvt_pk_bf16(x1[0], x1[1]); w.w = cvt_pk_bf16(x1[2], x1[3]);
;                         *(v4u*)(xb + p) = w;
;                         const f32x4 r0 = {x0[0] - bflo(w.x), x0[1] - bfhi(w.x), x0[2] - bflo(w.y), x0[3] - bfhi(w.y)}, r1 = {x1[0] - bflo(w.z), x1[1] - bfhi(w.z), x1[2] - bflo(w.w), x1[3] - bfhi(w.w)};
;                         v4u q; q.x = cvt_pk_bf16(r0[0], r0[1]); q.y = cvt_pk_bf16(r0[2], r0[3]); q.z = cvt_pk_bf16(r1[0], r1[1]); q.w = cvt_pk_bf16(r1[2], r1[3]);
;                         *(v4u*)(xl + p) = q;
;                     }
;                     s += (x0[0] * x0[0] + x0[1] * x0[1]) + (x0[2] * x0[2] + x0[3] * x0[3]) + (x1[0] * x1[0] + x1[1] * x1[1]) + (x1[2] * x1[2] + x1[3] * x1[3]);
	v_lshlrev_b32_e32 v152, 16, v196
	v_and_b32_e32 v153, 0xffff0000, v196
	v_lshlrev_b32_e32 v154, 16, v200
	v_and_b32_e32 v155, 0xffff0000, v200
	v_pk_add_f32 v[152:153], v[152:153], v[154:155]
	v_pk_fma_f32 v[94:95], v[94:95], 0.5, v[152:153] op_sel_hi:[1,0,1]
	v_lshlrev_b32_e32 v156, 16, v197
	v_and_b32_e32 v157, 0xffff0000, v197
	v_lshlrev_b32_e32 v158, 16, v201
	v_and_b32_e32 v159, 0xffff0000, v201
	v_pk_add_f32 v[156:157], v[156:157], v[158:159]
	v_pk_fma_f32 v[96:97], v[96:97], 0.5, v[156:157] op_sel_hi:[1,0,1]
	v_lshlrev_b32_e32 v152, 16, v198
	v_and_b32_e32 v153, 0xffff0000, v198
	v_lshlrev_b32_e32 v154, 16, v202
	v_and_b32_e32 v155, 0xffff0000, v202
	v_pk_add_f32 v[152:153], v[152:153], v[154:155]
	v_pk_fma_f32 v[90:91], v[90:91], 0.5, v[152:153] op_sel_hi:[1,0,1]
	v_lshlrev_b32_e32 v156, 16, v199
	v_and_b32_e32 v157, 0xffff0000, v199
	v_lshlrev_b32_e32 v158, 16, v203
	v_and_b32_e32 v159, 0xffff0000, v203
	v_pk_add_f32 v[156:157], v[156:157], v[158:159]
	v_pk_fma_f32 v[92:93], v[92:93], 0.5, v[156:157] op_sel_hi:[1,0,1]
	v_cvt_pk_bf16_f32 v196, v94, v95
	v_cvt_pk_bf16_f32 v197, v96, v97
	v_cvt_pk_bf16_f32 v198, v90, v91
	v_cvt_pk_bf16_f32 v199, v92, v93
	v_lshlrev_b32_e32 v152, 16, v196
	v_and_b32_e32 v153, 0xffff0000, v196
	v_pk_add_f32 v[152:153], v[94:95], v[152:153] neg_lo:[0,1] neg_hi:[0,1]
	v_lshlrev_b32_e32 v154, 16, v197
	v_and_b32_e32 v155, 0xffff0000, v197
	v_pk_add_f32 v[154:155], v[96:97], v[154:155] neg_lo:[0,1] neg_hi:[0,1]
	v_lshlrev_b32_e32 v156, 16, v198
	v_and_b32_e32 v157, 0xffff0000, v198
	v_pk_add_f32 v[156:157], v[90:91], v[156:157] neg_lo:[0,1] neg_hi:[0,1]
	v_lshlrev_b32_e32 v158, 16, v199
	v_and_b32_e32 v159, 0xffff0000, v199
	v_pk_add_f32 v[158:159], v[92:93], v[158:159] neg_lo:[0,1] neg_hi:[0,1]
	v_cvt_pk_bf16_f32 v200, v152, v153
	v_cvt_pk_bf16_f32 v201, v154, v155
	v_cvt_pk_bf16_f32 v202, v156, v157
	v_cvt_pk_bf16_f32 v203, v158, v159
	v_pk_mul_f32 v[152:153], v[94:95], v[94:95]
	v_pk_mul_f32 v[154:155], v[96:97], v[96:97]
	v_pk_mul_f32 v[156:157], v[90:91], v[90:91]
	v_pk_mul_f32 v[158:159], v[92:93], v[92:93]
	v_pk_add_f32 v[152:153], v[152:153], v[154:155]
	v_pk_add_f32 v[156:157], v[156:157], v[158:159]
	v_pk_add_f32 v[152:153], v[152:153], v[156:157]
	v_add_f32_e32 v242, v152, v153
	v_lshlrev_b32_e32 v152, 16, v204
	v_and_b32_e32 v153, 0xffff0000, v204
	v_lshlrev_b32_e32 v154, 16, v208
	v_and_b32_e32 v155, 0xffff0000, v208
	v_pk_add_f32 v[152:153], v[152:153], v[154:155]
	v_pk_fma_f32 v[86:87], v[86:87], 0.5, v[152:153] op_sel_hi:[1,0,1]
	v_lshlrev_b32_e32 v156, 16, v205
	v_and_b32_e32 v157, 0xffff0000, v205
	v_lshlrev_b32_e32 v158, 16, v209
	v_and_b32_e32 v159, 0xffff0000, v209
	v_pk_add_f32 v[156:157], v[156:157], v[158:159]
	v_pk_fma_f32 v[88:89], v[88:89], 0.5, v[156:157] op_sel_hi:[1,0,1]
	v_lshlrev_b32_e32 v152, 16, v206
	v_and_b32_e32 v153, 0xffff0000, v206
	v_lshlrev_b32_e32 v154, 16, v210
	v_and_b32_e32 v155, 0xffff0000, v210
	v_pk_add_f32 v[152:153], v[152:153], v[154:155]
	v_pk_fma_f32 v[82:83], v[82:83], 0.5, v[152:153] op_sel_hi:[1,0,1]
	v_lshlrev_b32_e32 v156, 16, v207
	v_and_b32_e32 v157, 0xffff0000, v207
	v_lshlrev_b32_e32 v158, 16, v211
	v_and_b32_e32 v159, 0xffff0000, v211
	v_pk_add_f32 v[156:157], v[156:157], v[158:159]
	v_pk_fma_f32 v[84:85], v[84:85], 0.5, v[156:157] op_sel_hi:[1,0,1]
	v_cvt_pk_bf16_f32 v204, v86, v87
	v_cvt_pk_bf16_f32 v205, v88, v89
	v_cvt_pk_bf16_f32 v206, v82, v83
	v_cvt_pk_bf16_f32 v207, v84, v85
	v_lshlrev_b32_e32 v152, 16, v204
	v_and_b32_e32 v153, 0xffff0000, v204
	v_pk_add_f32 v[152:153], v[86:87], v[152:153] neg_lo:[0,1] neg_hi:[0,1]
	v_lshlrev_b32_e32 v154, 16, v205
	v_and_b32_e32 v155, 0xffff0000, v205
	v_pk_add_f32 v[154:155], v[88:89], v[154:155] neg_lo:[0,1] neg_hi:[0,1]
	v_lshlrev_b32_e32 v156, 16, v206
	v_and_b32_e32 v157, 0xffff0000, v206
	v_pk_add_f32 v[156:157], v[82:83], v[156:157] neg_lo:[0,1] neg_hi:[0,1]
	v_lshlrev_b32_e32 v158, 16, v207
	v_and_b32_e32 v159, 0xffff0000, v207
	v_pk_add_f32 v[158:159], v[84:85], v[158:159] neg_lo:[0,1] neg_hi:[0,1]
	v_cvt_pk_bf16_f32 v208, v152, v153
	v_cvt_pk_bf16_f32 v209, v154, v155
	v_cvt_pk_bf16_f32 v210, v156, v157
	v_cvt_pk_bf16_f32 v211, v158, v159
	v_pk_mul_f32 v[152:153], v[86:87], v[86:87]
	v_pk_mul_f32 v[154:155], v[88:89], v[88:89]
	v_pk_mul_f32 v[156:157], v[82:83], v[82:83]
	v_pk_mul_f32 v[158:159], v[84:85], v[84:85]
	v_pk_add_f32 v[152:153], v[152:153], v[154:155]
	v_pk_add_f32 v[156:157], v[156:157], v[158:159]
	v_pk_add_f32 v[152:153], v[152:153], v[156:157]
	v_add_f32_e32 v152, v152, v153
	v_add_f32_e32 v242, v242, v152
	v_lshlrev_b32_e32 v152, 16, v224
	v_and_b32_e32 v153, 0xffff0000, v224
	v_lshlrev_b32_e32 v154, 16, v228
	v_and_b32_e32 v155, 0xffff0000, v228
	v_pk_add_f32 v[152:153], v[152:153], v[154:155]
	v_pk_fma_f32 v[78:79], v[78:79], 0.5, v[152:153] op_sel_hi:[1,0,1]
	v_lshlrev_b32_e32 v156, 16, v225
	v_and_b32_e32 v157, 0xffff0000, v225
	v_lshlrev_b32_e32 v158, 16, v229
	v_and_b32_e32 v159, 0xffff0000, v229
	v_pk_add_f32 v[156:157], v[156:157], v[158:159]
	v_pk_fma_f32 v[80:81], v[80:81], 0.5, v[156:157] op_sel_hi:[1,0,1]
	v_lshlrev_b32_e32 v152, 16, v226
	v_and_b32_e32 v153, 0xffff0000, v226
	v_lshlrev_b32_e32 v154, 16, v230
	v_and_b32_e32 v155, 0xffff0000, v230
	v_pk_add_f32 v[152:153], v[152:153], v[154:155]
	v_pk_fma_f32 v[74:75], v[74:75], 0.5, v[152:153] op_sel_hi:[1,0,1]
	v_lshlrev_b32_e32 v156, 16, v227
	v_and_b32_e32 v157, 0xffff0000, v227
	v_lshlrev_b32_e32 v158, 16, v231
	v_and_b32_e32 v159, 0xffff0000, v231
	v_pk_add_f32 v[156:157], v[156:157], v[158:159]
	v_pk_fma_f32 v[76:77], v[76:77], 0.5, v[156:157] op_sel_hi:[1,0,1]
	v_cvt_pk_bf16_f32 v224, v78, v79
; __device__ __forceinline__ unsigned cvt_pk_bf16(float lo, float hi) { unsigned r; asm volatile("v_cvt_pk_bf16_f32 %0, %1, %2" : "=v"(r) : "v"(lo), "v"(hi)); return r; }
;     __device__ __forceinline__ void operator()(AccRef acc, const Unit& u, int wr, int wc, int, int) const {
;     ...
;             for (int m = 0; m < 4; ++m) {
;                 const int row = row0 + ai * 128 + m * 16; float s = 0.f;
; #pragma unroll
;                 for (int bj = 0; bj < 2; ++bj) {
;                     const size_t p = (size_t)row * D + col0 + bj * 128;
;                     f32x4 x0, x1;
;                     if (xin32) { x0 = *(const f32x4*)(xin32 + p); x1 = *(const f32x4*)(xin32 + p + 4); }
;                     else { const v4u h = *(const v4u*)(xb + p), lo = *(const v4u*)(xl + p);
;                         x0 = (f32x4){bflo(h.x) + bflo(lo.x), bfhi(h.x) + bfhi(lo.x), bflo(h.y) + bflo(lo.y), bfhi(h.y) + bfhi(lo.y)};
;                         x1 = (f32x4){bflo(h.z) + bflo(lo.z), bfhi(h.z) + bfhi(lo.z), bflo(h.w) + bflo(lo.w), bfhi(h.w) + bfhi(lo.w)}; }
;                     x0 = x0 + alpha * acc[ai][bj][m][0]; x1 = x1 + alpha * acc[ai][bj][m][1];
;                     if (PROBE_ON) { x0 = x0 * pscale; x1 = x1 * pscale; if (p == 0) x0[0] += pspike; }
;                     if (xout32) { *(f32x4*)(xout32 + p) = x0; *(f32x4*)(xout32 + p + 4) = x1; }
;                     else {
;                         v4u w; w.x = cvt_pk_bf16(x0[0], x0[1]); w.y = cvt_pk_bf16(x0[2], x0[3]); w.z = cvt_pk_bf16(x1[0], x1[1]); w.w = cvt_pk_bf16(x1[2], x1[3]);
;                         *(v4u*)(xb + p) = w;
;                         const f32x4 r0 = {x0[0] - bflo(w.x), x0[1] - bfhi(w.x), x0[2] - bflo(w.y), x0[3] - bfhi(w.y)}, r1 = {x1[0] - bflo(w.z), x1[1] - bfhi(w.z), x1[2] - bflo(w.w), x1[3] - bfhi(w.w)};
;                         v4u q; q.x = cvt_pk_bf16(r0[0], r0[1]); q.y = cvt_pk_bf16(r0[2], r0[3]); q.z = cvt_pk_bf16(r1[0], r1[1]); q.w = cvt_pk_bf16(r1[2], r1[3]);
;                         *(v4u*)(xl + p) = q;
;                     }
;                     s += (x0[0] * x0[0] + x0[1] * x0[1]) + (x0[2] * x0[2] + x0[3] * x0[3]) + (x1[0] * x1[0] + x1[1] * x1[1]) + (x1[2] * x1[2] + x1[3] * x1[3]);
	v_cvt_pk_bf16_f32 v225, v80, v81
	v_cvt_pk_bf16_f32 v226, v74, v75
	v_cvt_pk_bf16_f32 v227, v76, v77
	v_lshlrev_b32_e32 v152, 16, v224
	v_and_b32_e32 v153, 0xffff0000, v224
	v_pk_add_f32 v[152:153], v[78:79], v[152:153] neg_lo:[0,1] neg_hi:[0,1]
	v_lshlrev_b32_e32 v154, 16, v225
	v_and_b32_e32 v155, 0xffff0000, v225
	v_pk_add_f32 v[154:155], v[80:81], v[154:155] neg_lo:[0,1] neg_hi:[0,1]
	v_lshlrev_b32_e32 v156, 16, v226
	v_and_b32_e32 v157, 0xffff0000, v226
	v_pk_add_f32 v[156:157], v[74:75], v[156:157] neg_lo:[0,1] neg_hi:[0,1]
	v_lshlrev_b32_e32 v158, 16, v227
	v_and_b32_e32 v159, 0xffff0000, v227
	v_pk_add_f32 v[158:159], v[76:77], v[158:159] neg_lo:[0,1] neg_hi:[0,1]
	v_cvt_pk_bf16_f32 v228, v152, v153
	v_cvt_pk_bf16_f32 v229, v154, v155
	v_cvt_pk_bf16_f32 v230, v156, v157
	v_cvt_pk_bf16_f32 v231, v158, v159
	v_pk_mul_f32 v[152:153], v[78:79], v[78:79]
	v_pk_mul_f32 v[154:155], v[80:81], v[80:81]
	v_pk_mul_f32 v[156:157], v[74:75], v[74:75]
	v_pk_mul_f32 v[158:159], v[76:77], v[76:77]
	v_pk_add_f32 v[152:153], v[152:153], v[154:155]
	v_pk_add_f32 v[156:157], v[156:157], v[158:159]
	v_pk_add_f32 v[152:153], v[152:153], v[156:157]
	v_add_f32_e32 v243, v152, v153
	v_lshlrev_b32_e32 v152, 16, v232
	v_and_b32_e32 v153, 0xffff0000, v232
	v_lshlrev_b32_e32 v154, 16, v236
	v_and_b32_e32 v155, 0xffff0000, v236
	v_pk_add_f32 v[152:153], v[152:153], v[154:155]
	v_pk_fma_f32 v[70:71], v[70:71], 0.5, v[152:153] op_sel_hi:[1,0,1]
	v_lshlrev_b32_e32 v156, 16, v233
	v_and_b32_e32 v157, 0xffff0000, v233
	v_lshlrev_b32_e32 v158, 16, v237
	v_and_b32_e32 v159, 0xffff0000, v237
	v_pk_add_f32 v[156:157], v[156:157], v[158:159]
	v_pk_fma_f32 v[72:73], v[72:73], 0.5, v[156:157] op_sel_hi:[1,0,1]
	v_lshlrev_b32_e32 v152, 16, v234
	v_and_b32_e32 v153, 0xffff0000, v234
	v_lshlrev_b32_e32 v154, 16, v238
	v_and_b32_e32 v155, 0xffff0000, v238
	v_pk_add_f32 v[152:153], v[152:153], v[154:155]
	v_pk_fma_f32 v[66:67], v[66:67], 0.5, v[152:153] op_sel_hi:[1,0,1]
	v_lshlrev_b32_e32 v156, 16, v235
	v_and_b32_e32 v157, 0xffff0000, v235
	v_lshlrev_b32_e32 v158, 16, v239
	v_and_b32_e32 v159, 0xffff0000, v239
	v_pk_add_f32 v[156:157], v[156:157], v[158:159]
	v_pk_fma_f32 v[68:69], v[68:69], 0.5, v[156:157] op_sel_hi:[1,0,1]
	v_cvt_pk_bf16_f32 v232, v70, v71
	v_cvt_pk_bf16_f32 v233, v72, v73
	v_cvt_pk_bf16_f32 v234, v66, v67
	v_cvt_pk_bf16_f32 v235, v68, v69
	v_lshlrev_b32_e32 v152, 16, v232
	v_and_b32_e32 v153, 0xffff0000, v232
	v_pk_add_f32 v[152:153], v[70:71], v[152:153] neg_lo:[0,1] neg_hi:[0,1]
	v_lshlrev_b32_e32 v154, 16, v233
	v_and_b32_e32 v155, 0xffff0000, v233
	v_pk_add_f32 v[154:155], v[72:73], v[154:155] neg_lo:[0,1] neg_hi:[0,1]
	v_lshlrev_b32_e32 v156, 16, v234
	v_and_b32_e32 v157, 0xffff0000, v234
	v_pk_add_f32 v[156:157], v[66:67], v[156:157] neg_lo:[0,1] neg_hi:[0,1]
	v_lshlrev_b32_e32 v158, 16, v235
	v_and_b32_e32 v159, 0xffff0000, v235
	v_pk_add_f32 v[158:159], v[68:69], v[158:159] neg_lo:[0,1] neg_hi:[0,1]
	v_cvt_pk_bf16_f32 v236, v152, v153
	v_cvt_pk_bf16_f32 v237, v154, v155
	v_cvt_pk_bf16_f32 v238, v156, v157
	v_cvt_pk_bf16_f32 v239, v158, v159
	v_pk_mul_f32 v[152:153], v[70:71], v[70:71]
	v_pk_mul_f32 v[154:155], v[72:73], v[72:73]
	v_pk_mul_f32 v[156:157], v[66:67], v[66:67]
	v_pk_mul_f32 v[158:159], v[68:69], v[68:69]
	v_pk_add_f32 v[152:153], v[152:153], v[154:155]
	v_pk_add_f32 v[156:157], v[156:157], v[158:159]
	v_pk_add_f32 v[152:153], v[152:153], v[156:157]
	v_add_f32_e32 v152, v152, v153
	v_add_f32_e32 v243, v243, v152
	s_add_u32 s28, s12, 0x20000
	s_addc_u32 s29, s13, 0
	s_add_u32 s98, s14, 0x20000
	s_addc_u32 s99, s15, 0
	global_store_dwordx4 v248, v[196:199], s[28:29]
	global_store_dwordx4 v248, v[200:203], s[98:99]
	global_store_dwordx4 v248, v[204:207], s[28:29] offset:256
	global_store_dwordx4 v248, v[208:211], s[98:99] offset:256
	s_add_u32 s28, s12, 0x30000
	s_addc_u32 s29, s13, 0
	s_add_u32 s98, s14, 0x30000
	s_addc_u32 s99, s15, 0
	global_store_dwordx4 v248, v[224:227], s[28:29]
	global_store_dwordx4 v248, v[228:231], s[98:99]
	global_store_dwordx4 v248, v[232:235], s[28:29] offset:256
	global_store_dwordx4 v248, v[236:239], s[98:99] offset:256
	s_add_u32 s28, s12, 0xa0000
	s_addc_u32 s29, s13, 0
	s_add_u32 s98, s14, 0xa0000
	s_addc_u32 s99, s15, 0
	global_load_dwordx4 v[196:199], v248, s[28:29]
	global_load_dwordx4 v[200:203], v248, s[98:99]
	global_load_dwordx4 v[204:207], v248, s[28:29] offset:256
	global_load_dwordx4 v[208:211], v248, s[98:99] offset:256
	s_add_u32 s28, s12, 0xb0000
	s_addc_u32 s29, s13, 0
	s_add_u32 s98, s14, 0xb0000
	s_addc_u32 s99, s15, 0
	global_load_dwordx4 v[224:227], v248, s[28:29]
	global_load_dwordx4 v[228:231], v248, s[98:99]
	global_load_dwordx4 v[232:235], v248, s[28:29] offset:256
	global_load_dwordx4 v[236:239], v248, s[98:99] offset:256
	s_waitcnt vmcnt(16)
; __device__ __forceinline__ unsigned cvt_pk_bf16(float lo, float hi) { unsigned r; asm volatile("v_cvt_pk_bf16_f32 %0, %1, %2" : "=v"(r) : "v"(lo), "v"(hi)); return r; }
;     __device__ __forceinline__ void operator()(AccRef acc, const Unit& u, int wr, int wc, int, int) const {
;     ...
;             for (int m = 0; m < 4; ++m) {
;                 const int row = row0 + ai * 128 + m * 16; float s = 0.f;
; #pragma unroll
;                 for (int bj = 0; bj < 2; ++bj) {
;                     const size_t p = (size_t)row * D + col0 + bj * 128;
;                     f32x4 x0, x1;
;                     if (xin32) { x0 = *(const f32x4*)(xin32 + p); x1 = *(const f32x4*)(xin32 + p + 4); }
;                     else { const v4u h = *(const v4u*)(xb + p), lo = *(const v4u*)(xl + p);
;                         x0 = (f32x4){bflo(h.x) + bflo(lo.x), bfhi(h.x) + bfhi(lo.x), bflo(h.y) + bflo(lo.y), bfhi(h.y) + bfhi(lo.y)};
;                         x1 = (f32x4){bflo(h.z) + bflo(lo.z), bfhi(h.z) + bfhi(lo.z), bflo(h.w) + bflo(lo.w), bfhi(h.w) + bfhi(lo.w)}; }
;                     x0 = x0 + alpha * acc[ai][bj][m][0]; x1 = x1 + alpha * acc[ai][bj][m][1];
;                     if (PROBE_ON) { x0 = x0 * pscale; x1 = x1 * pscale; if (p == 0) x0[0] += pspike; }
;                     if (xout32) { *(f32x4*)(xout32 + p) = x0; *(f32x4*)(xout32 + p + 4) = x1; }
;                     else {
;                         v4u w; w.x = cvt_pk_bf16(x0[0], x0[1]); w.y = cvt_pk_bf16(x0[2], x0[3]); w.z = cvt_pk_bf16(x1[0], x1[1]); w.w = cvt_pk_bf16(x1[2], x1[3]);
;                         *(v4u*)(xb + p) = w;
;                         const f32x4 r0 = {x0[0] - bflo(w.x), x0[1] - bfhi(w.x), x0[2] - bflo(w.y), x0[3] - bfhi(w.y)}, r1 = {x1[0] - bflo(w.z), x1[1] - bfhi(w.z), x1[2] - bflo(w.w), x1[3] - bfhi(w.w)};
;                         v4u q; q.x = cvt_pk_bf16(r0[0], r0[1]); q.y = cvt_pk_bf16(r0[2], r0[3]); q.z = cvt_pk_bf16(r1[0], r1[1]); q.w = cvt_pk_bf16(r1[2], r1[3]);
;                         *(v4u*)(xl + p) = q;
;                     }
;                     s += (x0[0] * x0[0] + x0[1] * x0[1]) + (x0[2] * x0[2] + x0[3] * x0[3]) + (x1[0] * x1[0] + x1[1] * x1[1]) + (x1[2] * x1[2] + x1[3] * x1[3]);
	v_lshlrev_b32_e32 v152, 16, v164
	v_and_b32_e32 v153, 0xffff0000, v164
	v_lshlrev_b32_e32 v154, 16, v168
	v_and_b32_e32 v155, 0xffff0000, v168
	v_pk_add_f32 v[152:153], v[152:153], v[154:155]
	v_pk_fma_f32 v[62:63], v[62:63], 0.5, v[152:153] op_sel_hi:[1,0,1]
	v_lshlrev_b32_e32 v156, 16, v165
	v_and_b32_e32 v157, 0xffff0000, v165
	v_lshlrev_b32_e32 v158, 16, v169
	v_and_b32_e32 v159, 0xffff0000, v169
	v_pk_add_f32 v[156:157], v[156:157], v[158:159]
	v_pk_fma_f32 v[64:65], v[64:65], 0.5, v[156:157] op_sel_hi:[1,0,1]
	v_lshlrev_b32_e32 v152, 16, v166
	v_and_b32_e32 v153, 0xffff0000, v166
	v_lshlrev_b32_e32 v154, 16, v170
	v_and_b32_e32 v155, 0xffff0000, v170
	v_pk_add_f32 v[152:153], v[152:153], v[154:155]
	v_pk_fma_f32 v[58:59], v[58:59], 0.5, v[152:153] op_sel_hi:[1,0,1]
	v_lshlrev_b32_e32 v156, 16, v167
	v_and_b32_e32 v157, 0xffff0000, v167
	v_lshlrev_b32_e32 v158, 16, v171
	v_and_b32_e32 v159, 0xffff0000, v171
	v_pk_add_f32 v[156:157], v[156:157], v[158:159]
	v_pk_fma_f32 v[60:61], v[60:61], 0.5, v[156:157] op_sel_hi:[1,0,1]
	v_cvt_pk_bf16_f32 v164, v62, v63
	v_cvt_pk_bf16_f32 v165, v64, v65
	v_cvt_pk_bf16_f32 v166, v58, v59
	v_cvt_pk_bf16_f32 v167, v60, v61
	v_lshlrev_b32_e32 v152, 16, v164
	v_and_b32_e32 v153, 0xffff0000, v164
	v_pk_add_f32 v[152:153], v[62:63], v[152:153] neg_lo:[0,1] neg_hi:[0,1]
	v_lshlrev_b32_e32 v154, 16, v165
	v_and_b32_e32 v155, 0xffff0000, v165
	v_pk_add_f32 v[154:155], v[64:65], v[154:155] neg_lo:[0,1] neg_hi:[0,1]
	v_lshlrev_b32_e32 v156, 16, v166
	v_and_b32_e32 v157, 0xffff0000, v166
	v_pk_add_f32 v[156:157], v[58:59], v[156:157] neg_lo:[0,1] neg_hi:[0,1]
	v_lshlrev_b32_e32 v158, 16, v167
	v_and_b32_e32 v159, 0xffff0000, v167
	v_pk_add_f32 v[158:159], v[60:61], v[158:159] neg_lo:[0,1] neg_hi:[0,1]
	v_cvt_pk_bf16_f32 v168, v152, v153
	v_cvt_pk_bf16_f32 v169, v154, v155
	v_cvt_pk_bf16_f32 v170, v156, v157
	v_cvt_pk_bf16_f32 v171, v158, v159
	v_pk_mul_f32 v[152:153], v[62:63], v[62:63]
	v_pk_mul_f32 v[154:155], v[64:65], v[64:65]
	v_pk_mul_f32 v[156:157], v[58:59], v[58:59]
	v_pk_mul_f32 v[158:159], v[60:61], v[60:61]
	v_pk_add_f32 v[152:153], v[152:153], v[154:155]
	v_pk_add_f32 v[156:157], v[156:157], v[158:159]
	v_pk_add_f32 v[152:153], v[152:153], v[156:157]
	v_add_f32_e32 v244, v152, v153
	v_lshlrev_b32_e32 v152, 16, v172
	v_and_b32_e32 v153, 0xffff0000, v172
	v_lshlrev_b32_e32 v154, 16, v176
	v_and_b32_e32 v155, 0xffff0000, v176
	v_pk_add_f32 v[152:153], v[152:153], v[154:155]
	v_pk_fma_f32 v[54:55], v[54:55], 0.5, v[152:153] op_sel_hi:[1,0,1]
	v_lshlrev_b32_e32 v156, 16, v173
	v_and_b32_e32 v157, 0xffff0000, v173
	v_lshlrev_b32_e32 v158, 16, v177
	v_and_b32_e32 v159, 0xffff0000, v177
	v_pk_add_f32 v[156:157], v[156:157], v[158:159]
	v_pk_fma_f32 v[56:57], v[56:57], 0.5, v[156:157] op_sel_hi:[1,0,1]
	v_lshlrev_b32_e32 v152, 16, v174
	v_and_b32_e32 v153, 0xffff0000, v174
	v_lshlrev_b32_e32 v154, 16, v178
	v_and_b32_e32 v155, 0xffff0000, v178
	v_pk_add_f32 v[152:153], v[152:153], v[154:155]
	v_pk_fma_f32 v[50:51], v[50:51], 0.5, v[152:153] op_sel_hi:[1,0,1]
	v_lshlrev_b32_e32 v156, 16, v175
	v_and_b32_e32 v157, 0xffff0000, v175
	v_lshlrev_b32_e32 v158, 16, v179
	v_and_b32_e32 v159, 0xffff0000, v179
	v_pk_add_f32 v[156:157], v[156:157], v[158:159]
	v_pk_fma_f32 v[52:53], v[52:53], 0.5, v[156:157] op_sel_hi:[1,0,1]
	v_cvt_pk_bf16_f32 v172, v54, v55
	v_cvt_pk_bf16_f32 v173, v56, v57
	v_cvt_pk_bf16_f32 v174, v50, v51
	v_cvt_pk_bf16_f32 v175, v52, v53
	v_lshlrev_b32_e32 v152, 16, v172
	v_and_b32_e32 v153, 0xffff0000, v172
	v_pk_add_f32 v[152:153], v[54:55], v[152:153] neg_lo:[0,1] neg_hi:[0,1]
	v_lshlrev_b32_e32 v154, 16, v173
	v_and_b32_e32 v155, 0xffff0000, v173
	v_pk_add_f32 v[154:155], v[56:57], v[154:155] neg_lo:[0,1] neg_hi:[0,1]
	v_lshlrev_b32_e32 v156, 16, v174
	v_and_b32_e32 v157, 0xffff0000, v174
	v_pk_add_f32 v[156:157], v[50:51], v[156:157] neg_lo:[0,1] neg_hi:[0,1]
	v_lshlrev_b32_e32 v158, 16, v175
	v_and_b32_e32 v159, 0xffff0000, v175
	v_pk_add_f32 v[158:159], v[52:53], v[158:159] neg_lo:[0,1] neg_hi:[0,1]
	v_cvt_pk_bf16_f32 v176, v152, v153
	v_cvt_pk_bf16_f32 v177, v154, v155
	v_cvt_pk_bf16_f32 v178, v156, v157
	v_cvt_pk_bf16_f32 v179, v158, v159
	v_pk_mul_f32 v[152:153], v[54:55], v[54:55]
	v_pk_mul_f32 v[154:155], v[56:57], v[56:57]
	v_pk_mul_f32 v[156:157], v[50:51], v[50:51]
	v_pk_mul_f32 v[158:159], v[52:53], v[52:53]
	v_pk_add_f32 v[152:153], v[152:153], v[154:155]
	v_pk_add_f32 v[156:157], v[156:157], v[158:159]
	v_pk_add_f32 v[152:153], v[152:153], v[156:157]
	v_add_f32_e32 v152, v152, v153
	v_add_f32_e32 v244, v244, v152
	v_lshlrev_b32_e32 v152, 16, v180
	v_and_b32_e32 v153, 0xffff0000, v180
	v_lshlrev_b32_e32 v154, 16, v184
	v_and_b32_e32 v155, 0xffff0000, v184
	v_pk_add_f32 v[152:153], v[152:153], v[154:155]
	v_pk_fma_f32 v[46:47], v[46:47], 0.5, v[152:153] op_sel_hi:[1,0,1]
	v_lshlrev_b32_e32 v156, 16, v181
	v_and_b32_e32 v157, 0xffff0000, v181
	v_lshlrev_b32_e32 v158, 16, v185
	v_and_b32_e32 v159, 0xffff0000, v185
	v_pk_add_f32 v[156:157], v[156:157], v[158:159]
	v_pk_fma_f32 v[48:49], v[48:49], 0.5, v[156:157] op_sel_hi:[1,0,1]
	v_lshlrev_b32_e32 v152, 16, v182
	v_and_b32_e32 v153, 0xffff0000, v182
	v_lshlrev_b32_e32 v154, 16, v186
	v_and_b32_e32 v155, 0xffff0000, v186
	v_pk_add_f32 v[152:153], v[152:153], v[154:155]
	v_pk_fma_f32 v[42:43], v[42:43], 0.5, v[152:153] op_sel_hi:[1,0,1]
	v_lshlrev_b32_e32 v156, 16, v183
	v_and_b32_e32 v157, 0xffff0000, v183
	v_lshlrev_b32_e32 v158, 16, v187
	v_and_b32_e32 v159, 0xffff0000, v187
	v_pk_add_f32 v[156:157], v[156:157], v[158:159]
	v_pk_fma_f32 v[44:45], v[44:45], 0.5, v[156:157] op_sel_hi:[1,0,1]
	v_cvt_pk_bf16_f32 v180, v46, v47
; __device__ __forceinline__ unsigned cvt_pk_bf16(float lo, float hi) { unsigned r; asm volatile("v_cvt_pk_bf16_f32 %0, %1, %2" : "=v"(r) : "v"(lo), "v"(hi)); return r; }
;     __device__ __forceinline__ void operator()(AccRef acc, const Unit& u, int wr, int wc, int, int) const {
;     ...
;             for (int m = 0; m < 4; ++m) {
;                 const int row = row0 + ai * 128 + m * 16; float s = 0.f;
; #pragma unroll
;                 for (int bj = 0; bj < 2; ++bj) {
;                     const size_t p = (size_t)row * D + col0 + bj * 128;
;                     f32x4 x0, x1;
;                     if (xin32) { x0 = *(const f32x4*)(xin32 + p); x1 = *(const f32x4*)(xin32 + p + 4); }
;                     else { const v4u h = *(const v4u*)(xb + p), lo = *(const v4u*)(xl + p);
;                         x0 = (f32x4){bflo(h.x) + bflo(lo.x), bfhi(h.x) + bfhi(lo.x), bflo(h.y) + bflo(lo.y), bfhi(h.y) + bfhi(lo.y)};
;                         x1 = (f32x4){bflo(h.z) + bflo(lo.z), bfhi(h.z) + bfhi(lo.z), bflo(h.w) + bflo(lo.w), bfhi(h.w) + bfhi(lo.w)}; }
;                     x0 = x0 + alpha * acc[ai][bj][m][0]; x1 = x1 + alpha * acc[ai][bj][m][1];
;                     if (PROBE_ON) { x0 = x0 * pscale; x1 = x1 * pscale; if (p == 0) x0[0] += pspike; }
;                     if (xout32) { *(f32x4*)(xout32 + p) = x0; *(f32x4*)(xout32 + p + 4) = x1; }
;                     else {
;                         v4u w; w.x = cvt_pk_bf16(x0[0], x0[1]); w.y = cvt_pk_bf16(x0[2], x0[3]); w.z = cvt_pk_bf16(x1[0], x1[1]); w.w = cvt_pk_bf16(x1[2], x1[3]);
;                         *(v4u*)(xb + p) = w;
;                         const f32x4 r0 = {x0[0] - bflo(w.x), x0[1] - bfhi(w.x), x0[2] - bflo(w.y), x0[3] - bfhi(w.y)}, r1 = {x1[0] - bflo(w.z), x1[1] - bfhi(w.z), x1[2] - bflo(w.w), x1[3] - bfhi(w.w)};
;                         v4u q; q.x = cvt_pk_bf16(r0[0], r0[1]); q.y = cvt_pk_bf16(r0[2], r0[3]); q.z = cvt_pk_bf16(r1[0], r1[1]); q.w = cvt_pk_bf16(r1[2], r1[3]);
;                         *(v4u*)(xl + p) = q;
;                     }
;                     s += (x0[0] * x0[0] + x0[1] * x0[1]) + (x0[2] * x0[2] + x0[3] * x0[3]) + (x1[0] * x1[0] + x1[1] * x1[1]) + (x1[2] * x1[2] + x1[3] * x1[3]);
	v_cvt_pk_bf16_f32 v181, v48, v49
	v_cvt_pk_bf16_f32 v182, v42, v43
	v_cvt_pk_bf16_f32 v183, v44, v45
	v_lshlrev_b32_e32 v152, 16, v180
	v_and_b32_e32 v153, 0xffff0000, v180
	v_pk_add_f32 v[152:153], v[46:47], v[152:153] neg_lo:[0,1] neg_hi:[0,1]
	v_lshlrev_b32_e32 v154, 16, v181
	v_and_b32_e32 v155, 0xffff0000, v181
	v_pk_add_f32 v[154:155], v[48:49], v[154:155] neg_lo:[0,1] neg_hi:[0,1]
	v_lshlrev_b32_e32 v156, 16, v182
	v_and_b32_e32 v157, 0xffff0000, v182
	v_pk_add_f32 v[156:157], v[42:43], v[156:157] neg_lo:[0,1] neg_hi:[0,1]
	v_lshlrev_b32_e32 v158, 16, v183
	v_and_b32_e32 v159, 0xffff0000, v183
	v_pk_add_f32 v[158:159], v[44:45], v[158:159] neg_lo:[0,1] neg_hi:[0,1]
	v_cvt_pk_bf16_f32 v184, v152, v153
	v_cvt_pk_bf16_f32 v185, v154, v155
	v_cvt_pk_bf16_f32 v186, v156, v157
	v_cvt_pk_bf16_f32 v187, v158, v159
	v_pk_mul_f32 v[152:153], v[46:47], v[46:47]
	v_pk_mul_f32 v[154:155], v[48:49], v[48:49]
	v_pk_mul_f32 v[156:157], v[42:43], v[42:43]
	v_pk_mul_f32 v[158:159], v[44:45], v[44:45]
	v_pk_add_f32 v[152:153], v[152:153], v[154:155]
	v_pk_add_f32 v[156:157], v[156:157], v[158:159]
	v_pk_add_f32 v[152:153], v[152:153], v[156:157]
	v_add_f32_e32 v245, v152, v153
	v_lshlrev_b32_e32 v152, 16, v188
	v_and_b32_e32 v153, 0xffff0000, v188
	v_lshlrev_b32_e32 v154, 16, v192
	v_and_b32_e32 v155, 0xffff0000, v192
	v_pk_add_f32 v[152:153], v[152:153], v[154:155]
	v_pk_fma_f32 v[38:39], v[38:39], 0.5, v[152:153] op_sel_hi:[1,0,1]
	v_lshlrev_b32_e32 v156, 16, v189
	v_and_b32_e32 v157, 0xffff0000, v189
	v_lshlrev_b32_e32 v158, 16, v193
	v_and_b32_e32 v159, 0xffff0000, v193
	v_pk_add_f32 v[156:157], v[156:157], v[158:159]
	v_pk_fma_f32 v[40:41], v[40:41], 0.5, v[156:157] op_sel_hi:[1,0,1]
	v_lshlrev_b32_e32 v152, 16, v190
	v_and_b32_e32 v153, 0xffff0000, v190
	v_lshlrev_b32_e32 v154, 16, v194
	v_and_b32_e32 v155, 0xffff0000, v194
	v_pk_add_f32 v[152:153], v[152:153], v[154:155]
	v_pk_fma_f32 v[34:35], v[34:35], 0.5, v[152:153] op_sel_hi:[1,0,1]
	v_lshlrev_b32_e32 v156, 16, v191
	v_and_b32_e32 v157, 0xffff0000, v191
	v_lshlrev_b32_e32 v158, 16, v195
	v_and_b32_e32 v159, 0xffff0000, v195
	v_pk_add_f32 v[156:157], v[156:157], v[158:159]
	v_pk_fma_f32 v[36:37], v[36:37], 0.5, v[156:157] op_sel_hi:[1,0,1]
	v_cvt_pk_bf16_f32 v188, v38, v39
	v_cvt_pk_bf16_f32 v189, v40, v41
	v_cvt_pk_bf16_f32 v190, v34, v35
	v_cvt_pk_bf16_f32 v191, v36, v37
	v_lshlrev_b32_e32 v152, 16, v188
	v_and_b32_e32 v153, 0xffff0000, v188
	v_pk_add_f32 v[152:153], v[38:39], v[152:153] neg_lo:[0,1] neg_hi:[0,1]
	v_lshlrev_b32_e32 v154, 16, v189
	v_and_b32_e32 v155, 0xffff0000, v189
	v_pk_add_f32 v[154:155], v[40:41], v[154:155] neg_lo:[0,1] neg_hi:[0,1]
	v_lshlrev_b32_e32 v156, 16, v190
	v_and_b32_e32 v157, 0xffff0000, v190
	v_pk_add_f32 v[156:157], v[34:35], v[156:157] neg_lo:[0,1] neg_hi:[0,1]
	v_lshlrev_b32_e32 v158, 16, v191
	v_and_b32_e32 v159, 0xffff0000, v191
	v_pk_add_f32 v[158:159], v[36:37], v[158:159] neg_lo:[0,1] neg_hi:[0,1]
	v_cvt_pk_bf16_f32 v192, v152, v153
	v_cvt_pk_bf16_f32 v193, v154, v155
	v_cvt_pk_bf16_f32 v194, v156, v157
	v_cvt_pk_bf16_f32 v195, v158, v159
	v_pk_mul_f32 v[152:153], v[38:39], v[38:39]
	v_pk_mul_f32 v[154:155], v[40:41], v[40:41]
	v_pk_mul_f32 v[156:157], v[34:35], v[34:35]
	v_pk_mul_f32 v[158:159], v[36:37], v[36:37]
	v_pk_add_f32 v[152:153], v[152:153], v[154:155]
	v_pk_add_f32 v[156:157], v[156:157], v[158:159]
	v_pk_add_f32 v[152:153], v[152:153], v[156:157]
	v_add_f32_e32 v152, v152, v153
	v_add_f32_e32 v245, v245, v152
	s_add_u32 s28, s12, 0x80000
	s_addc_u32 s29, s13, 0
	s_add_u32 s98, s14, 0x80000
	s_addc_u32 s99, s15, 0
	global_store_dwordx4 v248, v[164:167], s[28:29]
	global_store_dwordx4 v248, v[168:171], s[98:99]
	global_store_dwordx4 v248, v[172:175], s[28:29] offset:256
	global_store_dwordx4 v248, v[176:179], s[98:99] offset:256
	s_add_u32 s28, s12, 0x90000
	s_addc_u32 s29, s13, 0
	s_add_u32 s98, s14, 0x90000
	s_addc_u32 s99, s15, 0
	global_store_dwordx4 v248, v[180:183], s[28:29]
	global_store_dwordx4 v248, v[184:187], s[98:99]
	global_store_dwordx4 v248, v[188:191], s[28:29] offset:256
	global_store_dwordx4 v248, v[192:195], s[98:99] offset:256
	s_waitcnt vmcnt(8)
	v_lshlrev_b32_e32 v152, 16, v196
	v_and_b32_e32 v153, 0xffff0000, v196
	v_lshlrev_b32_e32 v154, 16, v200
	v_and_b32_e32 v155, 0xffff0000, v200
	v_pk_add_f32 v[152:153], v[152:153], v[154:155]
	v_pk_fma_f32 v[30:31], v[30:31], 0.5, v[152:153] op_sel_hi:[1,0,1]
	v_lshlrev_b32_e32 v156, 16, v197
	v_and_b32_e32 v157, 0xffff0000, v197
	v_lshlrev_b32_e32 v158, 16, v201
	v_and_b32_e32 v159, 0xffff0000, v201
	v_pk_add_f32 v[156:157], v[156:157], v[158:159]
	v_pk_fma_f32 v[32:33], v[32:33], 0.5, v[156:157] op_sel_hi:[1,0,1]
	v_lshlrev_b32_e32 v152, 16, v198
	v_and_b32_e32 v153, 0xffff0000, v198
	v_lshlrev_b32_e32 v154, 16, v202
	v_and_b32_e32 v155, 0xffff0000, v202
	v_pk_add_f32 v[152:153], v[152:153], v[154:155]
	v_pk_fma_f32 v[26:27], v[26:27], 0.5, v[152:153] op_sel_hi:[1,0,1]
	v_lshlrev_b32_e32 v156, 16, v199
	v_and_b32_e32 v157, 0xffff0000, v199
	v_lshlrev_b32_e32 v158, 16, v203
	v_and_b32_e32 v159, 0xffff0000, v203
	v_pk_add_f32 v[156:157], v[156:157], v[158:159]
	v_pk_fma_f32 v[28:29], v[28:29], 0.5, v[156:157] op_sel_hi:[1,0,1]
	v_cvt_pk_bf16_f32 v196, v30, v31
	v_cvt_pk_bf16_f32 v197, v32, v33
	v_cvt_pk_bf16_f32 v198, v26, v27
	v_cvt_pk_bf16_f32 v199, v28, v29
	v_lshlrev_b32_e32 v152, 16, v196
	v_and_b32_e32 v153, 0xffff0000, v196
	v_pk_add_f32 v[152:153], v[30:31], v[152:153] neg_lo:[0,1] neg_hi:[0,1]
	v_lshlrev_b32_e32 v154, 16, v197
	v_and_b32_e32 v155, 0xffff0000, v197
	v_pk_add_f32 v[154:155], v[32:33], v[154:155] neg_lo:[0,1] neg_hi:[0,1]
	v_lshlrev_b32_e32 v156, 16, v198
; __device__ __forceinline__ unsigned cvt_pk_bf16(float lo, float hi) { unsigned r; asm volatile("v_cvt_pk_bf16_f32 %0, %1, %2" : "=v"(r) : "v"(lo), "v"(hi)); return r; }
;     __device__ __forceinline__ void operator()(AccRef acc, const Unit& u, int wr, int wc, int, int) const {
;     ...
;             for (int m = 0; m < 4; ++m) {
;                 const int row = row0 + ai * 128 + m * 16; float s = 0.f;
; #pragma unroll
;                 for (int bj = 0; bj < 2; ++bj) {
;                     const size_t p = (size_t)row * D + col0 + bj * 128;
;                     f32x4 x0, x1;
;                     if (xin32) { x0 = *(const f32x4*)(xin32 + p); x1 = *(const f32x4*)(xin32 + p + 4); }
;                     else { const v4u h = *(const v4u*)(xb + p), lo = *(const v4u*)(xl + p);
;                         x0 = (f32x4){bflo(h.x) + bflo(lo.x), bfhi(h.x) + bfhi(lo.x), bflo(h.y) + bflo(lo.y), bfhi(h.y) + bfhi(lo.y)};
;                         x1 = (f32x4){bflo(h.z) + bflo(lo.z), bfhi(h.z) + bfhi(lo.z), bflo(h.w) + bflo(lo.w), bfhi(h.w) + bfhi(lo.w)}; }
;                     x0 = x0 + alpha * acc[ai][bj][m][0]; x1 = x1 + alpha * acc[ai][bj][m][1];
;                     if (PROBE_ON) { x0 = x0 * pscale; x1 = x1 * pscale; if (p == 0) x0[0] += pspike; }
;                     if (xout32) { *(f32x4*)(xout32 + p) = x0; *(f32x4*)(xout32 + p + 4) = x1; }
;                     else {
;                         v4u w; w.x = cvt_pk_bf16(x0[0], x0[1]); w.y = cvt_pk_bf16(x0[2], x0[3]); w.z = cvt_pk_bf16(x1[0], x1[1]); w.w = cvt_pk_bf16(x1[2], x1[3]);
;                         *(v4u*)(xb + p) = w;
;                         const f32x4 r0 = {x0[0] - bflo(w.x), x0[1] - bfhi(w.x), x0[2] - bflo(w.y), x0[3] - bfhi(w.y)}, r1 = {x1[0] - bflo(w.z), x1[1] - bfhi(w.z), x1[2] - bflo(w.w), x1[3] - bfhi(w.w)};
;                         v4u q; q.x = cvt_pk_bf16(r0[0], r0[1]); q.y = cvt_pk_bf16(r0[2], r0[3]); q.z = cvt_pk_bf16(r1[0], r1[1]); q.w = cvt_pk_bf16(r1[2], r1[3]);
;                         *(v4u*)(xl + p) = q;
;                     }
;                     s += (x0[0] * x0[0] + x0[1] * x0[1]) + (x0[2] * x0[2] + x0[3] * x0[3]) + (x1[0] * x1[0] + x1[1] * x1[1]) + (x1[2] * x1[2] + x1[3] * x1[3]);
	v_and_b32_e32 v157, 0xffff0000, v198
	v_pk_add_f32 v[156:157], v[26:27], v[156:157] neg_lo:[0,1] neg_hi:[0,1]
	v_lshlrev_b32_e32 v158, 16, v199
	v_and_b32_e32 v159, 0xffff0000, v199
	v_pk_add_f32 v[158:159], v[28:29], v[158:159] neg_lo:[0,1] neg_hi:[0,1]
	v_cvt_pk_bf16_f32 v200, v152, v153
	v_cvt_pk_bf16_f32 v201, v154, v155
	v_cvt_pk_bf16_f32 v202, v156, v157
	v_cvt_pk_bf16_f32 v203, v158, v159
	v_pk_mul_f32 v[152:153], v[30:31], v[30:31]
	v_pk_mul_f32 v[154:155], v[32:33], v[32:33]
	v_pk_mul_f32 v[156:157], v[26:27], v[26:27]
	v_pk_mul_f32 v[158:159], v[28:29], v[28:29]
	v_pk_add_f32 v[152:153], v[152:153], v[154:155]
	v_pk_add_f32 v[156:157], v[156:157], v[158:159]
	v_pk_add_f32 v[152:153], v[152:153], v[156:157]
	v_add_f32_e32 v246, v152, v153
	v_lshlrev_b32_e32 v152, 16, v204
	v_and_b32_e32 v153, 0xffff0000, v204
	v_lshlrev_b32_e32 v154, 16, v208
	v_and_b32_e32 v155, 0xffff0000, v208
	v_pk_add_f32 v[152:153], v[152:153], v[154:155]
	v_pk_fma_f32 v[22:23], v[22:23], 0.5, v[152:153] op_sel_hi:[1,0,1]
	v_lshlrev_b32_e32 v156, 16, v205
	v_and_b32_e32 v157, 0xffff0000, v205
	v_lshlrev_b32_e32 v158, 16, v209
	v_and_b32_e32 v159, 0xffff0000, v209
	v_pk_add_f32 v[156:157], v[156:157], v[158:159]
	v_pk_fma_f32 v[24:25], v[24:25], 0.5, v[156:157] op_sel_hi:[1,0,1]
	v_lshlrev_b32_e32 v152, 16, v206
	v_and_b32_e32 v153, 0xffff0000, v206
	v_lshlrev_b32_e32 v154, 16, v210
	v_and_b32_e32 v155, 0xffff0000, v210
	v_pk_add_f32 v[152:153], v[152:153], v[154:155]
	v_pk_fma_f32 v[18:19], v[18:19], 0.5, v[152:153] op_sel_hi:[1,0,1]
	v_lshlrev_b32_e32 v156, 16, v207
	v_and_b32_e32 v157, 0xffff0000, v207
	v_lshlrev_b32_e32 v158, 16, v211
	v_and_b32_e32 v159, 0xffff0000, v211
	v_pk_add_f32 v[156:157], v[156:157], v[158:159]
	v_pk_fma_f32 v[20:21], v[20:21], 0.5, v[156:157] op_sel_hi:[1,0,1]
	v_cvt_pk_bf16_f32 v204, v22, v23
	v_cvt_pk_bf16_f32 v205, v24, v25
	v_cvt_pk_bf16_f32 v206, v18, v19
	v_cvt_pk_bf16_f32 v207, v20, v21
	v_lshlrev_b32_e32 v152, 16, v204
	v_and_b32_e32 v153, 0xffff0000, v204
	v_pk_add_f32 v[152:153], v[22:23], v[152:153] neg_lo:[0,1] neg_hi:[0,1]
	v_lshlrev_b32_e32 v154, 16, v205
	v_and_b32_e32 v155, 0xffff0000, v205
	v_pk_add_f32 v[154:155], v[24:25], v[154:155] neg_lo:[0,1] neg_hi:[0,1]
	v_lshlrev_b32_e32 v156, 16, v206
	v_and_b32_e32 v157, 0xffff0000, v206
	v_pk_add_f32 v[156:157], v[18:19], v[156:157] neg_lo:[0,1] neg_hi:[0,1]
	v_lshlrev_b32_e32 v158, 16, v207
	v_and_b32_e32 v159, 0xffff0000, v207
	v_pk_add_f32 v[158:159], v[20:21], v[158:159] neg_lo:[0,1] neg_hi:[0,1]
	v_cvt_pk_bf16_f32 v208, v152, v153
	v_cvt_pk_bf16_f32 v209, v154, v155
	v_cvt_pk_bf16_f32 v210, v156, v157
	v_cvt_pk_bf16_f32 v211, v158, v159
	v_pk_mul_f32 v[152:153], v[22:23], v[22:23]
	v_pk_mul_f32 v[154:155], v[24:25], v[24:25]
	v_pk_mul_f32 v[156:157], v[18:19], v[18:19]
	v_pk_mul_f32 v[158:159], v[20:21], v[20:21]
	v_pk_add_f32 v[152:153], v[152:153], v[154:155]
	v_pk_add_f32 v[156:157], v[156:157], v[158:159]
	v_pk_add_f32 v[152:153], v[152:153], v[156:157]
	v_add_f32_e32 v152, v152, v153
	v_add_f32_e32 v246, v246, v152
	v_lshlrev_b32_e32 v152, 16, v224
	v_and_b32_e32 v153, 0xffff0000, v224
	v_lshlrev_b32_e32 v154, 16, v228
	v_and_b32_e32 v155, 0xffff0000, v228
	v_pk_add_f32 v[152:153], v[152:153], v[154:155]
	v_pk_fma_f32 v[14:15], v[14:15], 0.5, v[152:153] op_sel_hi:[1,0,1]
	v_lshlrev_b32_e32 v156, 16, v225
	v_and_b32_e32 v157, 0xffff0000, v225
	v_lshlrev_b32_e32 v158, 16, v229
	v_and_b32_e32 v159, 0xffff0000, v229
	v_pk_add_f32 v[156:157], v[156:157], v[158:159]
	v_pk_fma_f32 v[16:17], v[16:17], 0.5, v[156:157] op_sel_hi:[1,0,1]
	v_lshlrev_b32_e32 v152, 16, v226
	v_and_b32_e32 v153, 0xffff0000, v226
	v_lshlrev_b32_e32 v154, 16, v230
	v_and_b32_e32 v155, 0xffff0000, v230
	v_pk_add_f32 v[152:153], v[152:153], v[154:155]
	v_pk_fma_f32 v[10:11], v[10:11], 0.5, v[152:153] op_sel_hi:[1,0,1]
	v_lshlrev_b32_e32 v156, 16, v227
	v_and_b32_e32 v157, 0xffff0000, v227
	v_lshlrev_b32_e32 v158, 16, v231
	v_and_b32_e32 v159, 0xffff0000, v231
	v_pk_add_f32 v[156:157], v[156:157], v[158:159]
	v_pk_fma_f32 v[12:13], v[12:13], 0.5, v[156:157] op_sel_hi:[1,0,1]
	v_cvt_pk_bf16_f32 v224, v14, v15
	v_cvt_pk_bf16_f32 v225, v16, v17
	v_cvt_pk_bf16_f32 v226, v10, v11
	v_cvt_pk_bf16_f32 v227, v12, v13
	v_lshlrev_b32_e32 v152, 16, v224
	v_and_b32_e32 v153, 0xffff0000, v224
	v_pk_add_f32 v[152:153], v[14:15], v[152:153] neg_lo:[0,1] neg_hi:[0,1]
	v_lshlrev_b32_e32 v154, 16, v225
	v_and_b32_e32 v155, 0xffff0000, v225
	v_pk_add_f32 v[154:155], v[16:17], v[154:155] neg_lo:[0,1] neg_hi:[0,1]
	v_lshlrev_b32_e32 v156, 16, v226
	v_and_b32_e32 v157, 0xffff0000, v226
	v_pk_add_f32 v[156:157], v[10:11], v[156:157] neg_lo:[0,1] neg_hi:[0,1]
	v_lshlrev_b32_e32 v158, 16, v227
	v_and_b32_e32 v159, 0xffff0000, v227
	v_pk_add_f32 v[158:159], v[12:13], v[158:159] neg_lo:[0,1] neg_hi:[0,1]
	v_cvt_pk_bf16_f32 v228, v152, v153
	v_cvt_pk_bf16_f32 v229, v154, v155
	v_cvt_pk_bf16_f32 v230, v156, v157
	v_cvt_pk_bf16_f32 v231, v158, v159
	v_pk_mul_f32 v[152:153], v[14:15], v[14:15]
; __device__ __forceinline__ unsigned cvt_pk_bf16(float lo, float hi) { unsigned r; asm volatile("v_cvt_pk_bf16_f32 %0, %1, %2" : "=v"(r) : "v"(lo), "v"(hi)); return r; }
;     __device__ __forceinline__ void operator()(AccRef acc, const Unit& u, int wr, int wc, int, int) const {
;     ...
;             for (int m = 0; m < 4; ++m) {
;                 const int row = row0 + ai * 128 + m * 16; float s = 0.f;
; #pragma unroll
;                 for (int bj = 0; bj < 2; ++bj) {
;                     const size_t p = (size_t)row * D + col0 + bj * 128;
;                     f32x4 x0, x1;
;                     if (xin32) { x0 = *(const f32x4*)(xin32 + p); x1 = *(const f32x4*)(xin32 + p + 4); }
;                     else { const v4u h = *(const v4u*)(xb + p), lo = *(const v4u*)(xl + p);
;                         x0 = (f32x4){bflo(h.x) + bflo(lo.x), bfhi(h.x) + bfhi(lo.x), bflo(h.y) + bflo(lo.y), bfhi(h.y) + bfhi(lo.y)};
;                         x1 = (f32x4){bflo(h.z) + bflo(lo.z), bfhi(h.z) + bfhi(lo.z), bflo(h.w) + bflo(lo.w), bfhi(h.w) + bfhi(lo.w)}; }
;                     x0 = x0 + alpha * acc[ai][bj][m][0]; x1 = x1 + alpha * acc[ai][bj][m][1];
;                     if (PROBE_ON) { x0 = x0 * pscale; x1 = x1 * pscale; if (p == 0) x0[0] += pspike; }
;                     if (xout32) { *(f32x4*)(xout32 + p) = x0; *(f32x4*)(xout32 + p + 4) = x1; }
;                     else {
;                         v4u w; w.x = cvt_pk_bf16(x0[0], x0[1]); w.y = cvt_pk_bf16(x0[2], x0[3]); w.z = cvt_pk_bf16(x1[0], x1[1]); w.w = cvt_pk_bf16(x1[2], x1[3]);
;                         *(v4u*)(xb + p) = w;
;                         const f32x4 r0 = {x0[0] - bflo(w.x), x0[1] - bfhi(w.x), x0[2] - bflo(w.y), x0[3] - bfhi(w.y)}, r1 = {x1[0] - bflo(w.z), x1[1] - bfhi(w.z), x1[2] - bflo(w.w), x1[3] - bfhi(w.w)};
;                         v4u q; q.x = cvt_pk_bf16(r0[0], r0[1]); q.y = cvt_pk_bf16(r0[2], r0[3]); q.z = cvt_pk_bf16(r1[0], r1[1]); q.w = cvt_pk_bf16(r1[2], r1[3]);
;                         *(v4u*)(xl + p) = q;
;                     }
;                     s += (x0[0] * x0[0] + x0[1] * x0[1]) + (x0[2] * x0[2] + x0[3] * x0[3]) + (x1[0] * x1[0] + x1[1] * x1[1]) + (x1[2] * x1[2] + x1[3] * x1[3]);
;                 }
;                 s += shx(s, 16, ln_); s += shx(s, 32, ln_);
;                 if (fq == 0) ss[(size_t)row * 32 + u.pn * 4 + wc] = s;
	v_pk_mul_f32 v[154:155], v[16:17], v[16:17]
	v_pk_mul_f32 v[156:157], v[10:11], v[10:11]
	v_pk_mul_f32 v[158:159], v[12:13], v[12:13]
	v_pk_add_f32 v[152:153], v[152:153], v[154:155]
	v_pk_add_f32 v[156:157], v[156:157], v[158:159]
	v_pk_add_f32 v[152:153], v[152:153], v[156:157]
	v_add_f32_e32 v247, v152, v153
	v_lshlrev_b32_e32 v152, 16, v232
	v_and_b32_e32 v153, 0xffff0000, v232
	v_lshlrev_b32_e32 v154, 16, v236
	v_and_b32_e32 v155, 0xffff0000, v236
	v_pk_add_f32 v[152:153], v[152:153], v[154:155]
	v_pk_fma_f32 v[4:5], v[4:5], 0.5, v[152:153] op_sel_hi:[1,0,1]
	v_lshlrev_b32_e32 v156, 16, v233
	v_and_b32_e32 v157, 0xffff0000, v233
	v_lshlrev_b32_e32 v158, 16, v237
	v_and_b32_e32 v159, 0xffff0000, v237
	v_pk_add_f32 v[156:157], v[156:157], v[158:159]
	v_pk_fma_f32 v[6:7], v[6:7], 0.5, v[156:157] op_sel_hi:[1,0,1]
	v_lshlrev_b32_e32 v152, 16, v234
	v_and_b32_e32 v153, 0xffff0000, v234
	v_lshlrev_b32_e32 v154, 16, v238
	v_and_b32_e32 v155, 0xffff0000, v238
	v_pk_add_f32 v[152:153], v[152:153], v[154:155]
	v_pk_fma_f32 v[0:1], v[0:1], 0.5, v[152:153] op_sel_hi:[1,0,1]
	v_lshlrev_b32_e32 v156, 16, v235
	v_and_b32_e32 v157, 0xffff0000, v235
	v_lshlrev_b32_e32 v158, 16, v239
	v_and_b32_e32 v159, 0xffff0000, v239
	v_pk_add_f32 v[156:157], v[156:157], v[158:159]
	v_pk_fma_f32 v[2:3], v[2:3], 0.5, v[156:157] op_sel_hi:[1,0,1]
	v_cvt_pk_bf16_f32 v232, v4, v5
	v_cvt_pk_bf16_f32 v233, v6, v7
	v_cvt_pk_bf16_f32 v234, v0, v1
	v_cvt_pk_bf16_f32 v235, v2, v3
	v_lshlrev_b32_e32 v152, 16, v232
	v_and_b32_e32 v153, 0xffff0000, v232
	v_pk_add_f32 v[152:153], v[4:5], v[152:153] neg_lo:[0,1] neg_hi:[0,1]
	v_lshlrev_b32_e32 v154, 16, v233
	v_and_b32_e32 v155, 0xffff0000, v233
	v_pk_add_f32 v[154:155], v[6:7], v[154:155] neg_lo:[0,1] neg_hi:[0,1]
	v_lshlrev_b32_e32 v156, 16, v234
	v_and_b32_e32 v157, 0xffff0000, v234
	v_pk_add_f32 v[156:157], v[0:1], v[156:157] neg_lo:[0,1] neg_hi:[0,1]
	v_lshlrev_b32_e32 v158, 16, v235
	v_and_b32_e32 v159, 0xffff0000, v235
	v_pk_add_f32 v[158:159], v[2:3], v[158:159] neg_lo:[0,1] neg_hi:[0,1]
	v_cvt_pk_bf16_f32 v236, v152, v153
	v_cvt_pk_bf16_f32 v237, v154, v155
	v_cvt_pk_bf16_f32 v238, v156, v157
	v_cvt_pk_bf16_f32 v239, v158, v159
	v_pk_mul_f32 v[152:153], v[4:5], v[4:5]
	v_pk_mul_f32 v[154:155], v[6:7], v[6:7]
	v_pk_mul_f32 v[156:157], v[0:1], v[0:1]
	v_pk_mul_f32 v[158:159], v[2:3], v[2:3]
	v_pk_add_f32 v[152:153], v[152:153], v[154:155]
	v_pk_add_f32 v[156:157], v[156:157], v[158:159]
	v_pk_add_f32 v[152:153], v[152:153], v[156:157]
	v_add_f32_e32 v152, v152, v153
	v_add_f32_e32 v247, v247, v152
	s_add_u32 s28, s12, 0xa0000
	s_addc_u32 s29, s13, 0
	s_add_u32 s98, s14, 0xa0000
	s_addc_u32 s99, s15, 0
	global_store_dwordx4 v248, v[196:199], s[28:29]
	global_store_dwordx4 v248, v[200:203], s[98:99]
	global_store_dwordx4 v248, v[204:207], s[28:29] offset:256
	global_store_dwordx4 v248, v[208:211], s[98:99] offset:256
	s_add_u32 s28, s12, 0xb0000
	s_addc_u32 s29, s13, 0
	s_add_u32 s98, s14, 0xb0000
	s_addc_u32 s99, s15, 0
	global_store_dwordx4 v248, v[224:227], s[28:29]
	global_store_dwordx4 v248, v[228:231], s[98:99]
	global_store_dwordx4 v248, v[232:235], s[28:29] offset:256
	global_store_dwordx4 v248, v[236:239], s[98:99] offset:256
	ds_bpermute_b32 v164, v162, v240
	ds_bpermute_b32 v165, v162, v241
	ds_bpermute_b32 v166, v162, v242
	ds_bpermute_b32 v167, v162, v243
	ds_bpermute_b32 v168, v162, v244
	ds_bpermute_b32 v169, v162, v245
	ds_bpermute_b32 v170, v162, v246
	ds_bpermute_b32 v171, v162, v247
	s_waitcnt lgkmcnt(0)
	v_add_f32_e32 v240, v240, v164
	v_add_f32_e32 v241, v241, v165
	v_add_f32_e32 v242, v242, v166
	v_add_f32_e32 v243, v243, v167
	v_add_f32_e32 v244, v244, v168
	v_add_f32_e32 v245, v245, v169
	v_add_f32_e32 v246, v246, v170
	v_add_f32_e32 v247, v247, v171
	ds_bpermute_b32 v164, v163, v240
	ds_bpermute_b32 v165, v163, v241
	ds_bpermute_b32 v166, v163, v242
	ds_bpermute_b32 v167, v163, v243
	ds_bpermute_b32 v168, v163, v244
	ds_bpermute_b32 v169, v163, v245
	ds_bpermute_b32 v170, v163, v246
	ds_bpermute_b32 v171, v163, v247
	s_waitcnt lgkmcnt(0)
	v_add_f32_e32 v240, v240, v164
	v_add_f32_e32 v241, v241, v165
	v_add_f32_e32 v242, v242, v166
	v_add_f32_e32 v243, v243, v167
	v_add_f32_e32 v244, v244, v168
	v_add_f32_e32 v245, v245, v169
	v_add_f32_e32 v246, v246, v170
	v_add_f32_e32 v247, v247, v171
	v_mbcnt_lo_u32_b32 v152, -1, 0
	v_mbcnt_hi_u32_b32 v152, -1, v152
	v_cmp_gt_u32_e32 vcc, 16, v152
	s_nop 4
	s_and_saveexec_b64 s[6:7], vcc
	global_store_dword v249, v240, s[16:17] offset:0
	global_store_dword v249, v241, s[16:17] offset:2048
	v_add_u32_e32 v166, 0x1000, v249
	global_store_dword v166, v242, s[16:17]
	v_add_u32_e32 v167, 0x1800, v249
	global_store_dword v167, v243, s[16:17]
	v_add_u32_e32 v168, 0x4000, v249
	global_store_dword v168, v244, s[16:17]
	v_add_u32_e32 v169, 0x4800, v249
	global_store_dword v169, v245, s[16:17]
	v_add_u32_e32 v170, 0x5000, v249
	global_store_dword v170, v246, s[16:17]
	v_add_u32_e32 v171, 0x5800, v249
	global_store_dword v171, v247, s[16:17]
	s_branch .LBB0_291

;     __device__ __forceinline__ void operator()(AccRef acc, const Unit& u, int wr, int wc, int, int) const {
;         const int ln_ = fresh_lane(), fr = ln_ & 15, fq = ln_ >> 4;
;         const int row0 = u.pm * 256 + wr * 64 + fr, col0 = u.pn * 256 + wc * 32 + 8 * fq;
; #pragma unroll
;         for (int ai = 0; ai < 2; ++ai)
; #pragma unroll
;             for (int m = 0; m < 4; ++m) {
;                 const int row = row0 + ai * 128 + m * 16; float s = 0.f;
; #pragma unroll
;                 for (int bj = 0; bj < 2; ++bj) {
;                     const size_t p = (size_t)row * D + col0 + bj * 128;
;                     f32x4 x0, x1;
;                     if (xin32) { x0 = *(const f32x4*)(xin32 + p); x1 = *(const f32x4*)(xin32 + p + 4); }
;                     else { const v4u h = *(const v4u*)(xb + p), lo = *(const v4u*)(xl + p);
;                         x0 = (f32x4){bflo(h.x) + bflo(lo.x), bfhi(h.x) + bfhi(lo.x), bflo(h.y) + bflo(lo.y), bfhi(h.y) + bfhi(lo.y)};
;                         x1 = (f32x4){bflo(h.z) + bflo(lo.z), bfhi(h.z) + bfhi(lo.z), bflo(h.w) + bflo(lo.w), bfhi(h.w) + bfhi(lo.w)}; }
;                     x0 = x0 + alpha * acc[ai][bj][m][0]; x1 = x1 + alpha * acc[ai][bj][m][1];
;                     if (PROBE_ON) { x0 = x0 * pscale; x1 = x1 * pscale; if (p == 0) x0[0] += pspike; }
;                     if (xout32) { *(f32x4*)(xout32 + p) = x0; *(f32x4*)(xout32 + p + 4) = x1; }
;                     else {
;                         v4u w; w.x = cvt_pk_bf16(x0[0], x0[1]); w.y = cvt_pk_bf16(x0[2], x0[3]); w.z = cvt_pk_bf16(x1[0], x1[1]); w.w = cvt_pk_bf16(x1[2], x1[3]);
;                         *(v4u*)(xb + p) = w;
;                         const f32x4 r0 = {x0[0] - bflo(w.x), x0[1] - bfhi(w.x), x0[2] - bflo(w.y), x0[3] - bfhi(w.y)}, r1 = {x1[0] - bflo(w.z), x1[1] - bfhi(w.z), x1[2] - bflo(w.w), x1[3] - bfhi(w.w)};
;                         v4u q; q.x = cvt_pk_bf16(r0[0], r0[1]); q.y = cvt_pk_bf16(r0[2], r0[3]); q.z = cvt_pk_bf16(r1[0], r1[1]); q.w = cvt_pk_bf16(r1[2], r1[3]);
;                         *(v4u*)(xl + p) = q;
;                     }
;                     s += (x0[0] * x0[0] + x0[1] * x0[1]) + (x0[2] * x0[2] + x0[3] * x0[3]) + (x1[0] * x1[0] + x1[1] * x1[1]) + (x1[2] * x1[2] + x1[3] * x1[3]);
.LBB0_1081:
	v_mbcnt_lo_u32_b32 v152, -1, 0
	v_mbcnt_hi_u32_b32 v152, -1, v152
	s_lshl_b32 s96, s24, 8
	s_add_i32 s96, s96, s47
	v_and_b32_e32 v153, 15, v152
	v_add_u32_e32 v153, s96, v153
	v_lshrrev_b32_e32 v154, 4, v152
	s_lshl_b32 s96, s22, 8
	s_or_b32 s96, s96, s48
	v_lshl_add_u32 v154, v154, 3, s96
	v_lshlrev_b32_e32 v248, 12, v153
	v_lshl_add_u32 v248, v154, 1, v248
	s_lshl_b32 s96, s22, 4
	s_lshl_b32 s22, s46, 2
	s_add_i32 s96, s96, s22
	v_lshl_add_u32 v249, v153, 7, s96
	v_lshlrev_b32_e32 v162, 2, v152
	v_xor_b32_e32 v163, 0x80, v162
	v_xor_b32_e32 v162, 64, v162
	s_mov_b64 s[22:23], s[6:7]
	s_mov_b64 s[98:99], s[8:9]
	global_load_dwordx4 v[164:167], v248, s[22:23]
	global_load_dwordx4 v[168:171], v248, s[98:99]
	global_load_dwordx4 v[172:175], v248, s[22:23] offset:256
	global_load_dwordx4 v[176:179], v248, s[98:99] offset:256
	s_add_u32 s22, s6, 0x10000
	s_addc_u32 s23, s7, 0
	s_add_u32 s98, s8, 0x10000
	s_addc_u32 s99, s9, 0
	global_load_dwordx4 v[180:183], v248, s[22:23]
	global_load_dwordx4 v[184:187], v248, s[98:99]
	global_load_dwordx4 v[188:191], v248, s[22:23] offset:256
	global_load_dwordx4 v[192:195], v248, s[98:99] offset:256
	s_add_u32 s22, s6, 0x20000
	s_addc_u32 s23, s7, 0
	s_add_u32 s98, s8, 0x20000
	s_addc_u32 s99, s9, 0
	global_load_dwordx4 v[196:199], v248, s[22:23]
	global_load_dwordx4 v[200:203], v248, s[98:99]
	global_load_dwordx4 v[204:207], v248, s[22:23] offset:256
	global_load_dwordx4 v[208:211], v248, s[98:99] offset:256
	s_add_u32 s22, s6, 0x30000
	s_addc_u32 s23, s7, 0
	s_add_u32 s98, s8, 0x30000
	s_addc_u32 s99, s9, 0
	global_load_dwordx4 v[224:227], v248, s[22:23]
	global_load_dwordx4 v[228:231], v248, s[98:99]
	global_load_dwordx4 v[232:235], v248, s[22:23] offset:256
	global_load_dwordx4 v[236:239], v248, s[98:99] offset:256
	s_waitcnt vmcnt(8)
	v_lshlrev_b32_e32 v152, 16, v164
	v_and_b32_e32 v153, 0xffff0000, v164
	v_lshlrev_b32_e32 v154, 16, v168
	v_and_b32_e32 v155, 0xffff0000, v168
	v_pk_add_f32 v[152:153], v[152:153], v[154:155]
	v_pk_add_f32 v[126:127], v[126:127], v[152:153]
	v_lshlrev_b32_e32 v156, 16, v165
	v_and_b32_e32 v157, 0xffff0000, v165
	v_lshlrev_b32_e32 v158, 16, v169
	v_and_b32_e32 v159, 0xffff0000, v169
	v_pk_add_f32 v[156:157], v[156:157], v[158:159]
	v_pk_add_f32 v[128:129], v[128:129], v[156:157]
	v_lshlrev_b32_e32 v152, 16, v166
	v_and_b32_e32 v153, 0xffff0000, v166
	v_lshlrev_b32_e32 v154, 16, v170
	v_and_b32_e32 v155, 0xffff0000, v170
	v_pk_add_f32 v[152:153], v[152:153], v[154:155]
	v_pk_add_f32 v[122:123], v[122:123], v[152:153]
	v_lshlrev_b32_e32 v156, 16, v167
	v_and_b32_e32 v157, 0xffff0000, v167
	v_lshlrev_b32_e32 v158, 16, v171
	v_and_b32_e32 v159, 0xffff0000, v171
	v_pk_add_f32 v[156:157], v[156:157], v[158:159]
	v_pk_add_f32 v[124:125], v[124:125], v[156:157]
	v_cvt_pk_bf16_f32 v164, v126, v127
	v_cvt_pk_bf16_f32 v165, v128, v129
	v_cvt_pk_bf16_f32 v166, v122, v123
	v_cvt_pk_bf16_f32 v167, v124, v125
	v_lshlrev_b32_e32 v152, 16, v164
	v_and_b32_e32 v153, 0xffff0000, v164
	v_pk_add_f32 v[152:153], v[126:127], v[152:153] neg_lo:[0,1] neg_hi:[0,1]
	v_lshlrev_b32_e32 v154, 16, v165
	v_and_b32_e32 v155, 0xffff0000, v165
	v_pk_add_f32 v[154:155], v[128:129], v[154:155] neg_lo:[0,1] neg_hi:[0,1]
	v_lshlrev_b32_e32 v156, 16, v166
	v_and_b32_e32 v157, 0xffff0000, v166
	v_pk_add_f32 v[156:157], v[122:123], v[156:157] neg_lo:[0,1] neg_hi:[0,1]
	v_lshlrev_b32_e32 v158, 16, v167
	v_and_b32_e32 v159, 0xffff0000, v167
	v_pk_add_f32 v[158:159], v[124:125], v[158:159] neg_lo:[0,1] neg_hi:[0,1]
	v_cvt_pk_bf16_f32 v168, v152, v153
	v_cvt_pk_bf16_f32 v169, v154, v155
	v_cvt_pk_bf16_f32 v170, v156, v157
	v_cvt_pk_bf16_f32 v171, v158, v159
	v_pk_mul_f32 v[152:153], v[126:127], v[126:127]
	v_pk_mul_f32 v[154:155], v[128:129], v[128:129]
	v_pk_mul_f32 v[156:157], v[122:123], v[122:123]
	v_pk_mul_f32 v[158:159], v[124:125], v[124:125]
	v_pk_add_f32 v[152:153], v[152:153], v[154:155]
	v_pk_add_f32 v[156:157], v[156:157], v[158:159]
	v_pk_add_f32 v[152:153], v[152:153], v[156:157]
	v_add_f32_e32 v240, v152, v153
	v_lshlrev_b32_e32 v152, 16, v172
	v_and_b32_e32 v153, 0xffff0000, v172
	v_lshlrev_b32_e32 v154, 16, v176
	v_and_b32_e32 v155, 0xffff0000, v176
	v_pk_add_f32 v[152:153], v[152:153], v[154:155]
	v_pk_add_f32 v[118:119], v[118:119], v[152:153]
	v_lshlrev_b32_e32 v156, 16, v173
	v_and_b32_e32 v157, 0xffff0000, v173
	v_lshlrev_b32_e32 v158, 16, v177
	v_and_b32_e32 v159, 0xffff0000, v177
	v_pk_add_f32 v[156:157], v[156:157], v[158:159]
	v_pk_add_f32 v[120:121], v[120:121], v[156:157]
	v_lshlrev_b32_e32 v152, 16, v174
	v_and_b32_e32 v153, 0xffff0000, v174
	v_lshlrev_b32_e32 v154, 16, v178
	v_and_b32_e32 v155, 0xffff0000, v178
	v_pk_add_f32 v[152:153], v[152:153], v[154:155]
	v_pk_add_f32 v[114:115], v[114:115], v[152:153]
	v_lshlrev_b32_e32 v156, 16, v175
	v_and_b32_e32 v157, 0xffff0000, v175
	v_lshlrev_b32_e32 v158, 16, v179
	v_and_b32_e32 v159, 0xffff0000, v179
	v_pk_add_f32 v[156:157], v[156:157], v[158:159]
	v_pk_add_f32 v[116:117], v[116:117], v[156:157]
	v_cvt_pk_bf16_f32 v172, v118, v119
	v_cvt_pk_bf16_f32 v173, v120, v121
	v_cvt_pk_bf16_f32 v174, v114, v115
	v_cvt_pk_bf16_f32 v175, v116, v117
	v_lshlrev_b32_e32 v152, 16, v172
	v_and_b32_e32 v153, 0xffff0000, v172
	v_pk_add_f32 v[152:153], v[118:119], v[152:153] neg_lo:[0,1] neg_hi:[0,1]
	v_lshlrev_b32_e32 v154, 16, v173
	v_and_b32_e32 v155, 0xffff0000, v173
	v_pk_add_f32 v[154:155], v[120:121], v[154:155] neg_lo:[0,1] neg_hi:[0,1]
	v_lshlrev_b32_e32 v156, 16, v174
	v_and_b32_e32 v157, 0xffff0000, v174
	v_pk_add_f32 v[156:157], v[114:115], v[156:157] neg_lo:[0,1] neg_hi:[0,1]
	v_lshlrev_b32_e32 v158, 16, v175
; __device__ __forceinline__ unsigned cvt_pk_bf16(float lo, float hi) { unsigned r; asm volatile("v_cvt_pk_bf16_f32 %0, %1, %2" : "=v"(r) : "v"(lo), "v"(hi)); return r; }
;     __device__ __forceinline__ void operator()(AccRef acc, const Unit& u, int wr, int wc, int, int) const {
;     ...
;             for (int m = 0; m < 4; ++m) {
;                 const int row = row0 + ai * 128 + m * 16; float s = 0.f;
; #pragma unroll
;                 for (int bj = 0; bj < 2; ++bj) {
;                     const size_t p = (size_t)row * D + col0 + bj * 128;
;                     f32x4 x0, x1;
;                     if (xin32) { x0 = *(const f32x4*)(xin32 + p); x1 = *(const f32x4*)(xin32 + p + 4); }
;                     else { const v4u h = *(const v4u*)(xb + p), lo = *(const v4u*)(xl + p);
;                         x0 = (f32x4){bflo(h.x) + bflo(lo.x), bfhi(h.x) + bfhi(lo.x), bflo(h.y) + bflo(lo.y), bfhi(h.y) + bfhi(lo.y)};
;                         x1 = (f32x4){bflo(h.z) + bflo(lo.z), bfhi(h.z) + bfhi(lo.z), bflo(h.w) + bflo(lo.w), bfhi(h.w) + bfhi(lo.w)}; }
;                     x0 = x0 + alpha * acc[ai][bj][m][0]; x1 = x1 + alpha * acc[ai][bj][m][1];
;                     if (PROBE_ON) { x0 = x0 * pscale; x1 = x1 * pscale; if (p == 0) x0[0] += pspike; }
;                     if (xout32) { *(f32x4*)(xout32 + p) = x0; *(f32x4*)(xout32 + p + 4) = x1; }
;                     else {
;                         v4u w; w.x = cvt_pk_bf16(x0[0], x0[1]); w.y = cvt_pk_bf16(x0[2], x0[3]); w.z = cvt_pk_bf16(x1[0], x1[1]); w.w = cvt_pk_bf16(x1[2], x1[3]);
;                         *(v4u*)(xb + p) = w;
;                         const f32x4 r0 = {x0[0] - bflo(w.x), x0[1] - bfhi(w.x), x0[2] - bflo(w.y), x0[3] - bfhi(w.y)}, r1 = {x1[0] - bflo(w.z), x1[1] - bfhi(w.z), x1[2] - bflo(w.w), x1[3] - bfhi(w.w)};
;                         v4u q; q.x = cvt_pk_bf16(r0[0], r0[1]); q.y = cvt_pk_bf16(r0[2], r0[3]); q.z = cvt_pk_bf16(r1[0], r1[1]); q.w = cvt_pk_bf16(r1[2], r1[3]);
;                         *(v4u*)(xl + p) = q;
;                     }
;                     s += (x0[0] * x0[0] + x0[1] * x0[1]) + (x0[2] * x0[2] + x0[3] * x0[3]) + (x1[0] * x1[0] + x1[1] * x1[1]) + (x1[2] * x1[2] + x1[3] * x1[3]);
	v_and_b32_e32 v159, 0xffff0000, v175
	v_pk_add_f32 v[158:159], v[116:117], v[158:159] neg_lo:[0,1] neg_hi:[0,1]
	v_cvt_pk_bf16_f32 v176, v152, v153
	v_cvt_pk_bf16_f32 v177, v154, v155
	v_cvt_pk_bf16_f32 v178, v156, v157
	v_cvt_pk_bf16_f32 v179, v158, v159
	v_pk_mul_f32 v[152:153], v[118:119], v[118:119]
	v_pk_mul_f32 v[154:155], v[120:121], v[120:121]
	v_pk_mul_f32 v[156:157], v[114:115], v[114:115]
	v_pk_mul_f32 v[158:159], v[116:117], v[116:117]
	v_pk_add_f32 v[152:153], v[152:153], v[154:155]
	v_pk_add_f32 v[156:157], v[156:157], v[158:159]
	v_pk_add_f32 v[152:153], v[152:153], v[156:157]
	v_add_f32_e32 v152, v152, v153
	v_add_f32_e32 v240, v240, v152
	v_lshlrev_b32_e32 v152, 16, v180
	v_and_b32_e32 v153, 0xffff0000, v180
	v_lshlrev_b32_e32 v154, 16, v184
	v_and_b32_e32 v155, 0xffff0000, v184
	v_pk_add_f32 v[152:153], v[152:153], v[154:155]
	v_pk_add_f32 v[110:111], v[110:111], v[152:153]
	v_lshlrev_b32_e32 v156, 16, v181
	v_and_b32_e32 v157, 0xffff0000, v181
	v_lshlrev_b32_e32 v158, 16, v185
	v_and_b32_e32 v159, 0xffff0000, v185
	v_pk_add_f32 v[156:157], v[156:157], v[158:159]
	v_pk_add_f32 v[112:113], v[112:113], v[156:157]
	v_lshlrev_b32_e32 v152, 16, v182
	v_and_b32_e32 v153, 0xffff0000, v182
	v_lshlrev_b32_e32 v154, 16, v186
	v_and_b32_e32 v155, 0xffff0000, v186
	v_pk_add_f32 v[152:153], v[152:153], v[154:155]
	v_pk_add_f32 v[106:107], v[106:107], v[152:153]
	v_lshlrev_b32_e32 v156, 16, v183
	v_and_b32_e32 v157, 0xffff0000, v183
	v_lshlrev_b32_e32 v158, 16, v187
	v_and_b32_e32 v159, 0xffff0000, v187
	v_pk_add_f32 v[156:157], v[156:157], v[158:159]
	v_pk_add_f32 v[108:109], v[108:109], v[156:157]
	v_cvt_pk_bf16_f32 v180, v110, v111
	v_cvt_pk_bf16_f32 v181, v112, v113
	v_cvt_pk_bf16_f32 v182, v106, v107
	v_cvt_pk_bf16_f32 v183, v108, v109
	v_lshlrev_b32_e32 v152, 16, v180
	v_and_b32_e32 v153, 0xffff0000, v180
	v_pk_add_f32 v[152:153], v[110:111], v[152:153] neg_lo:[0,1] neg_hi:[0,1]
	v_lshlrev_b32_e32 v154, 16, v181
	v_and_b32_e32 v155, 0xffff0000, v181
	v_pk_add_f32 v[154:155], v[112:113], v[154:155] neg_lo:[0,1] neg_hi:[0,1]
	v_lshlrev_b32_e32 v156, 16, v182
	v_and_b32_e32 v157, 0xffff0000, v182
	v_pk_add_f32 v[156:157], v[106:107], v[156:157] neg_lo:[0,1] neg_hi:[0,1]
	v_lshlrev_b32_e32 v158, 16, v183
	v_and_b32_e32 v159, 0xffff0000, v183
	v_pk_add_f32 v[158:159], v[108:109], v[158:159] neg_lo:[0,1] neg_hi:[0,1]
	v_cvt_pk_bf16_f32 v184, v152, v153
	v_cvt_pk_bf16_f32 v185, v154, v155
	v_cvt_pk_bf16_f32 v186, v156, v157
	v_cvt_pk_bf16_f32 v187, v158, v159
	v_pk_mul_f32 v[152:153], v[110:111], v[110:111]
	v_pk_mul_f32 v[154:155], v[112:113], v[112:113]
	v_pk_mul_f32 v[156:157], v[106:107], v[106:107]
	v_pk_mul_f32 v[158:159], v[108:109], v[108:109]
	v_pk_add_f32 v[152:153], v[152:153], v[154:155]
	v_pk_add_f32 v[156:157], v[156:157], v[158:159]
	v_pk_add_f32 v[152:153], v[152:153], v[156:157]
	v_add_f32_e32 v241, v152, v153
	v_lshlrev_b32_e32 v152, 16, v188
	v_and_b32_e32 v153, 0xffff0000, v188
	v_lshlrev_b32_e32 v154, 16, v192
	v_and_b32_e32 v155, 0xffff0000, v192
	v_pk_add_f32 v[152:153], v[152:153], v[154:155]
	v_pk_add_f32 v[102:103], v[102:103], v[152:153]
	v_lshlrev_b32_e32 v156, 16, v189
	v_and_b32_e32 v157, 0xffff0000, v189
	v_lshlrev_b32_e32 v158, 16, v193
	v_and_b32_e32 v159, 0xffff0000, v193
	v_pk_add_f32 v[156:157], v[156:157], v[158:159]
	v_pk_add_f32 v[104:105], v[104:105], v[156:157]
	v_lshlrev_b32_e32 v152, 16, v190
	v_and_b32_e32 v153, 0xffff0000, v190
	v_lshlrev_b32_e32 v154, 16, v194
	v_and_b32_e32 v155, 0xffff0000, v194
	v_pk_add_f32 v[152:153], v[152:153], v[154:155]
	v_pk_add_f32 v[98:99], v[98:99], v[152:153]
	v_lshlrev_b32_e32 v156, 16, v191
	v_and_b32_e32 v157, 0xffff0000, v191
	v_lshlrev_b32_e32 v158, 16, v195
	v_and_b32_e32 v159, 0xffff0000, v195
	v_pk_add_f32 v[156:157], v[156:157], v[158:159]
	v_pk_add_f32 v[100:101], v[100:101], v[156:157]
	v_cvt_pk_bf16_f32 v188, v102, v103
	v_cvt_pk_bf16_f32 v189, v104, v105
	v_cvt_pk_bf16_f32 v190, v98, v99
	v_cvt_pk_bf16_f32 v191, v100, v101
	v_lshlrev_b32_e32 v152, 16, v188
	v_and_b32_e32 v153, 0xffff0000, v188
	v_pk_add_f32 v[152:153], v[102:103], v[152:153] neg_lo:[0,1] neg_hi:[0,1]
	v_lshlrev_b32_e32 v154, 16, v189
	v_and_b32_e32 v155, 0xffff0000, v189
	v_pk_add_f32 v[154:155], v[104:105], v[154:155] neg_lo:[0,1] neg_hi:[0,1]
	v_lshlrev_b32_e32 v156, 16, v190
	v_and_b32_e32 v157, 0xffff0000, v190
	v_pk_add_f32 v[156:157], v[98:99], v[156:157] neg_lo:[0,1] neg_hi:[0,1]
	v_lshlrev_b32_e32 v158, 16, v191
	v_and_b32_e32 v159, 0xffff0000, v191
	v_pk_add_f32 v[158:159], v[100:101], v[158:159] neg_lo:[0,1] neg_hi:[0,1]
	v_cvt_pk_bf16_f32 v192, v152, v153
	v_cvt_pk_bf16_f32 v193, v154, v155
	v_cvt_pk_bf16_f32 v194, v156, v157
	v_cvt_pk_bf16_f32 v195, v158, v159
	v_pk_mul_f32 v[152:153], v[102:103], v[102:103]
	v_pk_mul_f32 v[154:155], v[104:105], v[104:105]
	v_pk_mul_f32 v[156:157], v[98:99], v[98:99]
	v_pk_mul_f32 v[158:159], v[100:101], v[100:101]
	v_pk_add_f32 v[152:153], v[152:153], v[154:155]
	v_pk_add_f32 v[156:157], v[156:157], v[158:159]
	v_pk_add_f32 v[152:153], v[152:153], v[156:157]
	v_add_f32_e32 v152, v152, v153
	v_add_f32_e32 v241, v241, v152
	s_mov_b64 s[22:23], s[6:7]
	s_mov_b64 s[98:99], s[8:9]
	global_store_dwordx4 v248, v[164:167], s[22:23]
	global_store_dwordx4 v248, v[168:171], s[98:99]
	global_store_dwordx4 v248, v[172:175], s[22:23] offset:256
	global_store_dwordx4 v248, v[176:179], s[98:99] offset:256
	s_add_u32 s22, s6, 0x10000
	s_addc_u32 s23, s7, 0
	s_add_u32 s98, s8, 0x10000
	s_addc_u32 s99, s9, 0
	global_store_dwordx4 v248, v[180:183], s[22:23]
	global_store_dwordx4 v248, v[184:187], s[98:99]
	global_store_dwordx4 v248, v[188:191], s[22:23] offset:256
	global_store_dwordx4 v248, v[192:195], s[98:99] offset:256
	s_add_u32 s22, s6, 0x80000
	s_addc_u32 s23, s7, 0
	s_add_u32 s98, s8, 0x80000
	s_addc_u32 s99, s9, 0
	global_load_dwordx4 v[164:167], v248, s[22:23]
	global_load_dwordx4 v[168:171], v248, s[98:99]
	global_load_dwordx4 v[172:175], v248, s[22:23] offset:256
	global_load_dwordx4 v[176:179], v248, s[98:99] offset:256
	s_add_u32 s22, s6, 0x90000
	s_addc_u32 s23, s7, 0
	s_add_u32 s98, s8, 0x90000
	s_addc_u32 s99, s9, 0
	global_load_dwordx4 v[180:183], v248, s[22:23]
	global_load_dwordx4 v[184:187], v248, s[98:99]
	global_load_dwordx4 v[188:191], v248, s[22:23] offset:256
	global_load_dwordx4 v[192:195], v248, s[98:99] offset:256
	s_waitcnt vmcnt(16)
; __device__ __forceinline__ unsigned cvt_pk_bf16(float lo, float hi) { unsigned r; asm volatile("v_cvt_pk_bf16_f32 %0, %1, %2" : "=v"(r) : "v"(lo), "v"(hi)); return r; }
;     __device__ __forceinline__ void operator()(AccRef acc, const Unit& u, int wr, int wc, int, int) const {
;     ...
;             for (int m = 0; m < 4; ++m) {
;                 const int row = row0 + ai * 128 + m * 16; float s = 0.f;
; #pragma unroll
;                 for (int bj = 0; bj < 2; ++bj) {
;                     const size_t p = (size_t)row * D + col0 + bj * 128;
;                     f32x4 x0, x1;
;                     if (xin32) { x0 = *(const f32x4*)(xin32 + p); x1 = *(const f32x4*)(xin32 + p + 4); }
;                     else { const v4u h = *(const v4u*)(xb + p), lo = *(const v4u*)(xl + p);
;                         x0 = (f32x4){bflo(h.x) + bflo(lo.x), bfhi(h.x) + bfhi(lo.x), bflo(h.y) + bflo(lo.y), bfhi(h.y) + bfhi(lo.y)};
;                         x1 = (f32x4){bflo(h.z) + bflo(lo.z), bfhi(h.z) + bfhi(lo.z), bflo(h.w) + bflo(lo.w), bfhi(h.w) + bfhi(lo.w)}; }
;                     x0 = x0 + alpha * acc[ai][bj][m][0]; x1 = x1 + alpha * acc[ai][bj][m][1];
;                     if (PROBE_ON) { x0 = x0 * pscale; x1 = x1 * pscale; if (p == 0) x0[0] += pspike; }
;                     if (xout32) { *(f32x4*)(xout32 + p) = x0; *(f32x4*)(xout32 + p + 4) = x1; }
;                     else {
;                         v4u w; w.x = cvt_pk_bf16(x0[0], x0[1]); w.y = cvt_pk_bf16(x0[2], x0[3]); w.z = cvt_pk_bf16(x1[0], x1[1]); w.w = cvt_pk_bf16(x1[2], x1[3]);
;                         *(v4u*)(xb + p) = w;
;                         const f32x4 r0 = {x0[0] - bflo(w.x), x0[1] - bfhi(w.x), x0[2] - bflo(w.y), x0[3] - bfhi(w.y)}, r1 = {x1[0] - bflo(w.z), x1[1] - bfhi(w.z), x1[2] - bflo(w.w), x1[3] - bfhi(w.w)};
;                         v4u q; q.x = cvt_pk_bf16(r0[0], r0[1]); q.y = cvt_pk_bf16(r0[2], r0[3]); q.z = cvt_pk_bf16(r1[0], r1[1]); q.w = cvt_pk_bf16(r1[2], r1[3]);
;                         *(v4u*)(xl + p) = q;
;                     }
;                     s += (x0[0] * x0[0] + x0[1] * x0[1]) + (x0[2] * x0[2] + x0[3] * x0[3]) + (x1[0] * x1[0] + x1[1] * x1[1]) + (x1[2] * x1[2] + x1[3] * x1[3]);
	v_lshlrev_b32_e32 v152, 16, v196
	v_and_b32_e32 v153, 0xffff0000, v196
	v_lshlrev_b32_e32 v154, 16, v200
	v_and_b32_e32 v155, 0xffff0000, v200
	v_pk_add_f32 v[152:153], v[152:153], v[154:155]
	v_pk_add_f32 v[94:95], v[94:95], v[152:153]
	v_lshlrev_b32_e32 v156, 16, v197
	v_and_b32_e32 v157, 0xffff0000, v197
	v_lshlrev_b32_e32 v158, 16, v201
	v_and_b32_e32 v159, 0xffff0000, v201
	v_pk_add_f32 v[156:157], v[156:157], v[158:159]
	v_pk_add_f32 v[96:97], v[96:97], v[156:157]
	v_lshlrev_b32_e32 v152, 16, v198
	v_and_b32_e32 v153, 0xffff0000, v198
	v_lshlrev_b32_e32 v154, 16, v202
	v_and_b32_e32 v155, 0xffff0000, v202
	v_pk_add_f32 v[152:153], v[152:153], v[154:155]
	v_pk_add_f32 v[90:91], v[90:91], v[152:153]
	v_lshlrev_b32_e32 v156, 16, v199
	v_and_b32_e32 v157, 0xffff0000, v199
	v_lshlrev_b32_e32 v158, 16, v203
	v_and_b32_e32 v159, 0xffff0000, v203
	v_pk_add_f32 v[156:157], v[156:157], v[158:159]
	v_pk_add_f32 v[92:93], v[92:93], v[156:157]
	v_cvt_pk_bf16_f32 v196, v94, v95
	v_cvt_pk_bf16_f32 v197, v96, v97
	v_cvt_pk_bf16_f32 v198, v90, v91
	v_cvt_pk_bf16_f32 v199, v92, v93
	v_lshlrev_b32_e32 v152, 16, v196
	v_and_b32_e32 v153, 0xffff0000, v196
	v_pk_add_f32 v[152:153], v[94:95], v[152:153] neg_lo:[0,1] neg_hi:[0,1]
	v_lshlrev_b32_e32 v154, 16, v197
	v_and_b32_e32 v155, 0xffff0000, v197
	v_pk_add_f32 v[154:155], v[96:97], v[154:155] neg_lo:[0,1] neg_hi:[0,1]
	v_lshlrev_b32_e32 v156, 16, v198
	v_and_b32_e32 v157, 0xffff0000, v198
	v_pk_add_f32 v[156:157], v[90:91], v[156:157] neg_lo:[0,1] neg_hi:[0,1]
	v_lshlrev_b32_e32 v158, 16, v199
	v_and_b32_e32 v159, 0xffff0000, v199
	v_pk_add_f32 v[158:159], v[92:93], v[158:159] neg_lo:[0,1] neg_hi:[0,1]
	v_cvt_pk_bf16_f32 v200, v152, v153
	v_cvt_pk_bf16_f32 v201, v154, v155
	v_cvt_pk_bf16_f32 v202, v156, v157
	v_cvt_pk_bf16_f32 v203, v158, v159
	v_pk_mul_f32 v[152:153], v[94:95], v[94:95]
	v_pk_mul_f32 v[154:155], v[96:97], v[96:97]
	v_pk_mul_f32 v[156:157], v[90:91], v[90:91]
	v_pk_mul_f32 v[158:159], v[92:93], v[92:93]
	v_pk_add_f32 v[152:153], v[152:153], v[154:155]
	v_pk_add_f32 v[156:157], v[156:157], v[158:159]
	v_pk_add_f32 v[152:153], v[152:153], v[156:157]
	v_add_f32_e32 v242, v152, v153
	v_lshlrev_b32_e32 v152, 16, v204
	v_and_b32_e32 v153, 0xffff0000, v204
	v_lshlrev_b32_e32 v154, 16, v208
	v_and_b32_e32 v155, 0xffff0000, v208
	v_pk_add_f32 v[152:153], v[152:153], v[154:155]
	v_pk_add_f32 v[86:87], v[86:87], v[152:153]
	v_lshlrev_b32_e32 v156, 16, v205
	v_and_b32_e32 v157, 0xffff0000, v205
	v_lshlrev_b32_e32 v158, 16, v209
	v_and_b32_e32 v159, 0xffff0000, v209
	v_pk_add_f32 v[156:157], v[156:157], v[158:159]
	v_pk_add_f32 v[88:89], v[88:89], v[156:157]
	v_lshlrev_b32_e32 v152, 16, v206
	v_and_b32_e32 v153, 0xffff0000, v206
	v_lshlrev_b32_e32 v154, 16, v210
	v_and_b32_e32 v155, 0xffff0000, v210
	v_pk_add_f32 v[152:153], v[152:153], v[154:155]
	v_pk_add_f32 v[82:83], v[82:83], v[152:153]
	v_lshlrev_b32_e32 v156, 16, v207
	v_and_b32_e32 v157, 0xffff0000, v207
	v_lshlrev_b32_e32 v158, 16, v211
	v_and_b32_e32 v159, 0xffff0000, v211
	v_pk_add_f32 v[156:157], v[156:157], v[158:159]
	v_pk_add_f32 v[84:85], v[84:85], v[156:157]
	v_cvt_pk_bf16_f32 v204, v86, v87
	v_cvt_pk_bf16_f32 v205, v88, v89
	v_cvt_pk_bf16_f32 v206, v82, v83
	v_cvt_pk_bf16_f32 v207, v84, v85
	v_lshlrev_b32_e32 v152, 16, v204
	v_and_b32_e32 v153, 0xffff0000, v204
	v_pk_add_f32 v[152:153], v[86:87], v[152:153] neg_lo:[0,1] neg_hi:[0,1]
	v_lshlrev_b32_e32 v154, 16, v205
	v_and_b32_e32 v155, 0xffff0000, v205
	v_pk_add_f32 v[154:155], v[88:89], v[154:155] neg_lo:[0,1] neg_hi:[0,1]
	v_lshlrev_b32_e32 v156, 16, v206
	v_and_b32_e32 v157, 0xffff0000, v206
	v_pk_add_f32 v[156:157], v[82:83], v[156:157] neg_lo:[0,1] neg_hi:[0,1]
	v_lshlrev_b32_e32 v158, 16, v207
	v_and_b32_e32 v159, 0xffff0000, v207
	v_pk_add_f32 v[158:159], v[84:85], v[158:159] neg_lo:[0,1] neg_hi:[0,1]
	v_cvt_pk_bf16_f32 v208, v152, v153
	v_cvt_pk_bf16_f32 v209, v154, v155
	v_cvt_pk_bf16_f32 v210, v156, v157
	v_cvt_pk_bf16_f32 v211, v158, v159
	v_pk_mul_f32 v[152:153], v[86:87], v[86:87]
	v_pk_mul_f32 v[154:155], v[88:89], v[88:89]
	v_pk_mul_f32 v[156:157], v[82:83], v[82:83]
	v_pk_mul_f32 v[158:159], v[84:85], v[84:85]
	v_pk_add_f32 v[152:153], v[152:153], v[154:155]
	v_pk_add_f32 v[156:157], v[156:157], v[158:159]
	v_pk_add_f32 v[152:153], v[152:153], v[156:157]
	v_add_f32_e32 v152, v152, v153
	v_add_f32_e32 v242, v242, v152
	v_lshlrev_b32_e32 v152, 16, v224
	v_and_b32_e32 v153, 0xffff0000, v224
	v_lshlrev_b32_e32 v154, 16, v228
	v_and_b32_e32 v155, 0xffff0000, v228
	v_pk_add_f32 v[152:153], v[152:153], v[154:155]
	v_pk_add_f32 v[78:79], v[78:79], v[152:153]
	v_lshlrev_b32_e32 v156, 16, v225
	v_and_b32_e32 v157, 0xffff0000, v225
	v_lshlrev_b32_e32 v158, 16, v229
	v_and_b32_e32 v159, 0xffff0000, v229
	v_pk_add_f32 v[156:157], v[156:157], v[158:159]
	v_pk_add_f32 v[80:81], v[80:81], v[156:157]
	v_lshlrev_b32_e32 v152, 16, v226
	v_and_b32_e32 v153, 0xffff0000, v226
	v_lshlrev_b32_e32 v154, 16, v230
	v_and_b32_e32 v155, 0xffff0000, v230
	v_pk_add_f32 v[152:153], v[152:153], v[154:155]
	v_pk_add_f32 v[74:75], v[74:75], v[152:153]
	v_lshlrev_b32_e32 v156, 16, v227
	v_and_b32_e32 v157, 0xffff0000, v227
	v_lshlrev_b32_e32 v158, 16, v231
	v_and_b32_e32 v159, 0xffff0000, v231
	v_pk_add_f32 v[156:157], v[156:157], v[158:159]
	v_pk_add_f32 v[76:77], v[76:77], v[156:157]
	v_cvt_pk_bf16_f32 v224, v78, v79
	v_cvt_pk_bf16_f32 v225, v80, v81
	v_cvt_pk_bf16_f32 v226, v74, v75
	v_cvt_pk_bf16_f32 v227, v76, v77
	v_lshlrev_b32_e32 v152, 16, v224
	v_and_b32_e32 v153, 0xffff0000, v224
	v_pk_add_f32 v[152:153], v[78:79], v[152:153] neg_lo:[0,1] neg_hi:[0,1]
	v_lshlrev_b32_e32 v154, 16, v225
; __device__ __forceinline__ unsigned cvt_pk_bf16(float lo, float hi) { unsigned r; asm volatile("v_cvt_pk_bf16_f32 %0, %1, %2" : "=v"(r) : "v"(lo), "v"(hi)); return r; }
;     __device__ __forceinline__ void operator()(AccRef acc, const Unit& u, int wr, int wc, int, int) const {
;     ...
;             for (int m = 0; m < 4; ++m) {
;                 const int row = row0 + ai * 128 + m * 16; float s = 0.f;
; #pragma unroll
;                 for (int bj = 0; bj < 2; ++bj) {
;                     const size_t p = (size_t)row * D + col0 + bj * 128;
;                     f32x4 x0, x1;
;                     if (xin32) { x0 = *(const f32x4*)(xin32 + p); x1 = *(const f32x4*)(xin32 + p + 4); }
;                     else { const v4u h = *(const v4u*)(xb + p), lo = *(const v4u*)(xl + p);
;                         x0 = (f32x4){bflo(h.x) + bflo(lo.x), bfhi(h.x) + bfhi(lo.x), bflo(h.y) + bflo(lo.y), bfhi(h.y) + bfhi(lo.y)};
;                         x1 = (f32x4){bflo(h.z) + bflo(lo.z), bfhi(h.z) + bfhi(lo.z), bflo(h.w) + bflo(lo.w), bfhi(h.w) + bfhi(lo.w)}; }
;                     x0 = x0 + alpha * acc[ai][bj][m][0]; x1 = x1 + alpha * acc[ai][bj][m][1];
;                     if (PROBE_ON) { x0 = x0 * pscale; x1 = x1 * pscale; if (p == 0) x0[0] += pspike; }
;                     if (xout32) { *(f32x4*)(xout32 + p) = x0; *(f32x4*)(xout32 + p + 4) = x1; }
;                     else {
;                         v4u w; w.x = cvt_pk_bf16(x0[0], x0[1]); w.y = cvt_pk_bf16(x0[2], x0[3]); w.z = cvt_pk_bf16(x1[0], x1[1]); w.w = cvt_pk_bf16(x1[2], x1[3]);
;                         *(v4u*)(xb + p) = w;
;                         const f32x4 r0 = {x0[0] - bflo(w.x), x0[1] - bfhi(w.x), x0[2] - bflo(w.y), x0[3] - bfhi(w.y)}, r1 = {x1[0] - bflo(w.z), x1[1] - bfhi(w.z), x1[2] - bflo(w.w), x1[3] - bfhi(w.w)};
;                         v4u q; q.x = cvt_pk_bf16(r0[0], r0[1]); q.y = cvt_pk_bf16(r0[2], r0[3]); q.z = cvt_pk_bf16(r1[0], r1[1]); q.w = cvt_pk_bf16(r1[2], r1[3]);
;                         *(v4u*)(xl + p) = q;
;                     }
;                     s += (x0[0] * x0[0] + x0[1] * x0[1]) + (x0[2] * x0[2] + x0[3] * x0[3]) + (x1[0] * x1[0] + x1[1] * x1[1]) + (x1[2] * x1[2] + x1[3] * x1[3]);
	v_and_b32_e32 v155, 0xffff0000, v225
	v_pk_add_f32 v[154:155], v[80:81], v[154:155] neg_lo:[0,1] neg_hi:[0,1]
	v_lshlrev_b32_e32 v156, 16, v226
	v_and_b32_e32 v157, 0xffff0000, v226
	v_pk_add_f32 v[156:157], v[74:75], v[156:157] neg_lo:[0,1] neg_hi:[0,1]
	v_lshlrev_b32_e32 v158, 16, v227
	v_and_b32_e32 v159, 0xffff0000, v227
	v_pk_add_f32 v[158:159], v[76:77], v[158:159] neg_lo:[0,1] neg_hi:[0,1]
	v_cvt_pk_bf16_f32 v228, v152, v153
	v_cvt_pk_bf16_f32 v229, v154, v155
	v_cvt_pk_bf16_f32 v230, v156, v157
	v_cvt_pk_bf16_f32 v231, v158, v159
	v_pk_mul_f32 v[152:153], v[78:79], v[78:79]
	v_pk_mul_f32 v[154:155], v[80:81], v[80:81]
	v_pk_mul_f32 v[156:157], v[74:75], v[74:75]
	v_pk_mul_f32 v[158:159], v[76:77], v[76:77]
	v_pk_add_f32 v[152:153], v[152:153], v[154:155]
	v_pk_add_f32 v[156:157], v[156:157], v[158:159]
	v_pk_add_f32 v[152:153], v[152:153], v[156:157]
	v_add_f32_e32 v243, v152, v153
	v_lshlrev_b32_e32 v152, 16, v232
	v_and_b32_e32 v153, 0xffff0000, v232
	v_lshlrev_b32_e32 v154, 16, v236
	v_and_b32_e32 v155, 0xffff0000, v236
	v_pk_add_f32 v[152:153], v[152:153], v[154:155]
	v_pk_add_f32 v[70:71], v[70:71], v[152:153]
	v_lshlrev_b32_e32 v156, 16, v233
	v_and_b32_e32 v157, 0xffff0000, v233
	v_lshlrev_b32_e32 v158, 16, v237
	v_and_b32_e32 v159, 0xffff0000, v237
	v_pk_add_f32 v[156:157], v[156:157], v[158:159]
	v_pk_add_f32 v[72:73], v[72:73], v[156:157]
	v_lshlrev_b32_e32 v152, 16, v234
	v_and_b32_e32 v153, 0xffff0000, v234
	v_lshlrev_b32_e32 v154, 16, v238
	v_and_b32_e32 v155, 0xffff0000, v238
	v_pk_add_f32 v[152:153], v[152:153], v[154:155]
	v_pk_add_f32 v[66:67], v[66:67], v[152:153]
	v_lshlrev_b32_e32 v156, 16, v235
	v_and_b32_e32 v157, 0xffff0000, v235
	v_lshlrev_b32_e32 v158, 16, v239
	v_and_b32_e32 v159, 0xffff0000, v239
	v_pk_add_f32 v[156:157], v[156:157], v[158:159]
	v_pk_add_f32 v[68:69], v[68:69], v[156:157]
	v_cvt_pk_bf16_f32 v232, v70, v71
	v_cvt_pk_bf16_f32 v233, v72, v73
	v_cvt_pk_bf16_f32 v234, v66, v67
	v_cvt_pk_bf16_f32 v235, v68, v69
	v_lshlrev_b32_e32 v152, 16, v232
	v_and_b32_e32 v153, 0xffff0000, v232
	v_pk_add_f32 v[152:153], v[70:71], v[152:153] neg_lo:[0,1] neg_hi:[0,1]
	v_lshlrev_b32_e32 v154, 16, v233
	v_and_b32_e32 v155, 0xffff0000, v233
	v_pk_add_f32 v[154:155], v[72:73], v[154:155] neg_lo:[0,1] neg_hi:[0,1]
	v_lshlrev_b32_e32 v156, 16, v234
	v_and_b32_e32 v157, 0xffff0000, v234
	v_pk_add_f32 v[156:157], v[66:67], v[156:157] neg_lo:[0,1] neg_hi:[0,1]
	v_lshlrev_b32_e32 v158, 16, v235
	v_and_b32_e32 v159, 0xffff0000, v235
	v_pk_add_f32 v[158:159], v[68:69], v[158:159] neg_lo:[0,1] neg_hi:[0,1]
	v_cvt_pk_bf16_f32 v236, v152, v153
	v_cvt_pk_bf16_f32 v237, v154, v155
	v_cvt_pk_bf16_f32 v238, v156, v157
	v_cvt_pk_bf16_f32 v239, v158, v159
	v_pk_mul_f32 v[152:153], v[70:71], v[70:71]
	v_pk_mul_f32 v[154:155], v[72:73], v[72:73]
	v_pk_mul_f32 v[156:157], v[66:67], v[66:67]
	v_pk_mul_f32 v[158:159], v[68:69], v[68:69]
	v_pk_add_f32 v[152:153], v[152:153], v[154:155]
	v_pk_add_f32 v[156:157], v[156:157], v[158:159]
	v_pk_add_f32 v[152:153], v[152:153], v[156:157]
	v_add_f32_e32 v152, v152, v153
	v_add_f32_e32 v243, v243, v152
	s_add_u32 s22, s6, 0x20000
	s_addc_u32 s23, s7, 0
	s_add_u32 s98, s8, 0x20000
	s_addc_u32 s99, s9, 0
	global_store_dwordx4 v248, v[196:199], s[22:23]
	global_store_dwordx4 v248, v[200:203], s[98:99]
	global_store_dwordx4 v248, v[204:207], s[22:23] offset:256
	global_store_dwordx4 v248, v[208:211], s[98:99] offset:256
	s_add_u32 s22, s6, 0x30000
	s_addc_u32 s23, s7, 0
	s_add_u32 s98, s8, 0x30000
	s_addc_u32 s99, s9, 0
	global_store_dwordx4 v248, v[224:227], s[22:23]
	global_store_dwordx4 v248, v[228:231], s[98:99]
	global_store_dwordx4 v248, v[232:235], s[22:23] offset:256
	global_store_dwordx4 v248, v[236:239], s[98:99] offset:256
	s_add_u32 s22, s6, 0xa0000
	s_addc_u32 s23, s7, 0
	s_add_u32 s98, s8, 0xa0000
	s_addc_u32 s99, s9, 0
	global_load_dwordx4 v[196:199], v248, s[22:23]
	global_load_dwordx4 v[200:203], v248, s[98:99]
	global_load_dwordx4 v[204:207], v248, s[22:23] offset:256
	global_load_dwordx4 v[208:211], v248, s[98:99] offset:256
	s_add_u32 s22, s6, 0xb0000
	s_addc_u32 s23, s7, 0
	s_add_u32 s98, s8, 0xb0000
	s_addc_u32 s99, s9, 0
	global_load_dwordx4 v[224:227], v248, s[22:23]
	global_load_dwordx4 v[228:231], v248, s[98:99]
	global_load_dwordx4 v[232:235], v248, s[22:23] offset:256
	global_load_dwordx4 v[236:239], v248, s[98:99] offset:256
	s_waitcnt vmcnt(16)
; __device__ __forceinline__ unsigned cvt_pk_bf16(float lo, float hi) { unsigned r; asm volatile("v_cvt_pk_bf16_f32 %0, %1, %2" : "=v"(r) : "v"(lo), "v"(hi)); return r; }
;     __device__ __forceinline__ void operator()(AccRef acc, const Unit& u, int wr, int wc, int, int) const {
;     ...
;             for (int m = 0; m < 4; ++m) {
;                 const int row = row0 + ai * 128 + m * 16; float s = 0.f;
; #pragma unroll
;                 for (int bj = 0; bj < 2; ++bj) {
;                     const size_t p = (size_t)row * D + col0 + bj * 128;
;                     f32x4 x0, x1;
;                     if (xin32) { x0 = *(const f32x4*)(xin32 + p); x1 = *(const f32x4*)(xin32 + p + 4); }
;                     else { const v4u h = *(const v4u*)(xb + p), lo = *(const v4u*)(xl + p);
;                         x0 = (f32x4){bflo(h.x) + bflo(lo.x), bfhi(h.x) + bfhi(lo.x), bflo(h.y) + bflo(lo.y), bfhi(h.y) + bfhi(lo.y)};
;                         x1 = (f32x4){bflo(h.z) + bflo(lo.z), bfhi(h.z) + bfhi(lo.z), bflo(h.w) + bflo(lo.w), bfhi(h.w) + bfhi(lo.w)}; }
;                     x0 = x0 + alpha * acc[ai][bj][m][0]; x1 = x1 + alpha * acc[ai][bj][m][1];
;                     if (PROBE_ON) { x0 = x0 * pscale; x1 = x1 * pscale; if (p == 0) x0[0] += pspike; }
;                     if (xout32) { *(f32x4*)(xout32 + p) = x0; *(f32x4*)(xout32 + p + 4) = x1; }
;                     else {
;                         v4u w; w.x = cvt_pk_bf16(x0[0], x0[1]); w.y = cvt_pk_bf16(x0[2], x0[3]); w.z = cvt_pk_bf16(x1[0], x1[1]); w.w = cvt_pk_bf16(x1[2], x1[3]);
;                         *(v4u*)(xb + p) = w;
;                         const f32x4 r0 = {x0[0] - bflo(w.x), x0[1] - bfhi(w.x), x0[2] - bflo(w.y), x0[3] - bfhi(w.y)}, r1 = {x1[0] - bflo(w.z), x1[1] - bfhi(w.z), x1[2] - bflo(w.w), x1[3] - bfhi(w.w)};
;                         v4u q; q.x = cvt_pk_bf16(r0[0], r0[1]); q.y = cvt_pk_bf16(r0[2], r0[3]); q.z = cvt_pk_bf16(r1[0], r1[1]); q.w = cvt_pk_bf16(r1[2], r1[3]);
;                         *(v4u*)(xl + p) = q;
;                     }
;                     s += (x0[0] * x0[0] + x0[1] * x0[1]) + (x0[2] * x0[2] + x0[3] * x0[3]) + (x1[0] * x1[0] + x1[1] * x1[1]) + (x1[2] * x1[2] + x1[3] * x1[3]);
	v_lshlrev_b32_e32 v152, 16, v164
	v_and_b32_e32 v153, 0xffff0000, v164
	v_lshlrev_b32_e32 v154, 16, v168
	v_and_b32_e32 v155, 0xffff0000, v168
	v_pk_add_f32 v[152:153], v[152:153], v[154:155]
	v_pk_add_f32 v[62:63], v[62:63], v[152:153]
	v_lshlrev_b32_e32 v156, 16, v165
	v_and_b32_e32 v157, 0xffff0000, v165
	v_lshlrev_b32_e32 v158, 16, v169
	v_and_b32_e32 v159, 0xffff0000, v169
	v_pk_add_f32 v[156:157], v[156:157], v[158:159]
	v_pk_add_f32 v[64:65], v[64:65], v[156:157]
	v_lshlrev_b32_e32 v152, 16, v166
	v_and_b32_e32 v153, 0xffff0000, v166
	v_lshlrev_b32_e32 v154, 16, v170
	v_and_b32_e32 v155, 0xffff0000, v170
	v_pk_add_f32 v[152:153], v[152:153], v[154:155]
	v_pk_add_f32 v[58:59], v[58:59], v[152:153]
	v_lshlrev_b32_e32 v156, 16, v167
	v_and_b32_e32 v157, 0xffff0000, v167
	v_lshlrev_b32_e32 v158, 16, v171
	v_and_b32_e32 v159, 0xffff0000, v171
	v_pk_add_f32 v[156:157], v[156:157], v[158:159]
	v_pk_add_f32 v[60:61], v[60:61], v[156:157]
	v_cvt_pk_bf16_f32 v164, v62, v63
	v_cvt_pk_bf16_f32 v165, v64, v65
	v_cvt_pk_bf16_f32 v166, v58, v59
	v_cvt_pk_bf16_f32 v167, v60, v61
	v_lshlrev_b32_e32 v152, 16, v164
	v_and_b32_e32 v153, 0xffff0000, v164
	v_pk_add_f32 v[152:153], v[62:63], v[152:153] neg_lo:[0,1] neg_hi:[0,1]
	v_lshlrev_b32_e32 v154, 16, v165
	v_and_b32_e32 v155, 0xffff0000, v165
	v_pk_add_f32 v[154:155], v[64:65], v[154:155] neg_lo:[0,1] neg_hi:[0,1]
	v_lshlrev_b32_e32 v156, 16, v166
	v_and_b32_e32 v157, 0xffff0000, v166
	v_pk_add_f32 v[156:157], v[58:59], v[156:157] neg_lo:[0,1] neg_hi:[0,1]
	v_lshlrev_b32_e32 v158, 16, v167
	v_and_b32_e32 v159, 0xffff0000, v167
	v_pk_add_f32 v[158:159], v[60:61], v[158:159] neg_lo:[0,1] neg_hi:[0,1]
	v_cvt_pk_bf16_f32 v168, v152, v153
	v_cvt_pk_bf16_f32 v169, v154, v155
	v_cvt_pk_bf16_f32 v170, v156, v157
	v_cvt_pk_bf16_f32 v171, v158, v159
	v_pk_mul_f32 v[152:153], v[62:63], v[62:63]
	v_pk_mul_f32 v[154:155], v[64:65], v[64:65]
	v_pk_mul_f32 v[156:157], v[58:59], v[58:59]
	v_pk_mul_f32 v[158:159], v[60:61], v[60:61]
	v_pk_add_f32 v[152:153], v[152:153], v[154:155]
	v_pk_add_f32 v[156:157], v[156:157], v[158:159]
	v_pk_add_f32 v[152:153], v[152:153], v[156:157]
	v_add_f32_e32 v244, v152, v153
	v_lshlrev_b32_e32 v152, 16, v172
	v_and_b32_e32 v153, 0xffff0000, v172
	v_lshlrev_b32_e32 v154, 16, v176
	v_and_b32_e32 v155, 0xffff0000, v176
	v_pk_add_f32 v[152:153], v[152:153], v[154:155]
	v_pk_add_f32 v[54:55], v[54:55], v[152:153]
	v_lshlrev_b32_e32 v156, 16, v173
	v_and_b32_e32 v157, 0xffff0000, v173
	v_lshlrev_b32_e32 v158, 16, v177
	v_and_b32_e32 v159, 0xffff0000, v177
	v_pk_add_f32 v[156:157], v[156:157], v[158:159]
	v_pk_add_f32 v[56:57], v[56:57], v[156:157]
	v_lshlrev_b32_e32 v152, 16, v174
	v_and_b32_e32 v153, 0xffff0000, v174
	v_lshlrev_b32_e32 v154, 16, v178
	v_and_b32_e32 v155, 0xffff0000, v178
	v_pk_add_f32 v[152:153], v[152:153], v[154:155]
	v_pk_add_f32 v[50:51], v[50:51], v[152:153]
	v_lshlrev_b32_e32 v156, 16, v175
	v_and_b32_e32 v157, 0xffff0000, v175
	v_lshlrev_b32_e32 v158, 16, v179
	v_and_b32_e32 v159, 0xffff0000, v179
	v_pk_add_f32 v[156:157], v[156:157], v[158:159]
	v_pk_add_f32 v[52:53], v[52:53], v[156:157]
	v_cvt_pk_bf16_f32 v172, v54, v55
	v_cvt_pk_bf16_f32 v173, v56, v57
	v_cvt_pk_bf16_f32 v174, v50, v51
	v_cvt_pk_bf16_f32 v175, v52, v53
	v_lshlrev_b32_e32 v152, 16, v172
	v_and_b32_e32 v153, 0xffff0000, v172
	v_pk_add_f32 v[152:153], v[54:55], v[152:153] neg_lo:[0,1] neg_hi:[0,1]
	v_lshlrev_b32_e32 v154, 16, v173
	v_and_b32_e32 v155, 0xffff0000, v173
	v_pk_add_f32 v[154:155], v[56:57], v[154:155] neg_lo:[0,1] neg_hi:[0,1]
	v_lshlrev_b32_e32 v156, 16, v174
	v_and_b32_e32 v157, 0xffff0000, v174
	v_pk_add_f32 v[156:157], v[50:51], v[156:157] neg_lo:[0,1] neg_hi:[0,1]
	v_lshlrev_b32_e32 v158, 16, v175
	v_and_b32_e32 v159, 0xffff0000, v175
	v_pk_add_f32 v[158:159], v[52:53], v[158:159] neg_lo:[0,1] neg_hi:[0,1]
	v_cvt_pk_bf16_f32 v176, v152, v153
	v_cvt_pk_bf16_f32 v177, v154, v155
	v_cvt_pk_bf16_f32 v178, v156, v157
	v_cvt_pk_bf16_f32 v179, v158, v159
	v_pk_mul_f32 v[152:153], v[54:55], v[54:55]
	v_pk_mul_f32 v[154:155], v[56:57], v[56:57]
	v_pk_mul_f32 v[156:157], v[50:51], v[50:51]
	v_pk_mul_f32 v[158:159], v[52:53], v[52:53]
	v_pk_add_f32 v[152:153], v[152:153], v[154:155]
	v_pk_add_f32 v[156:157], v[156:157], v[158:159]
	v_pk_add_f32 v[152:153], v[152:153], v[156:157]
	v_add_f32_e32 v152, v152, v153
	v_add_f32_e32 v244, v244, v152
	v_lshlrev_b32_e32 v152, 16, v180
	v_and_b32_e32 v153, 0xffff0000, v180
	v_lshlrev_b32_e32 v154, 16, v184
	v_and_b32_e32 v155, 0xffff0000, v184
	v_pk_add_f32 v[152:153], v[152:153], v[154:155]
	v_pk_add_f32 v[46:47], v[46:47], v[152:153]
	v_lshlrev_b32_e32 v156, 16, v181
	v_and_b32_e32 v157, 0xffff0000, v181
	v_lshlrev_b32_e32 v158, 16, v185
	v_and_b32_e32 v159, 0xffff0000, v185
	v_pk_add_f32 v[156:157], v[156:157], v[158:159]
	v_pk_add_f32 v[48:49], v[48:49], v[156:157]
	v_lshlrev_b32_e32 v152, 16, v182
	v_and_b32_e32 v153, 0xffff0000, v182
	v_lshlrev_b32_e32 v154, 16, v186
	v_and_b32_e32 v155, 0xffff0000, v186
	v_pk_add_f32 v[152:153], v[152:153], v[154:155]
	v_pk_add_f32 v[42:43], v[42:43], v[152:153]
	v_lshlrev_b32_e32 v156, 16, v183
	v_and_b32_e32 v157, 0xffff0000, v183
	v_lshlrev_b32_e32 v158, 16, v187
	v_and_b32_e32 v159, 0xffff0000, v187
	v_pk_add_f32 v[156:157], v[156:157], v[158:159]
	v_pk_add_f32 v[44:45], v[44:45], v[156:157]
	v_cvt_pk_bf16_f32 v180, v46, v47
	v_cvt_pk_bf16_f32 v181, v48, v49
	v_cvt_pk_bf16_f32 v182, v42, v43
	v_cvt_pk_bf16_f32 v183, v44, v45
	v_lshlrev_b32_e32 v152, 16, v180
	v_and_b32_e32 v153, 0xffff0000, v180
	v_pk_add_f32 v[152:153], v[46:47], v[152:153] neg_lo:[0,1] neg_hi:[0,1]
	v_lshlrev_b32_e32 v154, 16, v181
; __device__ __forceinline__ unsigned cvt_pk_bf16(float lo, float hi) { unsigned r; asm volatile("v_cvt_pk_bf16_f32 %0, %1, %2" : "=v"(r) : "v"(lo), "v"(hi)); return r; }
;     __device__ __forceinline__ void operator()(AccRef acc, const Unit& u, int wr, int wc, int, int) const {
;     ...
;             for (int m = 0; m < 4; ++m) {
;                 const int row = row0 + ai * 128 + m * 16; float s = 0.f;
; #pragma unroll
;                 for (int bj = 0; bj < 2; ++bj) {
;                     const size_t p = (size_t)row * D + col0 + bj * 128;
;                     f32x4 x0, x1;
;                     if (xin32) { x0 = *(const f32x4*)(xin32 + p); x1 = *(const f32x4*)(xin32 + p + 4); }
;                     else { const v4u h = *(const v4u*)(xb + p), lo = *(const v4u*)(xl + p);
;                         x0 = (f32x4){bflo(h.x) + bflo(lo.x), bfhi(h.x) + bfhi(lo.x), bflo(h.y) + bflo(lo.y), bfhi(h.y) + bfhi(lo.y)};
;                         x1 = (f32x4){bflo(h.z) + bflo(lo.z), bfhi(h.z) + bfhi(lo.z), bflo(h.w) + bflo(lo.w), bfhi(h.w) + bfhi(lo.w)}; }
;                     x0 = x0 + alpha * acc[ai][bj][m][0]; x1 = x1 + alpha * acc[ai][bj][m][1];
;                     if (PROBE_ON) { x0 = x0 * pscale; x1 = x1 * pscale; if (p == 0) x0[0] += pspike; }
;                     if (xout32) { *(f32x4*)(xout32 + p) = x0; *(f32x4*)(xout32 + p + 4) = x1; }
;                     else {
;                         v4u w; w.x = cvt_pk_bf16(x0[0], x0[1]); w.y = cvt_pk_bf16(x0[2], x0[3]); w.z = cvt_pk_bf16(x1[0], x1[1]); w.w = cvt_pk_bf16(x1[2], x1[3]);
;                         *(v4u*)(xb + p) = w;
;                         const f32x4 r0 = {x0[0] - bflo(w.x), x0[1] - bfhi(w.x), x0[2] - bflo(w.y), x0[3] - bfhi(w.y)}, r1 = {x1[0] - bflo(w.z), x1[1] - bfhi(w.z), x1[2] - bflo(w.w), x1[3] - bfhi(w.w)};
;                         v4u q; q.x = cvt_pk_bf16(r0[0], r0[1]); q.y = cvt_pk_bf16(r0[2], r0[3]); q.z = cvt_pk_bf16(r1[0], r1[1]); q.w = cvt_pk_bf16(r1[2], r1[3]);
;                         *(v4u*)(xl + p) = q;
;                     }
;                     s += (x0[0] * x0[0] + x0[1] * x0[1]) + (x0[2] * x0[2] + x0[3] * x0[3]) + (x1[0] * x1[0] + x1[1] * x1[1]) + (x1[2] * x1[2] + x1[3] * x1[3]);
	v_and_b32_e32 v155, 0xffff0000, v181
	v_pk_add_f32 v[154:155], v[48:49], v[154:155] neg_lo:[0,1] neg_hi:[0,1]
	v_lshlrev_b32_e32 v156, 16, v182
	v_and_b32_e32 v157, 0xffff0000, v182
	v_pk_add_f32 v[156:157], v[42:43], v[156:157] neg_lo:[0,1] neg_hi:[0,1]
	v_lshlrev_b32_e32 v158, 16, v183
	v_and_b32_e32 v159, 0xffff0000, v183
	v_pk_add_f32 v[158:159], v[44:45], v[158:159] neg_lo:[0,1] neg_hi:[0,1]
	v_cvt_pk_bf16_f32 v184, v152, v153
	v_cvt_pk_bf16_f32 v185, v154, v155
	v_cvt_pk_bf16_f32 v186, v156, v157
	v_cvt_pk_bf16_f32 v187, v158, v159
	v_pk_mul_f32 v[152:153], v[46:47], v[46:47]
	v_pk_mul_f32 v[154:155], v[48:49], v[48:49]
	v_pk_mul_f32 v[156:157], v[42:43], v[42:43]
	v_pk_mul_f32 v[158:159], v[44:45], v[44:45]
	v_pk_add_f32 v[152:153], v[152:153], v[154:155]
	v_pk_add_f32 v[156:157], v[156:157], v[158:159]
	v_pk_add_f32 v[152:153], v[152:153], v[156:157]
	v_add_f32_e32 v245, v152, v153
	v_lshlrev_b32_e32 v152, 16, v188
	v_and_b32_e32 v153, 0xffff0000, v188
	v_lshlrev_b32_e32 v154, 16, v192
	v_and_b32_e32 v155, 0xffff0000, v192
	v_pk_add_f32 v[152:153], v[152:153], v[154:155]
	v_pk_add_f32 v[38:39], v[38:39], v[152:153]
	v_lshlrev_b32_e32 v156, 16, v189
	v_and_b32_e32 v157, 0xffff0000, v189
	v_lshlrev_b32_e32 v158, 16, v193
	v_and_b32_e32 v159, 0xffff0000, v193
	v_pk_add_f32 v[156:157], v[156:157], v[158:159]
	v_pk_add_f32 v[40:41], v[40:41], v[156:157]
	v_lshlrev_b32_e32 v152, 16, v190
	v_and_b32_e32 v153, 0xffff0000, v190
	v_lshlrev_b32_e32 v154, 16, v194
	v_and_b32_e32 v155, 0xffff0000, v194
	v_pk_add_f32 v[152:153], v[152:153], v[154:155]
	v_pk_add_f32 v[34:35], v[34:35], v[152:153]
	v_lshlrev_b32_e32 v156, 16, v191
	v_and_b32_e32 v157, 0xffff0000, v191
	v_lshlrev_b32_e32 v158, 16, v195
	v_and_b32_e32 v159, 0xffff0000, v195
	v_pk_add_f32 v[156:157], v[156:157], v[158:159]
	v_pk_add_f32 v[36:37], v[36:37], v[156:157]
	v_cvt_pk_bf16_f32 v188, v38, v39
	v_cvt_pk_bf16_f32 v189, v40, v41
	v_cvt_pk_bf16_f32 v190, v34, v35
	v_cvt_pk_bf16_f32 v191, v36, v37
	v_lshlrev_b32_e32 v152, 16, v188
	v_and_b32_e32 v153, 0xffff0000, v188
	v_pk_add_f32 v[152:153], v[38:39], v[152:153] neg_lo:[0,1] neg_hi:[0,1]
	v_lshlrev_b32_e32 v154, 16, v189
	v_and_b32_e32 v155, 0xffff0000, v189
	v_pk_add_f32 v[154:155], v[40:41], v[154:155] neg_lo:[0,1] neg_hi:[0,1]
	v_lshlrev_b32_e32 v156, 16, v190
	v_and_b32_e32 v157, 0xffff0000, v190
	v_pk_add_f32 v[156:157], v[34:35], v[156:157] neg_lo:[0,1] neg_hi:[0,1]
	v_lshlrev_b32_e32 v158, 16, v191
	v_and_b32_e32 v159, 0xffff0000, v191
	v_pk_add_f32 v[158:159], v[36:37], v[158:159] neg_lo:[0,1] neg_hi:[0,1]
	v_cvt_pk_bf16_f32 v192, v152, v153
	v_cvt_pk_bf16_f32 v193, v154, v155
	v_cvt_pk_bf16_f32 v194, v156, v157
	v_cvt_pk_bf16_f32 v195, v158, v159
	v_pk_mul_f32 v[152:153], v[38:39], v[38:39]
	v_pk_mul_f32 v[154:155], v[40:41], v[40:41]
	v_pk_mul_f32 v[156:157], v[34:35], v[34:35]
	v_pk_mul_f32 v[158:159], v[36:37], v[36:37]
	v_pk_add_f32 v[152:153], v[152:153], v[154:155]
	v_pk_add_f32 v[156:157], v[156:157], v[158:159]
	v_pk_add_f32 v[152:153], v[152:153], v[156:157]
	v_add_f32_e32 v152, v152, v153
	v_add_f32_e32 v245, v245, v152
	s_add_u32 s22, s6, 0x80000
	s_addc_u32 s23, s7, 0
	s_add_u32 s98, s8, 0x80000
	s_addc_u32 s99, s9, 0
	global_store_dwordx4 v248, v[164:167], s[22:23]
	global_store_dwordx4 v248, v[168:171], s[98:99]
	global_store_dwordx4 v248, v[172:175], s[22:23] offset:256
	global_store_dwordx4 v248, v[176:179], s[98:99] offset:256
	s_add_u32 s22, s6, 0x90000
	s_addc_u32 s23, s7, 0
	s_add_u32 s98, s8, 0x90000
	s_addc_u32 s99, s9, 0
	global_store_dwordx4 v248, v[180:183], s[22:23]
	global_store_dwordx4 v248, v[184:187], s[98:99]
	global_store_dwordx4 v248, v[188:191], s[22:23] offset:256
	global_store_dwordx4 v248, v[192:195], s[98:99] offset:256
	s_waitcnt vmcnt(8)
	v_lshlrev_b32_e32 v152, 16, v196
	v_and_b32_e32 v153, 0xffff0000, v196
	v_lshlrev_b32_e32 v154, 16, v200
	v_and_b32_e32 v155, 0xffff0000, v200
	v_pk_add_f32 v[152:153], v[152:153], v[154:155]
	v_pk_add_f32 v[30:31], v[30:31], v[152:153]
	v_lshlrev_b32_e32 v156, 16, v197
	v_and_b32_e32 v157, 0xffff0000, v197
	v_lshlrev_b32_e32 v158, 16, v201
	v_and_b32_e32 v159, 0xffff0000, v201
	v_pk_add_f32 v[156:157], v[156:157], v[158:159]
	v_pk_add_f32 v[32:33], v[32:33], v[156:157]
	v_lshlrev_b32_e32 v152, 16, v198
	v_and_b32_e32 v153, 0xffff0000, v198
	v_lshlrev_b32_e32 v154, 16, v202
	v_and_b32_e32 v155, 0xffff0000, v202
	v_pk_add_f32 v[152:153], v[152:153], v[154:155]
	v_pk_add_f32 v[26:27], v[26:27], v[152:153]
	v_lshlrev_b32_e32 v156, 16, v199
	v_and_b32_e32 v157, 0xffff0000, v199
	v_lshlrev_b32_e32 v158, 16, v203
	v_and_b32_e32 v159, 0xffff0000, v203
	v_pk_add_f32 v[156:157], v[156:157], v[158:159]
	v_pk_add_f32 v[28:29], v[28:29], v[156:157]
	v_cvt_pk_bf16_f32 v196, v30, v31
	v_cvt_pk_bf16_f32 v197, v32, v33
	v_cvt_pk_bf16_f32 v198, v26, v27
	v_cvt_pk_bf16_f32 v199, v28, v29
	v_lshlrev_b32_e32 v152, 16, v196
	v_and_b32_e32 v153, 0xffff0000, v196
	v_pk_add_f32 v[152:153], v[30:31], v[152:153] neg_lo:[0,1] neg_hi:[0,1]
	v_lshlrev_b32_e32 v154, 16, v197
	v_and_b32_e32 v155, 0xffff0000, v197
	v_pk_add_f32 v[154:155], v[32:33], v[154:155] neg_lo:[0,1] neg_hi:[0,1]
	v_lshlrev_b32_e32 v156, 16, v198
	v_and_b32_e32 v157, 0xffff0000, v198
	v_pk_add_f32 v[156:157], v[26:27], v[156:157] neg_lo:[0,1] neg_hi:[0,1]
	v_lshlrev_b32_e32 v158, 16, v199
	v_and_b32_e32 v159, 0xffff0000, v199
	v_pk_add_f32 v[158:159], v[28:29], v[158:159] neg_lo:[0,1] neg_hi:[0,1]
	v_cvt_pk_bf16_f32 v200, v152, v153
	v_cvt_pk_bf16_f32 v201, v154, v155
	v_cvt_pk_bf16_f32 v202, v156, v157
	v_cvt_pk_bf16_f32 v203, v158, v159
	v_pk_mul_f32 v[152:153], v[30:31], v[30:31]
; __device__ __forceinline__ unsigned cvt_pk_bf16(float lo, float hi) { unsigned r; asm volatile("v_cvt_pk_bf16_f32 %0, %1, %2" : "=v"(r) : "v"(lo), "v"(hi)); return r; }
;     __device__ __forceinline__ void operator()(AccRef acc, const Unit& u, int wr, int wc, int, int) const {
;     ...
;             for (int m = 0; m < 4; ++m) {
;                 const int row = row0 + ai * 128 + m * 16; float s = 0.f;
; #pragma unroll
;                 for (int bj = 0; bj < 2; ++bj) {
;                     const size_t p = (size_t)row * D + col0 + bj * 128;
;                     f32x4 x0, x1;
;                     if (xin32) { x0 = *(const f32x4*)(xin32 + p); x1 = *(const f32x4*)(xin32 + p + 4); }
;                     else { const v4u h = *(const v4u*)(xb + p), lo = *(const v4u*)(xl + p);
;                         x0 = (f32x4){bflo(h.x) + bflo(lo.x), bfhi(h.x) + bfhi(lo.x), bflo(h.y) + bflo(lo.y), bfhi(h.y) + bfhi(lo.y)};
;                         x1 = (f32x4){bflo(h.z) + bflo(lo.z), bfhi(h.z) + bfhi(lo.z), bflo(h.w) + bflo(lo.w), bfhi(h.w) + bfhi(lo.w)}; }
;                     x0 = x0 + alpha * acc[ai][bj][m][0]; x1 = x1 + alpha * acc[ai][bj][m][1];
;                     if (PROBE_ON) { x0 = x0 * pscale; x1 = x1 * pscale; if (p == 0) x0[0] += pspike; }
;                     if (xout32) { *(f32x4*)(xout32 + p) = x0; *(f32x4*)(xout32 + p + 4) = x1; }
;                     else {
;                         v4u w; w.x = cvt_pk_bf16(x0[0], x0[1]); w.y = cvt_pk_bf16(x0[2], x0[3]); w.z = cvt_pk_bf16(x1[0], x1[1]); w.w = cvt_pk_bf16(x1[2], x1[3]);
;                         *(v4u*)(xb + p) = w;
;                         const f32x4 r0 = {x0[0] - bflo(w.x), x0[1] - bfhi(w.x), x0[2] - bflo(w.y), x0[3] - bfhi(w.y)}, r1 = {x1[0] - bflo(w.z), x1[1] - bfhi(w.z), x1[2] - bflo(w.w), x1[3] - bfhi(w.w)};
;                         v4u q; q.x = cvt_pk_bf16(r0[0], r0[1]); q.y = cvt_pk_bf16(r0[2], r0[3]); q.z = cvt_pk_bf16(r1[0], r1[1]); q.w = cvt_pk_bf16(r1[2], r1[3]);
;                         *(v4u*)(xl + p) = q;
;                     }
;                     s += (x0[0] * x0[0] + x0[1] * x0[1]) + (x0[2] * x0[2] + x0[3] * x0[3]) + (x1[0] * x1[0] + x1[1] * x1[1]) + (x1[2] * x1[2] + x1[3] * x1[3]);
	v_pk_mul_f32 v[154:155], v[32:33], v[32:33]
	v_pk_mul_f32 v[156:157], v[26:27], v[26:27]
	v_pk_mul_f32 v[158:159], v[28:29], v[28:29]
	v_pk_add_f32 v[152:153], v[152:153], v[154:155]
	v_pk_add_f32 v[156:157], v[156:157], v[158:159]
	v_pk_add_f32 v[152:153], v[152:153], v[156:157]
	v_add_f32_e32 v246, v152, v153
	v_lshlrev_b32_e32 v152, 16, v204
	v_and_b32_e32 v153, 0xffff0000, v204
	v_lshlrev_b32_e32 v154, 16, v208
	v_and_b32_e32 v155, 0xffff0000, v208
	v_pk_add_f32 v[152:153], v[152:153], v[154:155]
	v_pk_add_f32 v[22:23], v[22:23], v[152:153]
	v_lshlrev_b32_e32 v156, 16, v205
	v_and_b32_e32 v157, 0xffff0000, v205
	v_lshlrev_b32_e32 v158, 16, v209
	v_and_b32_e32 v159, 0xffff0000, v209
	v_pk_add_f32 v[156:157], v[156:157], v[158:159]
	v_pk_add_f32 v[24:25], v[24:25], v[156:157]
	v_lshlrev_b32_e32 v152, 16, v206
	v_and_b32_e32 v153, 0xffff0000, v206
	v_lshlrev_b32_e32 v154, 16, v210
	v_and_b32_e32 v155, 0xffff0000, v210
	v_pk_add_f32 v[152:153], v[152:153], v[154:155]
	v_pk_add_f32 v[18:19], v[18:19], v[152:153]
	v_lshlrev_b32_e32 v156, 16, v207
	v_and_b32_e32 v157, 0xffff0000, v207
	v_lshlrev_b32_e32 v158, 16, v211
	v_and_b32_e32 v159, 0xffff0000, v211
	v_pk_add_f32 v[156:157], v[156:157], v[158:159]
	v_pk_add_f32 v[20:21], v[20:21], v[156:157]
	v_cvt_pk_bf16_f32 v204, v22, v23
	v_cvt_pk_bf16_f32 v205, v24, v25
	v_cvt_pk_bf16_f32 v206, v18, v19
	v_cvt_pk_bf16_f32 v207, v20, v21
	v_lshlrev_b32_e32 v152, 16, v204
	v_and_b32_e32 v153, 0xffff0000, v204
	v_pk_add_f32 v[152:153], v[22:23], v[152:153] neg_lo:[0,1] neg_hi:[0,1]
	v_lshlrev_b32_e32 v154, 16, v205
	v_and_b32_e32 v155, 0xffff0000, v205
	v_pk_add_f32 v[154:155], v[24:25], v[154:155] neg_lo:[0,1] neg_hi:[0,1]
	v_lshlrev_b32_e32 v156, 16, v206
	v_and_b32_e32 v157, 0xffff0000, v206
	v_pk_add_f32 v[156:157], v[18:19], v[156:157] neg_lo:[0,1] neg_hi:[0,1]
	v_lshlrev_b32_e32 v158, 16, v207
	v_and_b32_e32 v159, 0xffff0000, v207
	v_pk_add_f32 v[158:159], v[20:21], v[158:159] neg_lo:[0,1] neg_hi:[0,1]
	v_cvt_pk_bf16_f32 v208, v152, v153
	v_cvt_pk_bf16_f32 v209, v154, v155
	v_cvt_pk_bf16_f32 v210, v156, v157
	v_cvt_pk_bf16_f32 v211, v158, v159
	v_pk_mul_f32 v[152:153], v[22:23], v[22:23]
	v_pk_mul_f32 v[154:155], v[24:25], v[24:25]
	v_pk_mul_f32 v[156:157], v[18:19], v[18:19]
	v_pk_mul_f32 v[158:159], v[20:21], v[20:21]
	v_pk_add_f32 v[152:153], v[152:153], v[154:155]
	v_pk_add_f32 v[156:157], v[156:157], v[158:159]
	v_pk_add_f32 v[152:153], v[152:153], v[156:157]
	v_add_f32_e32 v152, v152, v153
	v_add_f32_e32 v246, v246, v152
	v_lshlrev_b32_e32 v152, 16, v224
	v_and_b32_e32 v153, 0xffff0000, v224
	v_lshlrev_b32_e32 v154, 16, v228
	v_and_b32_e32 v155, 0xffff0000, v228
	v_pk_add_f32 v[152:153], v[152:153], v[154:155]
	v_pk_add_f32 v[14:15], v[14:15], v[152:153]
	v_lshlrev_b32_e32 v156, 16, v225
	v_and_b32_e32 v157, 0xffff0000, v225
	v_lshlrev_b32_e32 v158, 16, v229
	v_and_b32_e32 v159, 0xffff0000, v229
	v_pk_add_f32 v[156:157], v[156:157], v[158:159]
	v_pk_add_f32 v[16:17], v[16:17], v[156:157]
	v_lshlrev_b32_e32 v152, 16, v226
	v_and_b32_e32 v153, 0xffff0000, v226
	v_lshlrev_b32_e32 v154, 16, v230
	v_and_b32_e32 v155, 0xffff0000, v230
	v_pk_add_f32 v[152:153], v[152:153], v[154:155]
	v_pk_add_f32 v[10:11], v[10:11], v[152:153]
	v_lshlrev_b32_e32 v156, 16, v227
	v_and_b32_e32 v157, 0xffff0000, v227
	v_lshlrev_b32_e32 v158, 16, v231
	v_and_b32_e32 v159, 0xffff0000, v231
	v_pk_add_f32 v[156:157], v[156:157], v[158:159]
	v_pk_add_f32 v[12:13], v[12:13], v[156:157]
	v_cvt_pk_bf16_f32 v224, v14, v15
	v_cvt_pk_bf16_f32 v225, v16, v17
	v_cvt_pk_bf16_f32 v226, v10, v11
	v_cvt_pk_bf16_f32 v227, v12, v13
	v_lshlrev_b32_e32 v152, 16, v224
	v_and_b32_e32 v153, 0xffff0000, v224
	v_pk_add_f32 v[152:153], v[14:15], v[152:153] neg_lo:[0,1] neg_hi:[0,1]
	v_lshlrev_b32_e32 v154, 16, v225
	v_and_b32_e32 v155, 0xffff0000, v225
	v_pk_add_f32 v[154:155], v[16:17], v[154:155] neg_lo:[0,1] neg_hi:[0,1]
	v_lshlrev_b32_e32 v156, 16, v226
	v_and_b32_e32 v157, 0xffff0000, v226
	v_pk_add_f32 v[156:157], v[10:11], v[156:157] neg_lo:[0,1] neg_hi:[0,1]
	v_lshlrev_b32_e32 v158, 16, v227
	v_and_b32_e32 v159, 0xffff0000, v227
	v_pk_add_f32 v[158:159], v[12:13], v[158:159] neg_lo:[0,1] neg_hi:[0,1]
	v_cvt_pk_bf16_f32 v228, v152, v153
	v_cvt_pk_bf16_f32 v229, v154, v155
	v_cvt_pk_bf16_f32 v230, v156, v157
	v_cvt_pk_bf16_f32 v231, v158, v159
	v_pk_mul_f32 v[152:153], v[14:15], v[14:15]
	v_pk_mul_f32 v[154:155], v[16:17], v[16:17]
	v_pk_mul_f32 v[156:157], v[10:11], v[10:11]
	v_pk_mul_f32 v[158:159], v[12:13], v[12:13]
	v_pk_add_f32 v[152:153], v[152:153], v[154:155]
	v_pk_add_f32 v[156:157], v[156:157], v[158:159]
	v_pk_add_f32 v[152:153], v[152:153], v[156:157]
; __device__ __forceinline__ unsigned cvt_pk_bf16(float lo, float hi) { unsigned r; asm volatile("v_cvt_pk_bf16_f32 %0, %1, %2" : "=v"(r) : "v"(lo), "v"(hi)); return r; }
;     __device__ __forceinline__ void operator()(AccRef acc, const Unit& u, int wr, int wc, int, int) const {
;     ...
;             for (int m = 0; m < 4; ++m) {
;                 const int row = row0 + ai * 128 + m * 16; float s = 0.f;
; #pragma unroll
;                 for (int bj = 0; bj < 2; ++bj) {
;                     const size_t p = (size_t)row * D + col0 + bj * 128;
;                     f32x4 x0, x1;
;                     if (xin32) { x0 = *(const f32x4*)(xin32 + p); x1 = *(const f32x4*)(xin32 + p + 4); }
;                     else { const v4u h = *(const v4u*)(xb + p), lo = *(const v4u*)(xl + p);
;                         x0 = (f32x4){bflo(h.x) + bflo(lo.x), bfhi(h.x) + bfhi(lo.x), bflo(h.y) + bflo(lo.y), bfhi(h.y) + bfhi(lo.y)};
;                         x1 = (f32x4){bflo(h.z) + bflo(lo.z), bfhi(h.z) + bfhi(lo.z), bflo(h.w) + bflo(lo.w), bfhi(h.w) + bfhi(lo.w)}; }
;                     x0 = x0 + alpha * acc[ai][bj][m][0]; x1 = x1 + alpha * acc[ai][bj][m][1];
;                     if (PROBE_ON) { x0 = x0 * pscale; x1 = x1 * pscale; if (p == 0) x0[0] += pspike; }
;                     if (xout32) { *(f32x4*)(xout32 + p) = x0; *(f32x4*)(xout32 + p + 4) = x1; }
;                     else {
;                         v4u w; w.x = cvt_pk_bf16(x0[0], x0[1]); w.y = cvt_pk_bf16(x0[2], x0[3]); w.z = cvt_pk_bf16(x1[0], x1[1]); w.w = cvt_pk_bf16(x1[2], x1[3]);
;                         *(v4u*)(xb + p) = w;
;                         const f32x4 r0 = {x0[0] - bflo(w.x), x0[1] - bfhi(w.x), x0[2] - bflo(w.y), x0[3] - bfhi(w.y)}, r1 = {x1[0] - bflo(w.z), x1[1] - bfhi(w.z), x1[2] - bflo(w.w), x1[3] - bfhi(w.w)};
;                         v4u q; q.x = cvt_pk_bf16(r0[0], r0[1]); q.y = cvt_pk_bf16(r0[2], r0[3]); q.z = cvt_pk_bf16(r1[0], r1[1]); q.w = cvt_pk_bf16(r1[2], r1[3]);
;                         *(v4u*)(xl + p) = q;
;                     }
;                     s += (x0[0] * x0[0] + x0[1] * x0[1]) + (x0[2] * x0[2] + x0[3] * x0[3]) + (x1[0] * x1[0] + x1[1] * x1[1]) + (x1[2] * x1[2] + x1[3] * x1[3]);
;                 }
;                 s += shx(s, 16, ln_); s += shx(s, 32, ln_);
;                 if (fq == 0) ss[(size_t)row * 32 + u.pn * 4 + wc] = s;
	v_add_f32_e32 v247, v152, v153
	v_lshlrev_b32_e32 v152, 16, v232
	v_and_b32_e32 v153, 0xffff0000, v232
	v_lshlrev_b32_e32 v154, 16, v236
	v_and_b32_e32 v155, 0xffff0000, v236
	v_pk_add_f32 v[152:153], v[152:153], v[154:155]
	v_pk_add_f32 v[4:5], v[4:5], v[152:153]
	v_lshlrev_b32_e32 v156, 16, v233
	v_and_b32_e32 v157, 0xffff0000, v233
	v_lshlrev_b32_e32 v158, 16, v237
	v_and_b32_e32 v159, 0xffff0000, v237
	v_pk_add_f32 v[156:157], v[156:157], v[158:159]
	v_pk_add_f32 v[6:7], v[6:7], v[156:157]
	v_lshlrev_b32_e32 v152, 16, v234
	v_and_b32_e32 v153, 0xffff0000, v234
	v_lshlrev_b32_e32 v154, 16, v238
	v_and_b32_e32 v155, 0xffff0000, v238
	v_pk_add_f32 v[152:153], v[152:153], v[154:155]
	v_pk_add_f32 v[0:1], v[0:1], v[152:153]
	v_lshlrev_b32_e32 v156, 16, v235
	v_and_b32_e32 v157, 0xffff0000, v235
	v_lshlrev_b32_e32 v158, 16, v239
	v_and_b32_e32 v159, 0xffff0000, v239
	v_pk_add_f32 v[156:157], v[156:157], v[158:159]
	v_pk_add_f32 v[2:3], v[2:3], v[156:157]
	v_cvt_pk_bf16_f32 v232, v4, v5
	v_cvt_pk_bf16_f32 v233, v6, v7
	v_cvt_pk_bf16_f32 v234, v0, v1
	v_cvt_pk_bf16_f32 v235, v2, v3
	v_lshlrev_b32_e32 v152, 16, v232
	v_and_b32_e32 v153, 0xffff0000, v232
	v_pk_add_f32 v[152:153], v[4:5], v[152:153] neg_lo:[0,1] neg_hi:[0,1]
	v_lshlrev_b32_e32 v154, 16, v233
	v_and_b32_e32 v155, 0xffff0000, v233
	v_pk_add_f32 v[154:155], v[6:7], v[154:155] neg_lo:[0,1] neg_hi:[0,1]
	v_lshlrev_b32_e32 v156, 16, v234
	v_and_b32_e32 v157, 0xffff0000, v234
	v_pk_add_f32 v[156:157], v[0:1], v[156:157] neg_lo:[0,1] neg_hi:[0,1]
	v_lshlrev_b32_e32 v158, 16, v235
	v_and_b32_e32 v159, 0xffff0000, v235
	v_pk_add_f32 v[158:159], v[2:3], v[158:159] neg_lo:[0,1] neg_hi:[0,1]
	v_cvt_pk_bf16_f32 v236, v152, v153
	v_cvt_pk_bf16_f32 v237, v154, v155
	v_cvt_pk_bf16_f32 v238, v156, v157
	v_cvt_pk_bf16_f32 v239, v158, v159
	v_pk_mul_f32 v[152:153], v[4:5], v[4:5]
	v_pk_mul_f32 v[154:155], v[6:7], v[6:7]
	v_pk_mul_f32 v[156:157], v[0:1], v[0:1]
	v_pk_mul_f32 v[158:159], v[2:3], v[2:3]
	v_pk_add_f32 v[152:153], v[152:153], v[154:155]
	v_pk_add_f32 v[156:157], v[156:157], v[158:159]
	v_pk_add_f32 v[152:153], v[152:153], v[156:157]
	v_add_f32_e32 v152, v152, v153
	v_add_f32_e32 v247, v247, v152
	s_add_u32 s22, s6, 0xa0000
	s_addc_u32 s23, s7, 0
	s_add_u32 s98, s8, 0xa0000
	s_addc_u32 s99, s9, 0
	global_store_dwordx4 v248, v[196:199], s[22:23]
	global_store_dwordx4 v248, v[200:203], s[98:99]
	global_store_dwordx4 v248, v[204:207], s[22:23] offset:256
	global_store_dwordx4 v248, v[208:211], s[98:99] offset:256
	s_add_u32 s22, s6, 0xb0000
	s_addc_u32 s23, s7, 0
	s_add_u32 s98, s8, 0xb0000
	s_addc_u32 s99, s9, 0
	global_store_dwordx4 v248, v[224:227], s[22:23]
	global_store_dwordx4 v248, v[228:231], s[98:99]
	global_store_dwordx4 v248, v[232:235], s[22:23] offset:256
	global_store_dwordx4 v248, v[236:239], s[98:99] offset:256
	ds_bpermute_b32 v164, v162, v240
	ds_bpermute_b32 v165, v162, v241
	ds_bpermute_b32 v166, v162, v242
	ds_bpermute_b32 v167, v162, v243
	ds_bpermute_b32 v168, v162, v244
	ds_bpermute_b32 v169, v162, v245
	ds_bpermute_b32 v170, v162, v246
	ds_bpermute_b32 v171, v162, v247
	s_waitcnt lgkmcnt(0)
	v_add_f32_e32 v240, v240, v164
	v_add_f32_e32 v241, v241, v165
	v_add_f32_e32 v242, v242, v166
	v_add_f32_e32 v243, v243, v167
	v_add_f32_e32 v244, v244, v168
	v_add_f32_e32 v245, v245, v169
	v_add_f32_e32 v246, v246, v170
	v_add_f32_e32 v247, v247, v171
	ds_bpermute_b32 v164, v163, v240
	ds_bpermute_b32 v165, v163, v241
	ds_bpermute_b32 v166, v163, v242
	ds_bpermute_b32 v167, v163, v243
	ds_bpermute_b32 v168, v163, v244
	ds_bpermute_b32 v169, v163, v245
	ds_bpermute_b32 v170, v163, v246
	ds_bpermute_b32 v171, v163, v247
	s_waitcnt lgkmcnt(0)
	v_add_f32_e32 v240, v240, v164
	v_add_f32_e32 v241, v241, v165
	v_add_f32_e32 v242, v242, v166
	v_add_f32_e32 v243, v243, v167
	v_add_f32_e32 v244, v244, v168
	v_add_f32_e32 v245, v245, v169
	v_add_f32_e32 v246, v246, v170
	v_add_f32_e32 v247, v247, v171
	v_mbcnt_lo_u32_b32 v152, -1, 0
	v_mbcnt_hi_u32_b32 v152, -1, v152
	v_cmp_gt_u32_e32 vcc, 16, v152
	s_nop 4
	s_and_saveexec_b64 s[24:25], vcc
	global_store_dword v249, v240, s[10:11] offset:0
	global_store_dword v249, v241, s[10:11] offset:2048
	v_add_u32_e32 v166, 0x1000, v249
	global_store_dword v166, v242, s[10:11]
	v_add_u32_e32 v167, 0x1800, v249
	global_store_dword v167, v243, s[10:11]
	v_add_u32_e32 v168, 0x4000, v249
	global_store_dword v168, v244, s[10:11]
	v_add_u32_e32 v169, 0x4800, v249
	global_store_dword v169, v245, s[10:11]
	v_add_u32_e32 v170, 0x5000, v249
	global_store_dword v170, v246, s[10:11]
	v_add_u32_e32 v171, 0x5800, v249
	global_store_dword v171, v247, s[10:11]

;     __device__ __forceinline__ void operator()(AccRef acc, const Unit& u, int wr, int wc, int, int) const {
;         const int ln_ = fresh_lane(), fr = ln_ & 15, fq = ln_ >> 4;
;         const int row0 = u.pm * 256 + wr * 64 + fr, col0 = u.pn * 256 + wc * 32 + 8 * fq;
; #pragma unroll
;         for (int ai = 0; ai < 2; ++ai)
; #pragma unroll
;             for (int m = 0; m < 4; ++m) {
;                 const int row = row0 + ai * 128 + m * 16; float s = 0.f;
; #pragma unroll
;                 for (int bj = 0; bj < 2; ++bj) {
;                     const size_t p = (size_t)row * D + col0 + bj * 128;
;                     f32x4 x0, x1;
;                     if (xin32) { x0 = *(const f32x4*)(xin32 + p); x1 = *(const f32x4*)(xin32 + p + 4); }
;                     else { const v4u h = *(const v4u*)(xb + p), lo = *(const v4u*)(xl + p);
;                         x0 = (f32x4){bflo(h.x) + bflo(lo.x), bfhi(h.x) + bfhi(lo.x), bflo(h.y) + bflo(lo.y), bfhi(h.y) + bfhi(lo.y)};
;                         x1 = (f32x4){bflo(h.z) + bflo(lo.z), bfhi(h.z) + bfhi(lo.z), bflo(h.w) + bflo(lo.w), bfhi(h.w) + bfhi(lo.w)}; }
;                     x0 = x0 + alpha * acc[ai][bj][m][0]; x1 = x1 + alpha * acc[ai][bj][m][1];
;                     if (PROBE_ON) { x0 = x0 * pscale; x1 = x1 * pscale; if (p == 0) x0[0] += pspike; }
;                     if (xout32) { *(f32x4*)(xout32 + p) = x0; *(f32x4*)(xout32 + p + 4) = x1; }
;                     else {
;                         v4u w; w.x = cvt_pk_bf16(x0[0], x0[1]); w.y = cvt_pk_bf16(x0[2], x0[3]); w.z = cvt_pk_bf16(x1[0], x1[1]); w.w = cvt_pk_bf16(x1[2], x1[3]);
;                         *(v4u*)(xb + p) = w;
;                         const f32x4 r0 = {x0[0] - bflo(w.x), x0[1] - bfhi(w.x), x0[2] - bflo(w.y), x0[3] - bfhi(w.y)}, r1 = {x1[0] - bflo(w.z), x1[1] - bfhi(w.z), x1[2] - bflo(w.w), x1[3] - bfhi(w.w)};
;                         v4u q; q.x = cvt_pk_bf16(r0[0], r0[1]); q.y = cvt_pk_bf16(r0[2], r0[3]); q.z = cvt_pk_bf16(r1[0], r1[1]); q.w = cvt_pk_bf16(r1[2], r1[3]);
;                         *(v4u*)(xl + p) = q;
;                     }
;                     s += (x0[0] * x0[0] + x0[1] * x0[1]) + (x0[2] * x0[2] + x0[3] * x0[3]) + (x1[0] * x1[0] + x1[1] * x1[1]) + (x1[2] * x1[2] + x1[3] * x1[3]);
.LBB0_1213:
	s_and_b64 vcc, exec, s[20:21]
	s_cbranch_vccnz .Lmy_re14_orig
	v_mbcnt_lo_u32_b32 v152, -1, 0
	v_mbcnt_hi_u32_b32 v152, -1, v152
	s_lshl_b32 s96, s54, 8
	s_add_i32 s96, s96, s45
	v_and_b32_e32 v153, 15, v152
	v_add_u32_e32 v153, s96, v153
	v_lshrrev_b32_e32 v154, 4, v152
	s_lshl_b32 s96, s33, 8
	s_or_b32 s96, s96, s46
	v_lshl_add_u32 v154, v154, 3, s96
	v_lshlrev_b32_e32 v248, 12, v153
	v_lshl_add_u32 v248, v154, 1, v248
	s_lshl_b32 s96, s33, 4
	s_lshl_b32 s28, s44, 2
	s_add_i32 s96, s96, s28
	v_lshl_add_u32 v249, v153, 7, s96
	v_lshlrev_b32_e32 v162, 2, v152
	v_xor_b32_e32 v163, 0x80, v162
	v_xor_b32_e32 v162, 64, v162
	s_mov_b64 s[28:29], s[12:13]
	s_mov_b64 s[98:99], s[14:15]
	global_load_dwordx4 v[164:167], v248, s[28:29]
	global_load_dwordx4 v[168:171], v248, s[98:99]
	global_load_dwordx4 v[172:175], v248, s[28:29] offset:256
	global_load_dwordx4 v[176:179], v248, s[98:99] offset:256
	s_add_u32 s28, s12, 0x10000
	s_addc_u32 s29, s13, 0
	s_add_u32 s98, s14, 0x10000
	s_addc_u32 s99, s15, 0
	global_load_dwordx4 v[180:183], v248, s[28:29]
	global_load_dwordx4 v[184:187], v248, s[98:99]
	global_load_dwordx4 v[188:191], v248, s[28:29] offset:256
	global_load_dwordx4 v[192:195], v248, s[98:99] offset:256
	s_add_u32 s28, s12, 0x20000
	s_addc_u32 s29, s13, 0
	s_add_u32 s98, s14, 0x20000
	s_addc_u32 s99, s15, 0
	global_load_dwordx4 v[196:199], v248, s[28:29]
	global_load_dwordx4 v[200:203], v248, s[98:99]
	global_load_dwordx4 v[204:207], v248, s[28:29] offset:256
	global_load_dwordx4 v[208:211], v248, s[98:99] offset:256
	s_add_u32 s28, s12, 0x30000
	s_addc_u32 s29, s13, 0
	s_add_u32 s98, s14, 0x30000
	s_addc_u32 s99, s15, 0
	global_load_dwordx4 v[224:227], v248, s[28:29]
	global_load_dwordx4 v[228:231], v248, s[98:99]
	global_load_dwordx4 v[232:235], v248, s[28:29] offset:256
	global_load_dwordx4 v[236:239], v248, s[98:99] offset:256
	s_waitcnt vmcnt(8)
	v_lshlrev_b32_e32 v152, 16, v164
	v_and_b32_e32 v153, 0xffff0000, v164
	v_lshlrev_b32_e32 v154, 16, v168
	v_and_b32_e32 v155, 0xffff0000, v168
	v_pk_add_f32 v[152:153], v[152:153], v[154:155]
	v_pk_fma_f32 v[126:127], v[126:127], 0.5, v[152:153] op_sel_hi:[1,0,1]
	v_lshlrev_b32_e32 v156, 16, v165
	v_and_b32_e32 v157, 0xffff0000, v165
	v_lshlrev_b32_e32 v158, 16, v169
	v_and_b32_e32 v159, 0xffff0000, v169
	v_pk_add_f32 v[156:157], v[156:157], v[158:159]
	v_pk_fma_f32 v[128:129], v[128:129], 0.5, v[156:157] op_sel_hi:[1,0,1]
	v_lshlrev_b32_e32 v152, 16, v166
	v_and_b32_e32 v153, 0xffff0000, v166
	v_lshlrev_b32_e32 v154, 16, v170
	v_and_b32_e32 v155, 0xffff0000, v170
	v_pk_add_f32 v[152:153], v[152:153], v[154:155]
	v_pk_fma_f32 v[122:123], v[122:123], 0.5, v[152:153] op_sel_hi:[1,0,1]
	v_lshlrev_b32_e32 v156, 16, v167
	v_and_b32_e32 v157, 0xffff0000, v167
	v_lshlrev_b32_e32 v158, 16, v171
	v_and_b32_e32 v159, 0xffff0000, v171
	v_pk_add_f32 v[156:157], v[156:157], v[158:159]
	v_pk_fma_f32 v[124:125], v[124:125], 0.5, v[156:157] op_sel_hi:[1,0,1]
	v_cvt_pk_bf16_f32 v164, v126, v127
	v_cvt_pk_bf16_f32 v165, v128, v129
	v_cvt_pk_bf16_f32 v166, v122, v123
	v_cvt_pk_bf16_f32 v167, v124, v125
	v_lshlrev_b32_e32 v152, 16, v164
	v_and_b32_e32 v153, 0xffff0000, v164
	v_pk_add_f32 v[152:153], v[126:127], v[152:153] neg_lo:[0,1] neg_hi:[0,1]
	v_lshlrev_b32_e32 v154, 16, v165
	v_and_b32_e32 v155, 0xffff0000, v165
	v_pk_add_f32 v[154:155], v[128:129], v[154:155] neg_lo:[0,1] neg_hi:[0,1]
	v_lshlrev_b32_e32 v156, 16, v166
	v_and_b32_e32 v157, 0xffff0000, v166
	v_pk_add_f32 v[156:157], v[122:123], v[156:157] neg_lo:[0,1] neg_hi:[0,1]
	v_lshlrev_b32_e32 v158, 16, v167
	v_and_b32_e32 v159, 0xffff0000, v167
	v_pk_add_f32 v[158:159], v[124:125], v[158:159] neg_lo:[0,1] neg_hi:[0,1]
	v_cvt_pk_bf16_f32 v168, v152, v153
	v_cvt_pk_bf16_f32 v169, v154, v155
	v_cvt_pk_bf16_f32 v170, v156, v157
	v_cvt_pk_bf16_f32 v171, v158, v159
	v_pk_mul_f32 v[152:153], v[126:127], v[126:127]
	v_pk_mul_f32 v[154:155], v[128:129], v[128:129]
	v_pk_mul_f32 v[156:157], v[122:123], v[122:123]
	v_pk_mul_f32 v[158:159], v[124:125], v[124:125]
	v_pk_add_f32 v[152:153], v[152:153], v[154:155]
	v_pk_add_f32 v[156:157], v[156:157], v[158:159]
	v_pk_add_f32 v[152:153], v[152:153], v[156:157]
	v_add_f32_e32 v240, v152, v153
	v_lshlrev_b32_e32 v152, 16, v172
	v_and_b32_e32 v153, 0xffff0000, v172
	v_lshlrev_b32_e32 v154, 16, v176
	v_and_b32_e32 v155, 0xffff0000, v176
	v_pk_add_f32 v[152:153], v[152:153], v[154:155]
	v_pk_fma_f32 v[118:119], v[118:119], 0.5, v[152:153] op_sel_hi:[1,0,1]
	v_lshlrev_b32_e32 v156, 16, v173
	v_and_b32_e32 v157, 0xffff0000, v173
	v_lshlrev_b32_e32 v158, 16, v177
	v_and_b32_e32 v159, 0xffff0000, v177
	v_pk_add_f32 v[156:157], v[156:157], v[158:159]
	v_pk_fma_f32 v[120:121], v[120:121], 0.5, v[156:157] op_sel_hi:[1,0,1]
	v_lshlrev_b32_e32 v152, 16, v174
	v_and_b32_e32 v153, 0xffff0000, v174
	v_lshlrev_b32_e32 v154, 16, v178
	v_and_b32_e32 v155, 0xffff0000, v178
	v_pk_add_f32 v[152:153], v[152:153], v[154:155]
	v_pk_fma_f32 v[114:115], v[114:115], 0.5, v[152:153] op_sel_hi:[1,0,1]
	v_lshlrev_b32_e32 v156, 16, v175
	v_and_b32_e32 v157, 0xffff0000, v175
	v_lshlrev_b32_e32 v158, 16, v179
	v_and_b32_e32 v159, 0xffff0000, v179
	v_pk_add_f32 v[156:157], v[156:157], v[158:159]
	v_pk_fma_f32 v[116:117], v[116:117], 0.5, v[156:157] op_sel_hi:[1,0,1]
	v_cvt_pk_bf16_f32 v172, v118, v119
	v_cvt_pk_bf16_f32 v173, v120, v121
	v_cvt_pk_bf16_f32 v174, v114, v115
	v_cvt_pk_bf16_f32 v175, v116, v117
	v_lshlrev_b32_e32 v152, 16, v172
	v_and_b32_e32 v153, 0xffff0000, v172
	v_pk_add_f32 v[152:153], v[118:119], v[152:153] neg_lo:[0,1] neg_hi:[0,1]
	v_lshlrev_b32_e32 v154, 16, v173
	v_and_b32_e32 v155, 0xffff0000, v173
; __device__ __forceinline__ unsigned cvt_pk_bf16(float lo, float hi) { unsigned r; asm volatile("v_cvt_pk_bf16_f32 %0, %1, %2" : "=v"(r) : "v"(lo), "v"(hi)); return r; }
;     __device__ __forceinline__ void operator()(AccRef acc, const Unit& u, int wr, int wc, int, int) const {
;     ...
;                 const int row = row0 + ai * 128 + m * 16; float s = 0.f;
; #pragma unroll
;                 for (int bj = 0; bj < 2; ++bj) {
;                     const size_t p = (size_t)row * D + col0 + bj * 128;
;                     f32x4 x0, x1;
;                     if (xin32) { x0 = *(const f32x4*)(xin32 + p); x1 = *(const f32x4*)(xin32 + p + 4); }
;                     else { const v4u h = *(const v4u*)(xb + p), lo = *(const v4u*)(xl + p);
;                         x0 = (f32x4){bflo(h.x) + bflo(lo.x), bfhi(h.x) + bfhi(lo.x), bflo(h.y) + bflo(lo.y), bfhi(h.y) + bfhi(lo.y)};
;                         x1 = (f32x4){bflo(h.z) + bflo(lo.z), bfhi(h.z) + bfhi(lo.z), bflo(h.w) + bflo(lo.w), bfhi(h.w) + bfhi(lo.w)}; }
;                     x0 = x0 + alpha * acc[ai][bj][m][0]; x1 = x1 + alpha * acc[ai][bj][m][1];
;                     if (PROBE_ON) { x0 = x0 * pscale; x1 = x1 * pscale; if (p == 0) x0[0] += pspike; }
;                     if (xout32) { *(f32x4*)(xout32 + p) = x0; *(f32x4*)(xout32 + p + 4) = x1; }
;                     else {
;                         v4u w; w.x = cvt_pk_bf16(x0[0], x0[1]); w.y = cvt_pk_bf16(x0[2], x0[3]); w.z = cvt_pk_bf16(x1[0], x1[1]); w.w = cvt_pk_bf16(x1[2], x1[3]);
;                         *(v4u*)(xb + p) = w;
;                         const f32x4 r0 = {x0[0] - bflo(w.x), x0[1] - bfhi(w.x), x0[2] - bflo(w.y), x0[3] - bfhi(w.y)}, r1 = {x1[0] - bflo(w.z), x1[1] - bfhi(w.z), x1[2] - bflo(w.w), x1[3] - bfhi(w.w)};
;                         v4u q; q.x = cvt_pk_bf16(r0[0], r0[1]); q.y = cvt_pk_bf16(r0[2], r0[3]); q.z = cvt_pk_bf16(r1[0], r1[1]); q.w = cvt_pk_bf16(r1[2], r1[3]);
;                         *(v4u*)(xl + p) = q;
;                     }
;                     s += (x0[0] * x0[0] + x0[1] * x0[1]) + (x0[2] * x0[2] + x0[3] * x0[3]) + (x1[0] * x1[0] + x1[1] * x1[1]) + (x1[2] * x1[2] + x1[3] * x1[3]);
	v_pk_add_f32 v[154:155], v[120:121], v[154:155] neg_lo:[0,1] neg_hi:[0,1]
	v_lshlrev_b32_e32 v156, 16, v174
	v_and_b32_e32 v157, 0xffff0000, v174
	v_pk_add_f32 v[156:157], v[114:115], v[156:157] neg_lo:[0,1] neg_hi:[0,1]
	v_lshlrev_b32_e32 v158, 16, v175
	v_and_b32_e32 v159, 0xffff0000, v175
	v_pk_add_f32 v[158:159], v[116:117], v[158:159] neg_lo:[0,1] neg_hi:[0,1]
	v_cvt_pk_bf16_f32 v176, v152, v153
	v_cvt_pk_bf16_f32 v177, v154, v155
	v_cvt_pk_bf16_f32 v178, v156, v157
	v_cvt_pk_bf16_f32 v179, v158, v159
	v_pk_mul_f32 v[152:153], v[118:119], v[118:119]
	v_pk_mul_f32 v[154:155], v[120:121], v[120:121]
	v_pk_mul_f32 v[156:157], v[114:115], v[114:115]
	v_pk_mul_f32 v[158:159], v[116:117], v[116:117]
	v_pk_add_f32 v[152:153], v[152:153], v[154:155]
	v_pk_add_f32 v[156:157], v[156:157], v[158:159]
	v_pk_add_f32 v[152:153], v[152:153], v[156:157]
	v_add_f32_e32 v152, v152, v153
	v_add_f32_e32 v240, v240, v152
	v_lshlrev_b32_e32 v152, 16, v180
	v_and_b32_e32 v153, 0xffff0000, v180
	v_lshlrev_b32_e32 v154, 16, v184
	v_and_b32_e32 v155, 0xffff0000, v184
	v_pk_add_f32 v[152:153], v[152:153], v[154:155]
	v_pk_fma_f32 v[110:111], v[110:111], 0.5, v[152:153] op_sel_hi:[1,0,1]
	v_lshlrev_b32_e32 v156, 16, v181
	v_and_b32_e32 v157, 0xffff0000, v181
	v_lshlrev_b32_e32 v158, 16, v185
	v_and_b32_e32 v159, 0xffff0000, v185
	v_pk_add_f32 v[156:157], v[156:157], v[158:159]
	v_pk_fma_f32 v[112:113], v[112:113], 0.5, v[156:157] op_sel_hi:[1,0,1]
	v_lshlrev_b32_e32 v152, 16, v182
	v_and_b32_e32 v153, 0xffff0000, v182
	v_lshlrev_b32_e32 v154, 16, v186
	v_and_b32_e32 v155, 0xffff0000, v186
	v_pk_add_f32 v[152:153], v[152:153], v[154:155]
	v_pk_fma_f32 v[106:107], v[106:107], 0.5, v[152:153] op_sel_hi:[1,0,1]
	v_lshlrev_b32_e32 v156, 16, v183
	v_and_b32_e32 v157, 0xffff0000, v183
	v_lshlrev_b32_e32 v158, 16, v187
	v_and_b32_e32 v159, 0xffff0000, v187
	v_pk_add_f32 v[156:157], v[156:157], v[158:159]
	v_pk_fma_f32 v[108:109], v[108:109], 0.5, v[156:157] op_sel_hi:[1,0,1]
	v_cvt_pk_bf16_f32 v180, v110, v111
	v_cvt_pk_bf16_f32 v181, v112, v113
	v_cvt_pk_bf16_f32 v182, v106, v107
	v_cvt_pk_bf16_f32 v183, v108, v109
	v_lshlrev_b32_e32 v152, 16, v180
	v_and_b32_e32 v153, 0xffff0000, v180
	v_pk_add_f32 v[152:153], v[110:111], v[152:153] neg_lo:[0,1] neg_hi:[0,1]
	v_lshlrev_b32_e32 v154, 16, v181
	v_and_b32_e32 v155, 0xffff0000, v181
	v_pk_add_f32 v[154:155], v[112:113], v[154:155] neg_lo:[0,1] neg_hi:[0,1]
	v_lshlrev_b32_e32 v156, 16, v182
	v_and_b32_e32 v157, 0xffff0000, v182
	v_pk_add_f32 v[156:157], v[106:107], v[156:157] neg_lo:[0,1] neg_hi:[0,1]
	v_lshlrev_b32_e32 v158, 16, v183
	v_and_b32_e32 v159, 0xffff0000, v183
	v_pk_add_f32 v[158:159], v[108:109], v[158:159] neg_lo:[0,1] neg_hi:[0,1]
	v_cvt_pk_bf16_f32 v184, v152, v153
	v_cvt_pk_bf16_f32 v185, v154, v155
	v_cvt_pk_bf16_f32 v186, v156, v157
	v_cvt_pk_bf16_f32 v187, v158, v159
	v_pk_mul_f32 v[152:153], v[110:111], v[110:111]
	v_pk_mul_f32 v[154:155], v[112:113], v[112:113]
	v_pk_mul_f32 v[156:157], v[106:107], v[106:107]
	v_pk_mul_f32 v[158:159], v[108:109], v[108:109]
	v_pk_add_f32 v[152:153], v[152:153], v[154:155]
	v_pk_add_f32 v[156:157], v[156:157], v[158:159]
	v_pk_add_f32 v[152:153], v[152:153], v[156:157]
	v_add_f32_e32 v241, v152, v153
	v_lshlrev_b32_e32 v152, 16, v188
	v_and_b32_e32 v153, 0xffff0000, v188
	v_lshlrev_b32_e32 v154, 16, v192
	v_and_b32_e32 v155, 0xffff0000, v192
	v_pk_add_f32 v[152:153], v[152:153], v[154:155]
	v_pk_fma_f32 v[102:103], v[102:103], 0.5, v[152:153] op_sel_hi:[1,0,1]
	v_lshlrev_b32_e32 v156, 16, v189
	v_and_b32_e32 v157, 0xffff0000, v189
	v_lshlrev_b32_e32 v158, 16, v193
	v_and_b32_e32 v159, 0xffff0000, v193
	v_pk_add_f32 v[156:157], v[156:157], v[158:159]
	v_pk_fma_f32 v[104:105], v[104:105], 0.5, v[156:157] op_sel_hi:[1,0,1]
	v_lshlrev_b32_e32 v152, 16, v190
	v_and_b32_e32 v153, 0xffff0000, v190
	v_lshlrev_b32_e32 v154, 16, v194
	v_and_b32_e32 v155, 0xffff0000, v194
	v_pk_add_f32 v[152:153], v[152:153], v[154:155]
	v_pk_fma_f32 v[98:99], v[98:99], 0.5, v[152:153] op_sel_hi:[1,0,1]
	v_lshlrev_b32_e32 v156, 16, v191
	v_and_b32_e32 v157, 0xffff0000, v191
	v_lshlrev_b32_e32 v158, 16, v195
	v_and_b32_e32 v159, 0xffff0000, v195
	v_pk_add_f32 v[156:157], v[156:157], v[158:159]
	v_pk_fma_f32 v[100:101], v[100:101], 0.5, v[156:157] op_sel_hi:[1,0,1]
	v_cvt_pk_bf16_f32 v188, v102, v103
	v_cvt_pk_bf16_f32 v189, v104, v105
	v_cvt_pk_bf16_f32 v190, v98, v99
	v_cvt_pk_bf16_f32 v191, v100, v101
	v_lshlrev_b32_e32 v152, 16, v188
	v_and_b32_e32 v153, 0xffff0000, v188
	v_pk_add_f32 v[152:153], v[102:103], v[152:153] neg_lo:[0,1] neg_hi:[0,1]
	v_lshlrev_b32_e32 v154, 16, v189
	v_and_b32_e32 v155, 0xffff0000, v189
	v_pk_add_f32 v[154:155], v[104:105], v[154:155] neg_lo:[0,1] neg_hi:[0,1]
	v_lshlrev_b32_e32 v156, 16, v190
	v_and_b32_e32 v157, 0xffff0000, v190
	v_pk_add_f32 v[156:157], v[98:99], v[156:157] neg_lo:[0,1] neg_hi:[0,1]
	v_lshlrev_b32_e32 v158, 16, v191
	v_and_b32_e32 v159, 0xffff0000, v191
	v_pk_add_f32 v[158:159], v[100:101], v[158:159] neg_lo:[0,1] neg_hi:[0,1]
	v_cvt_pk_bf16_f32 v192, v152, v153
	v_cvt_pk_bf16_f32 v193, v154, v155
	v_cvt_pk_bf16_f32 v194, v156, v157
	v_cvt_pk_bf16_f32 v195, v158, v159
	v_pk_mul_f32 v[152:153], v[102:103], v[102:103]
	v_pk_mul_f32 v[154:155], v[104:105], v[104:105]
	v_pk_mul_f32 v[156:157], v[98:99], v[98:99]
	v_pk_mul_f32 v[158:159], v[100:101], v[100:101]
	v_pk_add_f32 v[152:153], v[152:153], v[154:155]
	v_pk_add_f32 v[156:157], v[156:157], v[158:159]
	v_pk_add_f32 v[152:153], v[152:153], v[156:157]
	v_add_f32_e32 v152, v152, v153
	v_add_f32_e32 v241, v241, v152
	s_mov_b64 s[28:29], s[12:13]
	s_mov_b64 s[98:99], s[14:15]
	global_store_dwordx4 v248, v[164:167], s[28:29]
	global_store_dwordx4 v248, v[168:171], s[98:99]
	global_store_dwordx4 v248, v[172:175], s[28:29] offset:256
	global_store_dwordx4 v248, v[176:179], s[98:99] offset:256
	s_add_u32 s28, s12, 0x10000
	s_addc_u32 s29, s13, 0
	s_add_u32 s98, s14, 0x10000
	s_addc_u32 s99, s15, 0
	global_store_dwordx4 v248, v[180:183], s[28:29]
	global_store_dwordx4 v248, v[184:187], s[98:99]
	global_store_dwordx4 v248, v[188:191], s[28:29] offset:256
	global_store_dwordx4 v248, v[192:195], s[98:99] offset:256
	s_add_u32 s28, s12, 0x80000
	s_addc_u32 s29, s13, 0
	s_add_u32 s98, s14, 0x80000
	s_addc_u32 s99, s15, 0
	global_load_dwordx4 v[164:167], v248, s[28:29]
	global_load_dwordx4 v[168:171], v248, s[98:99]
	global_load_dwordx4 v[172:175], v248, s[28:29] offset:256
	global_load_dwordx4 v[176:179], v248, s[98:99] offset:256
	s_add_u32 s28, s12, 0x90000
	s_addc_u32 s29, s13, 0
	s_add_u32 s98, s14, 0x90000
	s_addc_u32 s99, s15, 0
	global_load_dwordx4 v[180:183], v248, s[28:29]
	global_load_dwordx4 v[184:187], v248, s[98:99]
	global_load_dwordx4 v[188:191], v248, s[28:29] offset:256
	global_load_dwordx4 v[192:195], v248, s[98:99] offset:256
	s_waitcnt vmcnt(16)
; __device__ __forceinline__ unsigned cvt_pk_bf16(float lo, float hi) { unsigned r; asm volatile("v_cvt_pk_bf16_f32 %0, %1, %2" : "=v"(r) : "v"(lo), "v"(hi)); return r; }
;     __device__ __forceinline__ void operator()(AccRef acc, const Unit& u, int wr, int wc, int, int) const {
;     ...
;                 const int row = row0 + ai * 128 + m * 16; float s = 0.f;
; #pragma unroll
;                 for (int bj = 0; bj < 2; ++bj) {
;                     const size_t p = (size_t)row * D + col0 + bj * 128;
;                     f32x4 x0, x1;
;                     if (xin32) { x0 = *(const f32x4*)(xin32 + p); x1 = *(const f32x4*)(xin32 + p + 4); }
;                     else { const v4u h = *(const v4u*)(xb + p), lo = *(const v4u*)(xl + p);
;                         x0 = (f32x4){bflo(h.x) + bflo(lo.x), bfhi(h.x) + bfhi(lo.x), bflo(h.y) + bflo(lo.y), bfhi(h.y) + bfhi(lo.y)};
;                         x1 = (f32x4){bflo(h.z) + bflo(lo.z), bfhi(h.z) + bfhi(lo.z), bflo(h.w) + bflo(lo.w), bfhi(h.w) + bfhi(lo.w)}; }
;                     x0 = x0 + alpha * acc[ai][bj][m][0]; x1 = x1 + alpha * acc[ai][bj][m][1];
;                     if (PROBE_ON) { x0 = x0 * pscale; x1 = x1 * pscale; if (p == 0) x0[0] += pspike; }
;                     if (xout32) { *(f32x4*)(xout32 + p) = x0; *(f32x4*)(xout32 + p + 4) = x1; }
;                     else {
;                         v4u w; w.x = cvt_pk_bf16(x0[0], x0[1]); w.y = cvt_pk_bf16(x0[2], x0[3]); w.z = cvt_pk_bf16(x1[0], x1[1]); w.w = cvt_pk_bf16(x1[2], x1[3]);
;                         *(v4u*)(xb + p) = w;
;                         const f32x4 r0 = {x0[0] - bflo(w.x), x0[1] - bfhi(w.x), x0[2] - bflo(w.y), x0[3] - bfhi(w.y)}, r1 = {x1[0] - bflo(w.z), x1[1] - bfhi(w.z), x1[2] - bflo(w.w), x1[3] - bfhi(w.w)};
;                         v4u q; q.x = cvt_pk_bf16(r0[0], r0[1]); q.y = cvt_pk_bf16(r0[2], r0[3]); q.z = cvt_pk_bf16(r1[0], r1[1]); q.w = cvt_pk_bf16(r1[2], r1[3]);
;                         *(v4u*)(xl + p) = q;
;                     }
;                     s += (x0[0] * x0[0] + x0[1] * x0[1]) + (x0[2] * x0[2] + x0[3] * x0[3]) + (x1[0] * x1[0] + x1[1] * x1[1]) + (x1[2] * x1[2] + x1[3] * x1[3]);
	v_lshlrev_b32_e32 v152, 16, v196
	v_and_b32_e32 v153, 0xffff0000, v196
	v_lshlrev_b32_e32 v154, 16, v200
	v_and_b32_e32 v155, 0xffff0000, v200
	v_pk_add_f32 v[152:153], v[152:153], v[154:155]
	v_pk_fma_f32 v[94:95], v[94:95], 0.5, v[152:153] op_sel_hi:[1,0,1]
	v_lshlrev_b32_e32 v156, 16, v197
	v_and_b32_e32 v157, 0xffff0000, v197
	v_lshlrev_b32_e32 v158, 16, v201
	v_and_b32_e32 v159, 0xffff0000, v201
	v_pk_add_f32 v[156:157], v[156:157], v[158:159]
	v_pk_fma_f32 v[96:97], v[96:97], 0.5, v[156:157] op_sel_hi:[1,0,1]
	v_lshlrev_b32_e32 v152, 16, v198
	v_and_b32_e32 v153, 0xffff0000, v198
	v_lshlrev_b32_e32 v154, 16, v202
	v_and_b32_e32 v155, 0xffff0000, v202
	v_pk_add_f32 v[152:153], v[152:153], v[154:155]
	v_pk_fma_f32 v[90:91], v[90:91], 0.5, v[152:153] op_sel_hi:[1,0,1]
	v_lshlrev_b32_e32 v156, 16, v199
	v_and_b32_e32 v157, 0xffff0000, v199
	v_lshlrev_b32_e32 v158, 16, v203
	v_and_b32_e32 v159, 0xffff0000, v203
	v_pk_add_f32 v[156:157], v[156:157], v[158:159]
	v_pk_fma_f32 v[92:93], v[92:93], 0.5, v[156:157] op_sel_hi:[1,0,1]
	v_cvt_pk_bf16_f32 v196, v94, v95
	v_cvt_pk_bf16_f32 v197, v96, v97
	v_cvt_pk_bf16_f32 v198, v90, v91
	v_cvt_pk_bf16_f32 v199, v92, v93
	v_lshlrev_b32_e32 v152, 16, v196
	v_and_b32_e32 v153, 0xffff0000, v196
	v_pk_add_f32 v[152:153], v[94:95], v[152:153] neg_lo:[0,1] neg_hi:[0,1]
	v_lshlrev_b32_e32 v154, 16, v197
	v_and_b32_e32 v155, 0xffff0000, v197
	v_pk_add_f32 v[154:155], v[96:97], v[154:155] neg_lo:[0,1] neg_hi:[0,1]
	v_lshlrev_b32_e32 v156, 16, v198
	v_and_b32_e32 v157, 0xffff0000, v198
	v_pk_add_f32 v[156:157], v[90:91], v[156:157] neg_lo:[0,1] neg_hi:[0,1]
	v_lshlrev_b32_e32 v158, 16, v199
	v_and_b32_e32 v159, 0xffff0000, v199
	v_pk_add_f32 v[158:159], v[92:93], v[158:159] neg_lo:[0,1] neg_hi:[0,1]
	v_cvt_pk_bf16_f32 v200, v152, v153
	v_cvt_pk_bf16_f32 v201, v154, v155
	v_cvt_pk_bf16_f32 v202, v156, v157
	v_cvt_pk_bf16_f32 v203, v158, v159
	v_pk_mul_f32 v[152:153], v[94:95], v[94:95]
	v_pk_mul_f32 v[154:155], v[96:97], v[96:97]
	v_pk_mul_f32 v[156:157], v[90:91], v[90:91]
	v_pk_mul_f32 v[158:159], v[92:93], v[92:93]
	v_pk_add_f32 v[152:153], v[152:153], v[154:155]
	v_pk_add_f32 v[156:157], v[156:157], v[158:159]
	v_pk_add_f32 v[152:153], v[152:153], v[156:157]
	v_add_f32_e32 v242, v152, v153
	v_lshlrev_b32_e32 v152, 16, v204
	v_and_b32_e32 v153, 0xffff0000, v204
	v_lshlrev_b32_e32 v154, 16, v208
	v_and_b32_e32 v155, 0xffff0000, v208
	v_pk_add_f32 v[152:153], v[152:153], v[154:155]
	v_pk_fma_f32 v[86:87], v[86:87], 0.5, v[152:153] op_sel_hi:[1,0,1]
	v_lshlrev_b32_e32 v156, 16, v205
	v_and_b32_e32 v157, 0xffff0000, v205
	v_lshlrev_b32_e32 v158, 16, v209
	v_and_b32_e32 v159, 0xffff0000, v209
	v_pk_add_f32 v[156:157], v[156:157], v[158:159]
	v_pk_fma_f32 v[88:89], v[88:89], 0.5, v[156:157] op_sel_hi:[1,0,1]
	v_lshlrev_b32_e32 v152, 16, v206
	v_and_b32_e32 v153, 0xffff0000, v206
	v_lshlrev_b32_e32 v154, 16, v210
	v_and_b32_e32 v155, 0xffff0000, v210
	v_pk_add_f32 v[152:153], v[152:153], v[154:155]
	v_pk_fma_f32 v[82:83], v[82:83], 0.5, v[152:153] op_sel_hi:[1,0,1]
	v_lshlrev_b32_e32 v156, 16, v207
	v_and_b32_e32 v157, 0xffff0000, v207
	v_lshlrev_b32_e32 v158, 16, v211
	v_and_b32_e32 v159, 0xffff0000, v211
	v_pk_add_f32 v[156:157], v[156:157], v[158:159]
	v_pk_fma_f32 v[84:85], v[84:85], 0.5, v[156:157] op_sel_hi:[1,0,1]
	v_cvt_pk_bf16_f32 v204, v86, v87
	v_cvt_pk_bf16_f32 v205, v88, v89
	v_cvt_pk_bf16_f32 v206, v82, v83
	v_cvt_pk_bf16_f32 v207, v84, v85
	v_lshlrev_b32_e32 v152, 16, v204
	v_and_b32_e32 v153, 0xffff0000, v204
	v_pk_add_f32 v[152:153], v[86:87], v[152:153] neg_lo:[0,1] neg_hi:[0,1]
	v_lshlrev_b32_e32 v154, 16, v205
	v_and_b32_e32 v155, 0xffff0000, v205
	v_pk_add_f32 v[154:155], v[88:89], v[154:155] neg_lo:[0,1] neg_hi:[0,1]
	v_lshlrev_b32_e32 v156, 16, v206
	v_and_b32_e32 v157, 0xffff0000, v206
	v_pk_add_f32 v[156:157], v[82:83], v[156:157] neg_lo:[0,1] neg_hi:[0,1]
	v_lshlrev_b32_e32 v158, 16, v207
	v_and_b32_e32 v159, 0xffff0000, v207
	v_pk_add_f32 v[158:159], v[84:85], v[158:159] neg_lo:[0,1] neg_hi:[0,1]
	v_cvt_pk_bf16_f32 v208, v152, v153
	v_cvt_pk_bf16_f32 v209, v154, v155
	v_cvt_pk_bf16_f32 v210, v156, v157
	v_cvt_pk_bf16_f32 v211, v158, v159
	v_pk_mul_f32 v[152:153], v[86:87], v[86:87]
	v_pk_mul_f32 v[154:155], v[88:89], v[88:89]
	v_pk_mul_f32 v[156:157], v[82:83], v[82:83]
	v_pk_mul_f32 v[158:159], v[84:85], v[84:85]
	v_pk_add_f32 v[152:153], v[152:153], v[154:155]
	v_pk_add_f32 v[156:157], v[156:157], v[158:159]
	v_pk_add_f32 v[152:153], v[152:153], v[156:157]
	v_add_f32_e32 v152, v152, v153
	v_add_f32_e32 v242, v242, v152
	v_lshlrev_b32_e32 v152, 16, v224
	v_and_b32_e32 v153, 0xffff0000, v224
	v_lshlrev_b32_e32 v154, 16, v228
	v_and_b32_e32 v155, 0xffff0000, v228
	v_pk_add_f32 v[152:153], v[152:153], v[154:155]
	v_pk_fma_f32 v[78:79], v[78:79], 0.5, v[152:153] op_sel_hi:[1,0,1]
	v_lshlrev_b32_e32 v156, 16, v225
	v_and_b32_e32 v157, 0xffff0000, v225
	v_lshlrev_b32_e32 v158, 16, v229
	v_and_b32_e32 v159, 0xffff0000, v229
	v_pk_add_f32 v[156:157], v[156:157], v[158:159]
	v_pk_fma_f32 v[80:81], v[80:81], 0.5, v[156:157] op_sel_hi:[1,0,1]
	v_lshlrev_b32_e32 v152, 16, v226
	v_and_b32_e32 v153, 0xffff0000, v226
	v_lshlrev_b32_e32 v154, 16, v230
	v_and_b32_e32 v155, 0xffff0000, v230
	v_pk_add_f32 v[152:153], v[152:153], v[154:155]
	v_pk_fma_f32 v[74:75], v[74:75], 0.5, v[152:153] op_sel_hi:[1,0,1]
	v_lshlrev_b32_e32 v156, 16, v227
	v_and_b32_e32 v157, 0xffff0000, v227
	v_lshlrev_b32_e32 v158, 16, v231
	v_and_b32_e32 v159, 0xffff0000, v231
	v_pk_add_f32 v[156:157], v[156:157], v[158:159]
	v_pk_fma_f32 v[76:77], v[76:77], 0.5, v[156:157] op_sel_hi:[1,0,1]
	v_cvt_pk_bf16_f32 v224, v78, v79
; __device__ __forceinline__ unsigned cvt_pk_bf16(float lo, float hi) { unsigned r; asm volatile("v_cvt_pk_bf16_f32 %0, %1, %2" : "=v"(r) : "v"(lo), "v"(hi)); return r; }
;     __device__ __forceinline__ void operator()(AccRef acc, const Unit& u, int wr, int wc, int, int) const {
;     ...
;                 const int row = row0 + ai * 128 + m * 16; float s = 0.f;
; #pragma unroll
;                 for (int bj = 0; bj < 2; ++bj) {
;                     const size_t p = (size_t)row * D + col0 + bj * 128;
;                     f32x4 x0, x1;
;                     if (xin32) { x0 = *(const f32x4*)(xin32 + p); x1 = *(const f32x4*)(xin32 + p + 4); }
;                     else { const v4u h = *(const v4u*)(xb + p), lo = *(const v4u*)(xl + p);
;                         x0 = (f32x4){bflo(h.x) + bflo(lo.x), bfhi(h.x) + bfhi(lo.x), bflo(h.y) + bflo(lo.y), bfhi(h.y) + bfhi(lo.y)};
;                         x1 = (f32x4){bflo(h.z) + bflo(lo.z), bfhi(h.z) + bfhi(lo.z), bflo(h.w) + bflo(lo.w), bfhi(h.w) + bfhi(lo.w)}; }
;                     x0 = x0 + alpha * acc[ai][bj][m][0]; x1 = x1 + alpha * acc[ai][bj][m][1];
;                     if (PROBE_ON) { x0 = x0 * pscale; x1 = x1 * pscale; if (p == 0) x0[0] += pspike; }
;                     if (xout32) { *(f32x4*)(xout32 + p) = x0; *(f32x4*)(xout32 + p + 4) = x1; }
;                     else {
;                         v4u w; w.x = cvt_pk_bf16(x0[0], x0[1]); w.y = cvt_pk_bf16(x0[2], x0[3]); w.z = cvt_pk_bf16(x1[0], x1[1]); w.w = cvt_pk_bf16(x1[2], x1[3]);
;                         *(v4u*)(xb + p) = w;
;                         const f32x4 r0 = {x0[0] - bflo(w.x), x0[1] - bfhi(w.x), x0[2] - bflo(w.y), x0[3] - bfhi(w.y)}, r1 = {x1[0] - bflo(w.z), x1[1] - bfhi(w.z), x1[2] - bflo(w.w), x1[3] - bfhi(w.w)};
;                         v4u q; q.x = cvt_pk_bf16(r0[0], r0[1]); q.y = cvt_pk_bf16(r0[2], r0[3]); q.z = cvt_pk_bf16(r1[0], r1[1]); q.w = cvt_pk_bf16(r1[2], r1[3]);
;                         *(v4u*)(xl + p) = q;
;                     }
;                     s += (x0[0] * x0[0] + x0[1] * x0[1]) + (x0[2] * x0[2] + x0[3] * x0[3]) + (x1[0] * x1[0] + x1[1] * x1[1]) + (x1[2] * x1[2] + x1[3] * x1[3]);
	v_cvt_pk_bf16_f32 v225, v80, v81
	v_cvt_pk_bf16_f32 v226, v74, v75
	v_cvt_pk_bf16_f32 v227, v76, v77
	v_lshlrev_b32_e32 v152, 16, v224
	v_and_b32_e32 v153, 0xffff0000, v224
	v_pk_add_f32 v[152:153], v[78:79], v[152:153] neg_lo:[0,1] neg_hi:[0,1]
	v_lshlrev_b32_e32 v154, 16, v225
	v_and_b32_e32 v155, 0xffff0000, v225
	v_pk_add_f32 v[154:155], v[80:81], v[154:155] neg_lo:[0,1] neg_hi:[0,1]
	v_lshlrev_b32_e32 v156, 16, v226
	v_and_b32_e32 v157, 0xffff0000, v226
	v_pk_add_f32 v[156:157], v[74:75], v[156:157] neg_lo:[0,1] neg_hi:[0,1]
	v_lshlrev_b32_e32 v158, 16, v227
	v_and_b32_e32 v159, 0xffff0000, v227
	v_pk_add_f32 v[158:159], v[76:77], v[158:159] neg_lo:[0,1] neg_hi:[0,1]
	v_cvt_pk_bf16_f32 v228, v152, v153
	v_cvt_pk_bf16_f32 v229, v154, v155
	v_cvt_pk_bf16_f32 v230, v156, v157
	v_cvt_pk_bf16_f32 v231, v158, v159
	v_pk_mul_f32 v[152:153], v[78:79], v[78:79]
	v_pk_mul_f32 v[154:155], v[80:81], v[80:81]
	v_pk_mul_f32 v[156:157], v[74:75], v[74:75]
	v_pk_mul_f32 v[158:159], v[76:77], v[76:77]
	v_pk_add_f32 v[152:153], v[152:153], v[154:155]
	v_pk_add_f32 v[156:157], v[156:157], v[158:159]
	v_pk_add_f32 v[152:153], v[152:153], v[156:157]
	v_add_f32_e32 v243, v152, v153
	v_lshlrev_b32_e32 v152, 16, v232
	v_and_b32_e32 v153, 0xffff0000, v232
	v_lshlrev_b32_e32 v154, 16, v236
	v_and_b32_e32 v155, 0xffff0000, v236
	v_pk_add_f32 v[152:153], v[152:153], v[154:155]
	v_pk_fma_f32 v[70:71], v[70:71], 0.5, v[152:153] op_sel_hi:[1,0,1]
	v_lshlrev_b32_e32 v156, 16, v233
	v_and_b32_e32 v157, 0xffff0000, v233
	v_lshlrev_b32_e32 v158, 16, v237
	v_and_b32_e32 v159, 0xffff0000, v237
	v_pk_add_f32 v[156:157], v[156:157], v[158:159]
	v_pk_fma_f32 v[72:73], v[72:73], 0.5, v[156:157] op_sel_hi:[1,0,1]
	v_lshlrev_b32_e32 v152, 16, v234
	v_and_b32_e32 v153, 0xffff0000, v234
	v_lshlrev_b32_e32 v154, 16, v238
	v_and_b32_e32 v155, 0xffff0000, v238
	v_pk_add_f32 v[152:153], v[152:153], v[154:155]
	v_pk_fma_f32 v[66:67], v[66:67], 0.5, v[152:153] op_sel_hi:[1,0,1]
	v_lshlrev_b32_e32 v156, 16, v235
	v_and_b32_e32 v157, 0xffff0000, v235
	v_lshlrev_b32_e32 v158, 16, v239
	v_and_b32_e32 v159, 0xffff0000, v239
	v_pk_add_f32 v[156:157], v[156:157], v[158:159]
	v_pk_fma_f32 v[68:69], v[68:69], 0.5, v[156:157] op_sel_hi:[1,0,1]
	v_cvt_pk_bf16_f32 v232, v70, v71
	v_cvt_pk_bf16_f32 v233, v72, v73
	v_cvt_pk_bf16_f32 v234, v66, v67
	v_cvt_pk_bf16_f32 v235, v68, v69
	v_lshlrev_b32_e32 v152, 16, v232
	v_and_b32_e32 v153, 0xffff0000, v232
	v_pk_add_f32 v[152:153], v[70:71], v[152:153] neg_lo:[0,1] neg_hi:[0,1]
	v_lshlrev_b32_e32 v154, 16, v233
	v_and_b32_e32 v155, 0xffff0000, v233
	v_pk_add_f32 v[154:155], v[72:73], v[154:155] neg_lo:[0,1] neg_hi:[0,1]
	v_lshlrev_b32_e32 v156, 16, v234
	v_and_b32_e32 v157, 0xffff0000, v234
	v_pk_add_f32 v[156:157], v[66:67], v[156:157] neg_lo:[0,1] neg_hi:[0,1]
	v_lshlrev_b32_e32 v158, 16, v235
	v_and_b32_e32 v159, 0xffff0000, v235
	v_pk_add_f32 v[158:159], v[68:69], v[158:159] neg_lo:[0,1] neg_hi:[0,1]
	v_cvt_pk_bf16_f32 v236, v152, v153
	v_cvt_pk_bf16_f32 v237, v154, v155
	v_cvt_pk_bf16_f32 v238, v156, v157
	v_cvt_pk_bf16_f32 v239, v158, v159
	v_pk_mul_f32 v[152:153], v[70:71], v[70:71]
	v_pk_mul_f32 v[154:155], v[72:73], v[72:73]
	v_pk_mul_f32 v[156:157], v[66:67], v[66:67]
	v_pk_mul_f32 v[158:159], v[68:69], v[68:69]
	v_pk_add_f32 v[152:153], v[152:153], v[154:155]
	v_pk_add_f32 v[156:157], v[156:157], v[158:159]
	v_pk_add_f32 v[152:153], v[152:153], v[156:157]
	v_add_f32_e32 v152, v152, v153
	v_add_f32_e32 v243, v243, v152
	s_add_u32 s28, s12, 0x20000
	s_addc_u32 s29, s13, 0
	s_add_u32 s98, s14, 0x20000
	s_addc_u32 s99, s15, 0
	global_store_dwordx4 v248, v[196:199], s[28:29]
	global_store_dwordx4 v248, v[200:203], s[98:99]
	global_store_dwordx4 v248, v[204:207], s[28:29] offset:256
	global_store_dwordx4 v248, v[208:211], s[98:99] offset:256
	s_add_u32 s28, s12, 0x30000
	s_addc_u32 s29, s13, 0
	s_add_u32 s98, s14, 0x30000
	s_addc_u32 s99, s15, 0
	global_store_dwordx4 v248, v[224:227], s[28:29]
	global_store_dwordx4 v248, v[228:231], s[98:99]
	global_store_dwordx4 v248, v[232:235], s[28:29] offset:256
	global_store_dwordx4 v248, v[236:239], s[98:99] offset:256
	s_add_u32 s28, s12, 0xa0000
	s_addc_u32 s29, s13, 0
	s_add_u32 s98, s14, 0xa0000
	s_addc_u32 s99, s15, 0
	global_load_dwordx4 v[196:199], v248, s[28:29]
	global_load_dwordx4 v[200:203], v248, s[98:99]
	global_load_dwordx4 v[204:207], v248, s[28:29] offset:256
	global_load_dwordx4 v[208:211], v248, s[98:99] offset:256
	s_add_u32 s28, s12, 0xb0000
	s_addc_u32 s29, s13, 0
	s_add_u32 s98, s14, 0xb0000
	s_addc_u32 s99, s15, 0
	global_load_dwordx4 v[224:227], v248, s[28:29]
	global_load_dwordx4 v[228:231], v248, s[98:99]
	global_load_dwordx4 v[232:235], v248, s[28:29] offset:256
	global_load_dwordx4 v[236:239], v248, s[98:99] offset:256
	s_waitcnt vmcnt(16)
; __device__ __forceinline__ unsigned cvt_pk_bf16(float lo, float hi) { unsigned r; asm volatile("v_cvt_pk_bf16_f32 %0, %1, %2" : "=v"(r) : "v"(lo), "v"(hi)); return r; }
;     __device__ __forceinline__ void operator()(AccRef acc, const Unit& u, int wr, int wc, int, int) const {
;     ...
;                 const int row = row0 + ai * 128 + m * 16; float s = 0.f;
; #pragma unroll
;                 for (int bj = 0; bj < 2; ++bj) {
;                     const size_t p = (size_t)row * D + col0 + bj * 128;
;                     f32x4 x0, x1;
;                     if (xin32) { x0 = *(const f32x4*)(xin32 + p); x1 = *(const f32x4*)(xin32 + p + 4); }
;                     else { const v4u h = *(const v4u*)(xb + p), lo = *(const v4u*)(xl + p);
;                         x0 = (f32x4){bflo(h.x) + bflo(lo.x), bfhi(h.x) + bfhi(lo.x), bflo(h.y) + bflo(lo.y), bfhi(h.y) + bfhi(lo.y)};
;                         x1 = (f32x4){bflo(h.z) + bflo(lo.z), bfhi(h.z) + bfhi(lo.z), bflo(h.w) + bflo(lo.w), bfhi(h.w) + bfhi(lo.w)}; }
;                     x0 = x0 + alpha * acc[ai][bj][m][0]; x1 = x1 + alpha * acc[ai][bj][m][1];
;                     if (PROBE_ON) { x0 = x0 * pscale; x1 = x1 * pscale; if (p == 0) x0[0] += pspike; }
;                     if (xout32) { *(f32x4*)(xout32 + p) = x0; *(f32x4*)(xout32 + p + 4) = x1; }
;                     else {
;                         v4u w; w.x = cvt_pk_bf16(x0[0], x0[1]); w.y = cvt_pk_bf16(x0[2], x0[3]); w.z = cvt_pk_bf16(x1[0], x1[1]); w.w = cvt_pk_bf16(x1[2], x1[3]);
;                         *(v4u*)(xb + p) = w;
;                         const f32x4 r0 = {x0[0] - bflo(w.x), x0[1] - bfhi(w.x), x0[2] - bflo(w.y), x0[3] - bfhi(w.y)}, r1 = {x1[0] - bflo(w.z), x1[1] - bfhi(w.z), x1[2] - bflo(w.w), x1[3] - bfhi(w.w)};
;                         v4u q; q.x = cvt_pk_bf16(r0[0], r0[1]); q.y = cvt_pk_bf16(r0[2], r0[3]); q.z = cvt_pk_bf16(r1[0], r1[1]); q.w = cvt_pk_bf16(r1[2], r1[3]);
;                         *(v4u*)(xl + p) = q;
;                     }
;                     s += (x0[0] * x0[0] + x0[1] * x0[1]) + (x0[2] * x0[2] + x0[3] * x0[3]) + (x1[0] * x1[0] + x1[1] * x1[1]) + (x1[2] * x1[2] + x1[3] * x1[3]);
	v_lshlrev_b32_e32 v152, 16, v164
	v_and_b32_e32 v153, 0xffff0000, v164
	v_lshlrev_b32_e32 v154, 16, v168
	v_and_b32_e32 v155, 0xffff0000, v168
	v_pk_add_f32 v[152:153], v[152:153], v[154:155]
	v_pk_fma_f32 v[62:63], v[62:63], 0.5, v[152:153] op_sel_hi:[1,0,1]
	v_lshlrev_b32_e32 v156, 16, v165
	v_and_b32_e32 v157, 0xffff0000, v165
	v_lshlrev_b32_e32 v158, 16, v169
	v_and_b32_e32 v159, 0xffff0000, v169
	v_pk_add_f32 v[156:157], v[156:157], v[158:159]
	v_pk_fma_f32 v[64:65], v[64:65], 0.5, v[156:157] op_sel_hi:[1,0,1]
	v_lshlrev_b32_e32 v152, 16, v166
	v_and_b32_e32 v153, 0xffff0000, v166
	v_lshlrev_b32_e32 v154, 16, v170
	v_and_b32_e32 v155, 0xffff0000, v170
	v_pk_add_f32 v[152:153], v[152:153], v[154:155]
	v_pk_fma_f32 v[58:59], v[58:59], 0.5, v[152:153] op_sel_hi:[1,0,1]
	v_lshlrev_b32_e32 v156, 16, v167
	v_and_b32_e32 v157, 0xffff0000, v167
	v_lshlrev_b32_e32 v158, 16, v171
	v_and_b32_e32 v159, 0xffff0000, v171
	v_pk_add_f32 v[156:157], v[156:157], v[158:159]
	v_pk_fma_f32 v[60:61], v[60:61], 0.5, v[156:157] op_sel_hi:[1,0,1]
	v_cvt_pk_bf16_f32 v164, v62, v63
	v_cvt_pk_bf16_f32 v165, v64, v65
	v_cvt_pk_bf16_f32 v166, v58, v59
	v_cvt_pk_bf16_f32 v167, v60, v61
	v_lshlrev_b32_e32 v152, 16, v164
	v_and_b32_e32 v153, 0xffff0000, v164
	v_pk_add_f32 v[152:153], v[62:63], v[152:153] neg_lo:[0,1] neg_hi:[0,1]
	v_lshlrev_b32_e32 v154, 16, v165
	v_and_b32_e32 v155, 0xffff0000, v165
	v_pk_add_f32 v[154:155], v[64:65], v[154:155] neg_lo:[0,1] neg_hi:[0,1]
	v_lshlrev_b32_e32 v156, 16, v166
	v_and_b32_e32 v157, 0xffff0000, v166
	v_pk_add_f32 v[156:157], v[58:59], v[156:157] neg_lo:[0,1] neg_hi:[0,1]
	v_lshlrev_b32_e32 v158, 16, v167
	v_and_b32_e32 v159, 0xffff0000, v167
	v_pk_add_f32 v[158:159], v[60:61], v[158:159] neg_lo:[0,1] neg_hi:[0,1]
	v_cvt_pk_bf16_f32 v168, v152, v153
	v_cvt_pk_bf16_f32 v169, v154, v155
	v_cvt_pk_bf16_f32 v170, v156, v157
	v_cvt_pk_bf16_f32 v171, v158, v159
	v_pk_mul_f32 v[152:153], v[62:63], v[62:63]
	v_pk_mul_f32 v[154:155], v[64:65], v[64:65]
	v_pk_mul_f32 v[156:157], v[58:59], v[58:59]
	v_pk_mul_f32 v[158:159], v[60:61], v[60:61]
	v_pk_add_f32 v[152:153], v[152:153], v[154:155]
	v_pk_add_f32 v[156:157], v[156:157], v[158:159]
	v_pk_add_f32 v[152:153], v[152:153], v[156:157]
	v_add_f32_e32 v244, v152, v153
	v_lshlrev_b32_e32 v152, 16, v172
	v_and_b32_e32 v153, 0xffff0000, v172
	v_lshlrev_b32_e32 v154, 16, v176
	v_and_b32_e32 v155, 0xffff0000, v176
	v_pk_add_f32 v[152:153], v[152:153], v[154:155]
	v_pk_fma_f32 v[54:55], v[54:55], 0.5, v[152:153] op_sel_hi:[1,0,1]
	v_lshlrev_b32_e32 v156, 16, v173
	v_and_b32_e32 v157, 0xffff0000, v173
	v_lshlrev_b32_e32 v158, 16, v177
	v_and_b32_e32 v159, 0xffff0000, v177
	v_pk_add_f32 v[156:157], v[156:157], v[158:159]
	v_pk_fma_f32 v[56:57], v[56:57], 0.5, v[156:157] op_sel_hi:[1,0,1]
	v_lshlrev_b32_e32 v152, 16, v174
	v_and_b32_e32 v153, 0xffff0000, v174
	v_lshlrev_b32_e32 v154, 16, v178
	v_and_b32_e32 v155, 0xffff0000, v178
	v_pk_add_f32 v[152:153], v[152:153], v[154:155]
	v_pk_fma_f32 v[50:51], v[50:51], 0.5, v[152:153] op_sel_hi:[1,0,1]
	v_lshlrev_b32_e32 v156, 16, v175
	v_and_b32_e32 v157, 0xffff0000, v175
	v_lshlrev_b32_e32 v158, 16, v179
	v_and_b32_e32 v159, 0xffff0000, v179
	v_pk_add_f32 v[156:157], v[156:157], v[158:159]
	v_pk_fma_f32 v[52:53], v[52:53], 0.5, v[156:157] op_sel_hi:[1,0,1]
	v_cvt_pk_bf16_f32 v172, v54, v55
	v_cvt_pk_bf16_f32 v173, v56, v57
	v_cvt_pk_bf16_f32 v174, v50, v51
	v_cvt_pk_bf16_f32 v175, v52, v53
	v_lshlrev_b32_e32 v152, 16, v172
	v_and_b32_e32 v153, 0xffff0000, v172
	v_pk_add_f32 v[152:153], v[54:55], v[152:153] neg_lo:[0,1] neg_hi:[0,1]
	v_lshlrev_b32_e32 v154, 16, v173
	v_and_b32_e32 v155, 0xffff0000, v173
	v_pk_add_f32 v[154:155], v[56:57], v[154:155] neg_lo:[0,1] neg_hi:[0,1]
	v_lshlrev_b32_e32 v156, 16, v174
	v_and_b32_e32 v157, 0xffff0000, v174
	v_pk_add_f32 v[156:157], v[50:51], v[156:157] neg_lo:[0,1] neg_hi:[0,1]
	v_lshlrev_b32_e32 v158, 16, v175
	v_and_b32_e32 v159, 0xffff0000, v175
	v_pk_add_f32 v[158:159], v[52:53], v[158:159] neg_lo:[0,1] neg_hi:[0,1]
	v_cvt_pk_bf16_f32 v176, v152, v153
	v_cvt_pk_bf16_f32 v177, v154, v155
	v_cvt_pk_bf16_f32 v178, v156, v157
	v_cvt_pk_bf16_f32 v179, v158, v159
	v_pk_mul_f32 v[152:153], v[54:55], v[54:55]
	v_pk_mul_f32 v[154:155], v[56:57], v[56:57]
	v_pk_mul_f32 v[156:157], v[50:51], v[50:51]
	v_pk_mul_f32 v[158:159], v[52:53], v[52:53]
	v_pk_add_f32 v[152:153], v[152:153], v[154:155]
	v_pk_add_f32 v[156:157], v[156:157], v[158:159]
	v_pk_add_f32 v[152:153], v[152:153], v[156:157]
	v_add_f32_e32 v152, v152, v153
	v_add_f32_e32 v244, v244, v152
	v_lshlrev_b32_e32 v152, 16, v180
	v_and_b32_e32 v153, 0xffff0000, v180
	v_lshlrev_b32_e32 v154, 16, v184
	v_and_b32_e32 v155, 0xffff0000, v184
	v_pk_add_f32 v[152:153], v[152:153], v[154:155]
	v_pk_fma_f32 v[46:47], v[46:47], 0.5, v[152:153] op_sel_hi:[1,0,1]
	v_lshlrev_b32_e32 v156, 16, v181
	v_and_b32_e32 v157, 0xffff0000, v181
	v_lshlrev_b32_e32 v158, 16, v185
	v_and_b32_e32 v159, 0xffff0000, v185
	v_pk_add_f32 v[156:157], v[156:157], v[158:159]
	v_pk_fma_f32 v[48:49], v[48:49], 0.5, v[156:157] op_sel_hi:[1,0,1]
	v_lshlrev_b32_e32 v152, 16, v182
	v_and_b32_e32 v153, 0xffff0000, v182
	v_lshlrev_b32_e32 v154, 16, v186
	v_and_b32_e32 v155, 0xffff0000, v186
	v_pk_add_f32 v[152:153], v[152:153], v[154:155]
	v_pk_fma_f32 v[42:43], v[42:43], 0.5, v[152:153] op_sel_hi:[1,0,1]
	v_lshlrev_b32_e32 v156, 16, v183
	v_and_b32_e32 v157, 0xffff0000, v183
	v_lshlrev_b32_e32 v158, 16, v187
	v_and_b32_e32 v159, 0xffff0000, v187
	v_pk_add_f32 v[156:157], v[156:157], v[158:159]
	v_pk_fma_f32 v[44:45], v[44:45], 0.5, v[156:157] op_sel_hi:[1,0,1]
	v_cvt_pk_bf16_f32 v180, v46, v47
; __device__ __forceinline__ unsigned cvt_pk_bf16(float lo, float hi) { unsigned r; asm volatile("v_cvt_pk_bf16_f32 %0, %1, %2" : "=v"(r) : "v"(lo), "v"(hi)); return r; }
;     __device__ __forceinline__ void operator()(AccRef acc, const Unit& u, int wr, int wc, int, int) const {
;     ...
;                 const int row = row0 + ai * 128 + m * 16; float s = 0.f;
; #pragma unroll
;                 for (int bj = 0; bj < 2; ++bj) {
;                     const size_t p = (size_t)row * D + col0 + bj * 128;
;                     f32x4 x0, x1;
;                     if (xin32) { x0 = *(const f32x4*)(xin32 + p); x1 = *(const f32x4*)(xin32 + p + 4); }
;                     else { const v4u h = *(const v4u*)(xb + p), lo = *(const v4u*)(xl + p);
;                         x0 = (f32x4){bflo(h.x) + bflo(lo.x), bfhi(h.x) + bfhi(lo.x), bflo(h.y) + bflo(lo.y), bfhi(h.y) + bfhi(lo.y)};
;                         x1 = (f32x4){bflo(h.z) + bflo(lo.z), bfhi(h.z) + bfhi(lo.z), bflo(h.w) + bflo(lo.w), bfhi(h.w) + bfhi(lo.w)}; }
;                     x0 = x0 + alpha * acc[ai][bj][m][0]; x1 = x1 + alpha * acc[ai][bj][m][1];
;                     if (PROBE_ON) { x0 = x0 * pscale; x1 = x1 * pscale; if (p == 0) x0[0] += pspike; }
;                     if (xout32) { *(f32x4*)(xout32 + p) = x0; *(f32x4*)(xout32 + p + 4) = x1; }
;                     else {
;                         v4u w; w.x = cvt_pk_bf16(x0[0], x0[1]); w.y = cvt_pk_bf16(x0[2], x0[3]); w.z = cvt_pk_bf16(x1[0], x1[1]); w.w = cvt_pk_bf16(x1[2], x1[3]);
;                         *(v4u*)(xb + p) = w;
;                         const f32x4 r0 = {x0[0] - bflo(w.x), x0[1] - bfhi(w.x), x0[2] - bflo(w.y), x0[3] - bfhi(w.y)}, r1 = {x1[0] - bflo(w.z), x1[1] - bfhi(w.z), x1[2] - bflo(w.w), x1[3] - bfhi(w.w)};
;                         v4u q; q.x = cvt_pk_bf16(r0[0], r0[1]); q.y = cvt_pk_bf16(r0[2], r0[3]); q.z = cvt_pk_bf16(r1[0], r1[1]); q.w = cvt_pk_bf16(r1[2], r1[3]);
;                         *(v4u*)(xl + p) = q;
;                     }
;                     s += (x0[0] * x0[0] + x0[1] * x0[1]) + (x0[2] * x0[2] + x0[3] * x0[3]) + (x1[0] * x1[0] + x1[1] * x1[1]) + (x1[2] * x1[2] + x1[3] * x1[3]);
	v_cvt_pk_bf16_f32 v181, v48, v49
	v_cvt_pk_bf16_f32 v182, v42, v43
	v_cvt_pk_bf16_f32 v183, v44, v45
	v_lshlrev_b32_e32 v152, 16, v180
	v_and_b32_e32 v153, 0xffff0000, v180
	v_pk_add_f32 v[152:153], v[46:47], v[152:153] neg_lo:[0,1] neg_hi:[0,1]
	v_lshlrev_b32_e32 v154, 16, v181
	v_and_b32_e32 v155, 0xffff0000, v181
	v_pk_add_f32 v[154:155], v[48:49], v[154:155] neg_lo:[0,1] neg_hi:[0,1]
	v_lshlrev_b32_e32 v156, 16, v182
	v_and_b32_e32 v157, 0xffff0000, v182
	v_pk_add_f32 v[156:157], v[42:43], v[156:157] neg_lo:[0,1] neg_hi:[0,1]
	v_lshlrev_b32_e32 v158, 16, v183
	v_and_b32_e32 v159, 0xffff0000, v183
	v_pk_add_f32 v[158:159], v[44:45], v[158:159] neg_lo:[0,1] neg_hi:[0,1]
	v_cvt_pk_bf16_f32 v184, v152, v153
	v_cvt_pk_bf16_f32 v185, v154, v155
	v_cvt_pk_bf16_f32 v186, v156, v157
	v_cvt_pk_bf16_f32 v187, v158, v159
	v_pk_mul_f32 v[152:153], v[46:47], v[46:47]
	v_pk_mul_f32 v[154:155], v[48:49], v[48:49]
	v_pk_mul_f32 v[156:157], v[42:43], v[42:43]
	v_pk_mul_f32 v[158:159], v[44:45], v[44:45]
	v_pk_add_f32 v[152:153], v[152:153], v[154:155]
	v_pk_add_f32 v[156:157], v[156:157], v[158:159]
	v_pk_add_f32 v[152:153], v[152:153], v[156:157]
	v_add_f32_e32 v245, v152, v153
	v_lshlrev_b32_e32 v152, 16, v188
	v_and_b32_e32 v153, 0xffff0000, v188
	v_lshlrev_b32_e32 v154, 16, v192
	v_and_b32_e32 v155, 0xffff0000, v192
	v_pk_add_f32 v[152:153], v[152:153], v[154:155]
	v_pk_fma_f32 v[38:39], v[38:39], 0.5, v[152:153] op_sel_hi:[1,0,1]
	v_lshlrev_b32_e32 v156, 16, v189
	v_and_b32_e32 v157, 0xffff0000, v189
	v_lshlrev_b32_e32 v158, 16, v193
	v_and_b32_e32 v159, 0xffff0000, v193
	v_pk_add_f32 v[156:157], v[156:157], v[158:159]
	v_pk_fma_f32 v[40:41], v[40:41], 0.5, v[156:157] op_sel_hi:[1,0,1]
	v_lshlrev_b32_e32 v152, 16, v190
	v_and_b32_e32 v153, 0xffff0000, v190
	v_lshlrev_b32_e32 v154, 16, v194
	v_and_b32_e32 v155, 0xffff0000, v194
	v_pk_add_f32 v[152:153], v[152:153], v[154:155]
	v_pk_fma_f32 v[34:35], v[34:35], 0.5, v[152:153] op_sel_hi:[1,0,1]
	v_lshlrev_b32_e32 v156, 16, v191
	v_and_b32_e32 v157, 0xffff0000, v191
	v_lshlrev_b32_e32 v158, 16, v195
	v_and_b32_e32 v159, 0xffff0000, v195
	v_pk_add_f32 v[156:157], v[156:157], v[158:159]
	v_pk_fma_f32 v[36:37], v[36:37], 0.5, v[156:157] op_sel_hi:[1,0,1]
	v_cvt_pk_bf16_f32 v188, v38, v39
	v_cvt_pk_bf16_f32 v189, v40, v41
	v_cvt_pk_bf16_f32 v190, v34, v35
	v_cvt_pk_bf16_f32 v191, v36, v37
	v_lshlrev_b32_e32 v152, 16, v188
	v_and_b32_e32 v153, 0xffff0000, v188
	v_pk_add_f32 v[152:153], v[38:39], v[152:153] neg_lo:[0,1] neg_hi:[0,1]
	v_lshlrev_b32_e32 v154, 16, v189
	v_and_b32_e32 v155, 0xffff0000, v189
	v_pk_add_f32 v[154:155], v[40:41], v[154:155] neg_lo:[0,1] neg_hi:[0,1]
	v_lshlrev_b32_e32 v156, 16, v190
	v_and_b32_e32 v157, 0xffff0000, v190
	v_pk_add_f32 v[156:157], v[34:35], v[156:157] neg_lo:[0,1] neg_hi:[0,1]
	v_lshlrev_b32_e32 v158, 16, v191
	v_and_b32_e32 v159, 0xffff0000, v191
	v_pk_add_f32 v[158:159], v[36:37], v[158:159] neg_lo:[0,1] neg_hi:[0,1]
	v_cvt_pk_bf16_f32 v192, v152, v153
	v_cvt_pk_bf16_f32 v193, v154, v155
	v_cvt_pk_bf16_f32 v194, v156, v157
	v_cvt_pk_bf16_f32 v195, v158, v159
	v_pk_mul_f32 v[152:153], v[38:39], v[38:39]
	v_pk_mul_f32 v[154:155], v[40:41], v[40:41]
	v_pk_mul_f32 v[156:157], v[34:35], v[34:35]
	v_pk_mul_f32 v[158:159], v[36:37], v[36:37]
	v_pk_add_f32 v[152:153], v[152:153], v[154:155]
	v_pk_add_f32 v[156:157], v[156:157], v[158:159]
	v_pk_add_f32 v[152:153], v[152:153], v[156:157]
	v_add_f32_e32 v152, v152, v153
	v_add_f32_e32 v245, v245, v152
	s_add_u32 s28, s12, 0x80000
	s_addc_u32 s29, s13, 0
	s_add_u32 s98, s14, 0x80000
	s_addc_u32 s99, s15, 0
	global_store_dwordx4 v248, v[164:167], s[28:29]
	global_store_dwordx4 v248, v[168:171], s[98:99]
	global_store_dwordx4 v248, v[172:175], s[28:29] offset:256
	global_store_dwordx4 v248, v[176:179], s[98:99] offset:256
	s_add_u32 s28, s12, 0x90000
	s_addc_u32 s29, s13, 0
	s_add_u32 s98, s14, 0x90000
	s_addc_u32 s99, s15, 0
	global_store_dwordx4 v248, v[180:183], s[28:29]
	global_store_dwordx4 v248, v[184:187], s[98:99]
	global_store_dwordx4 v248, v[188:191], s[28:29] offset:256
	global_store_dwordx4 v248, v[192:195], s[98:99] offset:256
	s_waitcnt vmcnt(8)
	v_lshlrev_b32_e32 v152, 16, v196
	v_and_b32_e32 v153, 0xffff0000, v196
	v_lshlrev_b32_e32 v154, 16, v200
	v_and_b32_e32 v155, 0xffff0000, v200
	v_pk_add_f32 v[152:153], v[152:153], v[154:155]
	v_pk_fma_f32 v[30:31], v[30:31], 0.5, v[152:153] op_sel_hi:[1,0,1]
	v_lshlrev_b32_e32 v156, 16, v197
	v_and_b32_e32 v157, 0xffff0000, v197
	v_lshlrev_b32_e32 v158, 16, v201
	v_and_b32_e32 v159, 0xffff0000, v201
	v_pk_add_f32 v[156:157], v[156:157], v[158:159]
	v_pk_fma_f32 v[32:33], v[32:33], 0.5, v[156:157] op_sel_hi:[1,0,1]
	v_lshlrev_b32_e32 v152, 16, v198
	v_and_b32_e32 v153, 0xffff0000, v198
	v_lshlrev_b32_e32 v154, 16, v202
	v_and_b32_e32 v155, 0xffff0000, v202
	v_pk_add_f32 v[152:153], v[152:153], v[154:155]
	v_pk_fma_f32 v[26:27], v[26:27], 0.5, v[152:153] op_sel_hi:[1,0,1]
	v_lshlrev_b32_e32 v156, 16, v199
	v_and_b32_e32 v157, 0xffff0000, v199
	v_lshlrev_b32_e32 v158, 16, v203
	v_and_b32_e32 v159, 0xffff0000, v203
	v_pk_add_f32 v[156:157], v[156:157], v[158:159]
	v_pk_fma_f32 v[28:29], v[28:29], 0.5, v[156:157] op_sel_hi:[1,0,1]
	v_cvt_pk_bf16_f32 v196, v30, v31
	v_cvt_pk_bf16_f32 v197, v32, v33
	v_cvt_pk_bf16_f32 v198, v26, v27
	v_cvt_pk_bf16_f32 v199, v28, v29
	v_lshlrev_b32_e32 v152, 16, v196
	v_and_b32_e32 v153, 0xffff0000, v196
	v_pk_add_f32 v[152:153], v[30:31], v[152:153] neg_lo:[0,1] neg_hi:[0,1]
	v_lshlrev_b32_e32 v154, 16, v197
	v_and_b32_e32 v155, 0xffff0000, v197
	v_pk_add_f32 v[154:155], v[32:33], v[154:155] neg_lo:[0,1] neg_hi:[0,1]
	v_lshlrev_b32_e32 v156, 16, v198
; __device__ __forceinline__ unsigned cvt_pk_bf16(float lo, float hi) { unsigned r; asm volatile("v_cvt_pk_bf16_f32 %0, %1, %2" : "=v"(r) : "v"(lo), "v"(hi)); return r; }
;     __device__ __forceinline__ void operator()(AccRef acc, const Unit& u, int wr, int wc, int, int) const {
;     ...
;                 const int row = row0 + ai * 128 + m * 16; float s = 0.f;
; #pragma unroll
;                 for (int bj = 0; bj < 2; ++bj) {
;                     const size_t p = (size_t)row * D + col0 + bj * 128;
;                     f32x4 x0, x1;
;                     if (xin32) { x0 = *(const f32x4*)(xin32 + p); x1 = *(const f32x4*)(xin32 + p + 4); }
;                     else { const v4u h = *(const v4u*)(xb + p), lo = *(const v4u*)(xl + p);
;                         x0 = (f32x4){bflo(h.x) + bflo(lo.x), bfhi(h.x) + bfhi(lo.x), bflo(h.y) + bflo(lo.y), bfhi(h.y) + bfhi(lo.y)};
;                         x1 = (f32x4){bflo(h.z) + bflo(lo.z), bfhi(h.z) + bfhi(lo.z), bflo(h.w) + bflo(lo.w), bfhi(h.w) + bfhi(lo.w)}; }
;                     x0 = x0 + alpha * acc[ai][bj][m][0]; x1 = x1 + alpha * acc[ai][bj][m][1];
;                     if (PROBE_ON) { x0 = x0 * pscale; x1 = x1 * pscale; if (p == 0) x0[0] += pspike; }
;                     if (xout32) { *(f32x4*)(xout32 + p) = x0; *(f32x4*)(xout32 + p + 4) = x1; }
;                     else {
;                         v4u w; w.x = cvt_pk_bf16(x0[0], x0[1]); w.y = cvt_pk_bf16(x0[2], x0[3]); w.z = cvt_pk_bf16(x1[0], x1[1]); w.w = cvt_pk_bf16(x1[2], x1[3]);
;                         *(v4u*)(xb + p) = w;
;                         const f32x4 r0 = {x0[0] - bflo(w.x), x0[1] - bfhi(w.x), x0[2] - bflo(w.y), x0[3] - bfhi(w.y)}, r1 = {x1[0] - bflo(w.z), x1[1] - bfhi(w.z), x1[2] - bflo(w.w), x1[3] - bfhi(w.w)};
;                         v4u q; q.x = cvt_pk_bf16(r0[0], r0[1]); q.y = cvt_pk_bf16(r0[2], r0[3]); q.z = cvt_pk_bf16(r1[0], r1[1]); q.w = cvt_pk_bf16(r1[2], r1[3]);
;                         *(v4u*)(xl + p) = q;
;                     }
;                     s += (x0[0] * x0[0] + x0[1] * x0[1]) + (x0[2] * x0[2] + x0[3] * x0[3]) + (x1[0] * x1[0] + x1[1] * x1[1]) + (x1[2] * x1[2] + x1[3] * x1[3]);
	v_and_b32_e32 v157, 0xffff0000, v198
	v_pk_add_f32 v[156:157], v[26:27], v[156:157] neg_lo:[0,1] neg_hi:[0,1]
	v_lshlrev_b32_e32 v158, 16, v199
	v_and_b32_e32 v159, 0xffff0000, v199
	v_pk_add_f32 v[158:159], v[28:29], v[158:159] neg_lo:[0,1] neg_hi:[0,1]
	v_cvt_pk_bf16_f32 v200, v152, v153
	v_cvt_pk_bf16_f32 v201, v154, v155
	v_cvt_pk_bf16_f32 v202, v156, v157
	v_cvt_pk_bf16_f32 v203, v158, v159
	v_pk_mul_f32 v[152:153], v[30:31], v[30:31]
	v_pk_mul_f32 v[154:155], v[32:33], v[32:33]
	v_pk_mul_f32 v[156:157], v[26:27], v[26:27]
	v_pk_mul_f32 v[158:159], v[28:29], v[28:29]
	v_pk_add_f32 v[152:153], v[152:153], v[154:155]
	v_pk_add_f32 v[156:157], v[156:157], v[158:159]
	v_pk_add_f32 v[152:153], v[152:153], v[156:157]
	v_add_f32_e32 v246, v152, v153
	v_lshlrev_b32_e32 v152, 16, v204
	v_and_b32_e32 v153, 0xffff0000, v204
	v_lshlrev_b32_e32 v154, 16, v208
	v_and_b32_e32 v155, 0xffff0000, v208
	v_pk_add_f32 v[152:153], v[152:153], v[154:155]
	v_pk_fma_f32 v[22:23], v[22:23], 0.5, v[152:153] op_sel_hi:[1,0,1]
	v_lshlrev_b32_e32 v156, 16, v205
	v_and_b32_e32 v157, 0xffff0000, v205
	v_lshlrev_b32_e32 v158, 16, v209
	v_and_b32_e32 v159, 0xffff0000, v209
	v_pk_add_f32 v[156:157], v[156:157], v[158:159]
	v_pk_fma_f32 v[24:25], v[24:25], 0.5, v[156:157] op_sel_hi:[1,0,1]
	v_lshlrev_b32_e32 v152, 16, v206
	v_and_b32_e32 v153, 0xffff0000, v206
	v_lshlrev_b32_e32 v154, 16, v210
	v_and_b32_e32 v155, 0xffff0000, v210
	v_pk_add_f32 v[152:153], v[152:153], v[154:155]
	v_pk_fma_f32 v[18:19], v[18:19], 0.5, v[152:153] op_sel_hi:[1,0,1]
	v_lshlrev_b32_e32 v156, 16, v207
	v_and_b32_e32 v157, 0xffff0000, v207
	v_lshlrev_b32_e32 v158, 16, v211
	v_and_b32_e32 v159, 0xffff0000, v211
	v_pk_add_f32 v[156:157], v[156:157], v[158:159]
	v_pk_fma_f32 v[20:21], v[20:21], 0.5, v[156:157] op_sel_hi:[1,0,1]
	v_cvt_pk_bf16_f32 v204, v22, v23
	v_cvt_pk_bf16_f32 v205, v24, v25
	v_cvt_pk_bf16_f32 v206, v18, v19
	v_cvt_pk_bf16_f32 v207, v20, v21
	v_lshlrev_b32_e32 v152, 16, v204
	v_and_b32_e32 v153, 0xffff0000, v204
	v_pk_add_f32 v[152:153], v[22:23], v[152:153] neg_lo:[0,1] neg_hi:[0,1]
	v_lshlrev_b32_e32 v154, 16, v205
	v_and_b32_e32 v155, 0xffff0000, v205
	v_pk_add_f32 v[154:155], v[24:25], v[154:155] neg_lo:[0,1] neg_hi:[0,1]
	v_lshlrev_b32_e32 v156, 16, v206
	v_and_b32_e32 v157, 0xffff0000, v206
	v_pk_add_f32 v[156:157], v[18:19], v[156:157] neg_lo:[0,1] neg_hi:[0,1]
	v_lshlrev_b32_e32 v158, 16, v207
	v_and_b32_e32 v159, 0xffff0000, v207
	v_pk_add_f32 v[158:159], v[20:21], v[158:159] neg_lo:[0,1] neg_hi:[0,1]
	v_cvt_pk_bf16_f32 v208, v152, v153
	v_cvt_pk_bf16_f32 v209, v154, v155
	v_cvt_pk_bf16_f32 v210, v156, v157
	v_cvt_pk_bf16_f32 v211, v158, v159
	v_pk_mul_f32 v[152:153], v[22:23], v[22:23]
	v_pk_mul_f32 v[154:155], v[24:25], v[24:25]
	v_pk_mul_f32 v[156:157], v[18:19], v[18:19]
	v_pk_mul_f32 v[158:159], v[20:21], v[20:21]
	v_pk_add_f32 v[152:153], v[152:153], v[154:155]
	v_pk_add_f32 v[156:157], v[156:157], v[158:159]
	v_pk_add_f32 v[152:153], v[152:153], v[156:157]
	v_add_f32_e32 v152, v152, v153
	v_add_f32_e32 v246, v246, v152
	v_lshlrev_b32_e32 v152, 16, v224
	v_and_b32_e32 v153, 0xffff0000, v224
	v_lshlrev_b32_e32 v154, 16, v228
	v_and_b32_e32 v155, 0xffff0000, v228
	v_pk_add_f32 v[152:153], v[152:153], v[154:155]
	v_pk_fma_f32 v[14:15], v[14:15], 0.5, v[152:153] op_sel_hi:[1,0,1]
	v_lshlrev_b32_e32 v156, 16, v225
	v_and_b32_e32 v157, 0xffff0000, v225
	v_lshlrev_b32_e32 v158, 16, v229
	v_and_b32_e32 v159, 0xffff0000, v229
	v_pk_add_f32 v[156:157], v[156:157], v[158:159]
	v_pk_fma_f32 v[16:17], v[16:17], 0.5, v[156:157] op_sel_hi:[1,0,1]
	v_lshlrev_b32_e32 v152, 16, v226
	v_and_b32_e32 v153, 0xffff0000, v226
	v_lshlrev_b32_e32 v154, 16, v230
	v_and_b32_e32 v155, 0xffff0000, v230
	v_pk_add_f32 v[152:153], v[152:153], v[154:155]
	v_pk_fma_f32 v[10:11], v[10:11], 0.5, v[152:153] op_sel_hi:[1,0,1]
	v_lshlrev_b32_e32 v156, 16, v227
	v_and_b32_e32 v157, 0xffff0000, v227
	v_lshlrev_b32_e32 v158, 16, v231
	v_and_b32_e32 v159, 0xffff0000, v231
	v_pk_add_f32 v[156:157], v[156:157], v[158:159]
	v_pk_fma_f32 v[12:13], v[12:13], 0.5, v[156:157] op_sel_hi:[1,0,1]
	v_cvt_pk_bf16_f32 v224, v14, v15
	v_cvt_pk_bf16_f32 v225, v16, v17
	v_cvt_pk_bf16_f32 v226, v10, v11
	v_cvt_pk_bf16_f32 v227, v12, v13
	v_lshlrev_b32_e32 v152, 16, v224
	v_and_b32_e32 v153, 0xffff0000, v224
	v_pk_add_f32 v[152:153], v[14:15], v[152:153] neg_lo:[0,1] neg_hi:[0,1]
	v_lshlrev_b32_e32 v154, 16, v225
	v_and_b32_e32 v155, 0xffff0000, v225
	v_pk_add_f32 v[154:155], v[16:17], v[154:155] neg_lo:[0,1] neg_hi:[0,1]
	v_lshlrev_b32_e32 v156, 16, v226
	v_and_b32_e32 v157, 0xffff0000, v226
	v_pk_add_f32 v[156:157], v[10:11], v[156:157] neg_lo:[0,1] neg_hi:[0,1]
	v_lshlrev_b32_e32 v158, 16, v227
	v_and_b32_e32 v159, 0xffff0000, v227
	v_pk_add_f32 v[158:159], v[12:13], v[158:159] neg_lo:[0,1] neg_hi:[0,1]
	v_cvt_pk_bf16_f32 v228, v152, v153
	v_cvt_pk_bf16_f32 v229, v154, v155
	v_cvt_pk_bf16_f32 v230, v156, v157
	v_cvt_pk_bf16_f32 v231, v158, v159
	v_pk_mul_f32 v[152:153], v[14:15], v[14:15]
; __device__ __forceinline__ unsigned cvt_pk_bf16(float lo, float hi) { unsigned r; asm volatile("v_cvt_pk_bf16_f32 %0, %1, %2" : "=v"(r) : "v"(lo), "v"(hi)); return r; }
; __device__ __forceinline__ float shx(float v, int o, int lane) { return __builtin_bit_cast(float, __builtin_amdgcn_ds_bpermute((lane ^ o) << 2, __builtin_bit_cast(int, v))); }
;     __device__ __forceinline__ void operator()(AccRef acc, const Unit& u, int wr, int wc, int, int) const {
;     ...
;                         v4u w; w.x = cvt_pk_bf16(x0[0], x0[1]); w.y = cvt_pk_bf16(x0[2], x0[3]); w.z = cvt_pk_bf16(x1[0], x1[1]); w.w = cvt_pk_bf16(x1[2], x1[3]);
;                         *(v4u*)(xb + p) = w;
;                         const f32x4 r0 = {x0[0] - bflo(w.x), x0[1] - bfhi(w.x), x0[2] - bflo(w.y), x0[3] - bfhi(w.y)}, r1 = {x1[0] - bflo(w.z), x1[1] - bfhi(w.z), x1[2] - bflo(w.w), x1[3] - bfhi(w.w)};
;                         v4u q; q.x = cvt_pk_bf16(r0[0], r0[1]); q.y = cvt_pk_bf16(r0[2], r0[3]); q.z = cvt_pk_bf16(r1[0], r1[1]); q.w = cvt_pk_bf16(r1[2], r1[3]);
;                         *(v4u*)(xl + p) = q;
;                     }
;                     s += (x0[0] * x0[0] + x0[1] * x0[1]) + (x0[2] * x0[2] + x0[3] * x0[3]) + (x1[0] * x1[0] + x1[1] * x1[1]) + (x1[2] * x1[2] + x1[3] * x1[3]);
;                 }
;                 s += shx(s, 16, ln_); s += shx(s, 32, ln_);
;                 if (fq == 0) ss[(size_t)row * 32 + u.pn * 4 + wc] = s;
	v_pk_mul_f32 v[154:155], v[16:17], v[16:17]
	v_pk_mul_f32 v[156:157], v[10:11], v[10:11]
	v_pk_mul_f32 v[158:159], v[12:13], v[12:13]
	v_pk_add_f32 v[152:153], v[152:153], v[154:155]
	v_pk_add_f32 v[156:157], v[156:157], v[158:159]
	v_pk_add_f32 v[152:153], v[152:153], v[156:157]
	v_add_f32_e32 v247, v152, v153
	v_lshlrev_b32_e32 v152, 16, v232
	v_and_b32_e32 v153, 0xffff0000, v232
	v_lshlrev_b32_e32 v154, 16, v236
	v_and_b32_e32 v155, 0xffff0000, v236
	v_pk_add_f32 v[152:153], v[152:153], v[154:155]
	v_pk_fma_f32 v[4:5], v[4:5], 0.5, v[152:153] op_sel_hi:[1,0,1]
	v_lshlrev_b32_e32 v156, 16, v233
	v_and_b32_e32 v157, 0xffff0000, v233
	v_lshlrev_b32_e32 v158, 16, v237
	v_and_b32_e32 v159, 0xffff0000, v237
	v_pk_add_f32 v[156:157], v[156:157], v[158:159]
	v_pk_fma_f32 v[6:7], v[6:7], 0.5, v[156:157] op_sel_hi:[1,0,1]
	v_lshlrev_b32_e32 v152, 16, v234
	v_and_b32_e32 v153, 0xffff0000, v234
	v_lshlrev_b32_e32 v154, 16, v238
	v_and_b32_e32 v155, 0xffff0000, v238
	v_pk_add_f32 v[152:153], v[152:153], v[154:155]
	v_pk_fma_f32 v[0:1], v[0:1], 0.5, v[152:153] op_sel_hi:[1,0,1]
	v_lshlrev_b32_e32 v156, 16, v235
	v_and_b32_e32 v157, 0xffff0000, v235
	v_lshlrev_b32_e32 v158, 16, v239
	v_and_b32_e32 v159, 0xffff0000, v239
	v_pk_add_f32 v[156:157], v[156:157], v[158:159]
	v_pk_fma_f32 v[2:3], v[2:3], 0.5, v[156:157] op_sel_hi:[1,0,1]
	v_cvt_pk_bf16_f32 v232, v4, v5
	v_cvt_pk_bf16_f32 v233, v6, v7
	v_cvt_pk_bf16_f32 v234, v0, v1
	v_cvt_pk_bf16_f32 v235, v2, v3
	v_lshlrev_b32_e32 v152, 16, v232
	v_and_b32_e32 v153, 0xffff0000, v232
	v_pk_add_f32 v[152:153], v[4:5], v[152:153] neg_lo:[0,1] neg_hi:[0,1]
	v_lshlrev_b32_e32 v154, 16, v233
	v_and_b32_e32 v155, 0xffff0000, v233
	v_pk_add_f32 v[154:155], v[6:7], v[154:155] neg_lo:[0,1] neg_hi:[0,1]
	v_lshlrev_b32_e32 v156, 16, v234
	v_and_b32_e32 v157, 0xffff0000, v234
	v_pk_add_f32 v[156:157], v[0:1], v[156:157] neg_lo:[0,1] neg_hi:[0,1]
	v_lshlrev_b32_e32 v158, 16, v235
	v_and_b32_e32 v159, 0xffff0000, v235
	v_pk_add_f32 v[158:159], v[2:3], v[158:159] neg_lo:[0,1] neg_hi:[0,1]
	v_cvt_pk_bf16_f32 v236, v152, v153
	v_cvt_pk_bf16_f32 v237, v154, v155
	v_cvt_pk_bf16_f32 v238, v156, v157
	v_cvt_pk_bf16_f32 v239, v158, v159
	v_pk_mul_f32 v[152:153], v[4:5], v[4:5]
	v_pk_mul_f32 v[154:155], v[6:7], v[6:7]
	v_pk_mul_f32 v[156:157], v[0:1], v[0:1]
	v_pk_mul_f32 v[158:159], v[2:3], v[2:3]
	v_pk_add_f32 v[152:153], v[152:153], v[154:155]
	v_pk_add_f32 v[156:157], v[156:157], v[158:159]
	v_pk_add_f32 v[152:153], v[152:153], v[156:157]
	v_add_f32_e32 v152, v152, v153
	v_add_f32_e32 v247, v247, v152
	s_add_u32 s28, s12, 0xa0000
	s_addc_u32 s29, s13, 0
	s_add_u32 s98, s14, 0xa0000
	s_addc_u32 s99, s15, 0
	global_store_dwordx4 v248, v[196:199], s[28:29]
	global_store_dwordx4 v248, v[200:203], s[98:99]
	global_store_dwordx4 v248, v[204:207], s[28:29] offset:256
	global_store_dwordx4 v248, v[208:211], s[98:99] offset:256
	s_add_u32 s28, s12, 0xb0000
	s_addc_u32 s29, s13, 0
	s_add_u32 s98, s14, 0xb0000
	s_addc_u32 s99, s15, 0
	global_store_dwordx4 v248, v[224:227], s[28:29]
	global_store_dwordx4 v248, v[228:231], s[98:99]
	global_store_dwordx4 v248, v[232:235], s[28:29] offset:256
	global_store_dwordx4 v248, v[236:239], s[98:99] offset:256
	ds_bpermute_b32 v164, v162, v240
	ds_bpermute_b32 v165, v162, v241
	ds_bpermute_b32 v166, v162, v242
	ds_bpermute_b32 v167, v162, v243
	ds_bpermute_b32 v168, v162, v244
	ds_bpermute_b32 v169, v162, v245
	ds_bpermute_b32 v170, v162, v246
	ds_bpermute_b32 v171, v162, v247
	s_waitcnt lgkmcnt(0)
	v_add_f32_e32 v240, v240, v164
	v_add_f32_e32 v241, v241, v165
	v_add_f32_e32 v242, v242, v166
	v_add_f32_e32 v243, v243, v167
	v_add_f32_e32 v244, v244, v168
	v_add_f32_e32 v245, v245, v169
	v_add_f32_e32 v246, v246, v170
	v_add_f32_e32 v247, v247, v171
	ds_bpermute_b32 v164, v163, v240
	ds_bpermute_b32 v165, v163, v241
	ds_bpermute_b32 v166, v163, v242
	ds_bpermute_b32 v167, v163, v243
	ds_bpermute_b32 v168, v163, v244
	ds_bpermute_b32 v169, v163, v245
	ds_bpermute_b32 v170, v163, v246
	ds_bpermute_b32 v171, v163, v247
	s_waitcnt lgkmcnt(0)
	v_add_f32_e32 v240, v240, v164
	v_add_f32_e32 v241, v241, v165
	v_add_f32_e32 v242, v242, v166
	v_add_f32_e32 v243, v243, v167
	v_add_f32_e32 v244, v244, v168
	v_add_f32_e32 v245, v245, v169
	v_add_f32_e32 v246, v246, v170
	v_add_f32_e32 v247, v247, v171
	v_mbcnt_lo_u32_b32 v152, -1, 0
	v_mbcnt_hi_u32_b32 v152, -1, v152
	v_cmp_gt_u32_e32 vcc, 16, v152
	s_nop 4
	s_and_saveexec_b64 s[6:7], vcc
	global_store_dword v249, v240, s[16:17] offset:0
	global_store_dword v249, v241, s[16:17] offset:2048
	v_add_u32_e32 v166, 0x1000, v249
	global_store_dword v166, v242, s[16:17]
	v_add_u32_e32 v167, 0x1800, v249
	global_store_dword v167, v243, s[16:17]
	v_add_u32_e32 v168, 0x4000, v249
	global_store_dword v168, v244, s[16:17]
	v_add_u32_e32 v169, 0x4800, v249
	global_store_dword v169, v245, s[16:17]
	v_add_u32_e32 v170, 0x5000, v249
	global_store_dword v170, v246, s[16:17]
	v_add_u32_e32 v171, 0x5800, v249
	global_store_dword v171, v247, s[16:17]
	s_branch .LBB0_1277
